# GEMM K-loops: last LDS-DMA of each load segment deferred into the following compute segment (after 2 MFMAs), counted wait vmcnt(8)->vmcnt(7)
# baseline (speedup 1.0000x reference)
.LBB0_378:
	s_add_u32 s28, s36, 0xfff80080
	s_addc_u32 s29, s37, -1
	s_add_i32 s42, 0, 0x10000
	s_cmp_eq_u32 vcc_hi, 28
	s_cselect_b32 s53, s11, s29
	s_cselect_b32 s52, s21, s28
	s_cselect_b32 s51, s41, s79
	s_cselect_b32 s50, vcc_lo, s78
	s_add_i32 s43, 0, 0x14000
	v_add_u32_e32 v140, s42, v169
	v_add_u32_e32 v173, s43, v169
	ds_read_b128 v[128:131], v140
	ds_read_b128 v[132:135], v140 offset:1024
	ds_read_b128 v[136:139], v140 offset:2048
	ds_read_b128 v[140:143], v140 offset:3072
	ds_read_b128 v[156:159], v173
	ds_read_b128 v[160:163], v173 offset:1024
	ds_read_b128 v[164:167], v173 offset:2048
	ds_read_b128 v[174:177], v173 offset:3072
	v_lshl_add_u64 v[182:183], s[36:37], 0, v[152:153]
	s_add_i32 m0, s88, 0xc000
	ds_read_b128 v[178:181], v172
	ds_read_b128 v[194:197], v172 offset:1024
	ds_read_b128 v[198:201], v172 offset:2048
	ds_read_b128 v[202:205], v172 offset:3072
	ds_read_b128 v[206:209], v172 offset:4096
	ds_read_b128 v[224:227], v172 offset:5120
	ds_read_b128 v[228:231], v172 offset:6144
	ds_read_b128 v[232:235], v172 offset:7168
	global_load_lds_dwordx4 v[182:183], off
	v_lshl_add_u64 v[182:183], s[36:37], 0, v[154:155]
	s_waitcnt vmcnt(7)
	s_waitcnt lgkmcnt(0)
	s_barrier
	s_setprio 1
	s_waitcnt lgkmcnt(0)
	v_mfma_f32_16x16x32_bf16 v[124:127], v[128:131], v[178:181], v[124:127]
	v_mfma_f32_16x16x32_bf16 v[120:123], v[136:139], v[178:181], v[120:123]
	s_add_i32 m0, s88, 0xe000
	s_nop 0
	global_load_lds_dwordx4 v[182:183], off
	v_mfma_f32_16x16x32_bf16 v[116:119], v[128:131], v[198:201], v[116:119]
	v_mfma_f32_16x16x32_bf16 v[108:111], v[136:139], v[198:201], v[108:111]
	v_mfma_f32_16x16x32_bf16 v[100:103], v[128:131], v[206:209], v[100:103]
	v_mfma_f32_16x16x32_bf16 v[92:95], v[136:139], v[206:209], v[92:95]
	v_mfma_f32_16x16x32_bf16 v[84:87], v[128:131], v[228:231], v[84:87]
	v_mfma_f32_16x16x32_bf16 v[76:79], v[136:139], v[228:231], v[76:79]
	v_mfma_f32_16x16x32_bf16 v[124:127], v[132:135], v[194:197], v[124:127]
	v_mfma_f32_16x16x32_bf16 v[120:123], v[140:143], v[194:197], v[120:123]
	v_mfma_f32_16x16x32_bf16 v[116:119], v[132:135], v[202:205], v[116:119]
	v_mfma_f32_16x16x32_bf16 v[108:111], v[140:143], v[202:205], v[108:111]
	v_mfma_f32_16x16x32_bf16 v[100:103], v[132:135], v[224:227], v[100:103]
	v_mfma_f32_16x16x32_bf16 v[92:95], v[140:143], v[224:227], v[92:95]
	v_mfma_f32_16x16x32_bf16 v[84:87], v[132:135], v[232:235], v[84:87]
	v_mfma_f32_16x16x32_bf16 v[76:79], v[140:143], v[232:235], v[76:79]
	s_setprio 0
	s_setprio 1
	v_mfma_f32_16x16x32_bf16 v[112:115], v[156:159], v[178:181], v[112:115]
	v_mfma_f32_16x16x32_bf16 v[104:107], v[164:167], v[178:181], v[104:107]
	v_mfma_f32_16x16x32_bf16 v[96:99], v[156:159], v[198:201], v[96:99]
	v_mfma_f32_16x16x32_bf16 v[88:91], v[164:167], v[198:201], v[88:91]
	v_mfma_f32_16x16x32_bf16 v[80:83], v[156:159], v[206:209], v[80:83]
	v_mfma_f32_16x16x32_bf16 v[72:75], v[164:167], v[206:209], v[72:75]
	v_mfma_f32_16x16x32_bf16 v[68:71], v[156:159], v[228:231], v[68:71]
	v_mfma_f32_16x16x32_bf16 v[64:67], v[164:167], v[228:231], v[64:67]
	v_mfma_f32_16x16x32_bf16 v[112:115], v[160:163], v[194:197], v[112:115]
	v_mfma_f32_16x16x32_bf16 v[104:107], v[174:177], v[194:197], v[104:107]
	v_mfma_f32_16x16x32_bf16 v[96:99], v[160:163], v[202:205], v[96:99]
	v_mfma_f32_16x16x32_bf16 v[88:91], v[174:177], v[202:205], v[88:91]
	v_mfma_f32_16x16x32_bf16 v[80:83], v[160:163], v[224:227], v[80:83]
	v_mfma_f32_16x16x32_bf16 v[72:75], v[174:177], v[224:227], v[72:75]
	v_mfma_f32_16x16x32_bf16 v[68:71], v[160:163], v[232:235], v[68:71]
	v_mfma_f32_16x16x32_bf16 v[64:67], v[174:177], v[232:235], v[64:67]
	s_setprio 0
	s_barrier
	s_add_i32 s28, s42, s62
	v_lshl_add_u64 v[182:183], s[50:51], 0, v[146:147]
	s_mov_b32 m0, s28
	ds_read_b128 v[178:181], v172 offset:16384
	ds_read_b128 v[194:197], v172 offset:17408
	ds_read_b128 v[198:201], v172 offset:18432
	ds_read_b128 v[202:205], v172 offset:19456
	ds_read_b128 v[206:209], v172 offset:20480
	ds_read_b128 v[224:227], v172 offset:21504
	ds_read_b128 v[228:231], v172 offset:22528
	ds_read_b128 v[232:235], v172 offset:23552
	global_load_lds_dwordx4 v[182:183], off
	s_add_i32 m0, s28, 0x2000
	s_add_u32 s28, s50, 0x80000
	v_lshl_add_u64 v[210:211], s[50:51], 0, v[150:151]
	s_addc_u32 s29, s51, 0
	s_add_i32 s42, s43, s62
	global_load_lds_dwordx4 v[210:211], off
	v_lshl_add_u64 v[236:237], s[28:29], 0, v[146:147]
	s_mov_b32 m0, s42
	v_lshl_add_u64 v[238:239], s[52:53], 0, v[148:149]
	global_load_lds_dwordx4 v[236:237], off
	v_lshl_add_u64 v[236:237], s[28:29], 0, v[150:151]
	s_add_i32 m0, s42, 0x2000
	s_nop 0
	global_load_lds_dwordx4 v[236:237], off
	v_lshl_add_u64 v[236:237], s[52:53], 0, v[144:145]
	s_mov_b32 m0, s88
	s_nop 0
	global_load_lds_dwordx4 v[236:237], off
	s_waitcnt vmcnt(7)
	s_waitcnt lgkmcnt(0)
	s_barrier
	s_setprio 1
	s_waitcnt lgkmcnt(0)
	v_mfma_f32_16x16x32_bf16 v[60:63], v[128:131], v[178:181], v[60:63]
	v_mfma_f32_16x16x32_bf16 v[56:59], v[136:139], v[178:181], v[56:59]
	s_mov_b32 m0, s89
	s_nop 0
	global_load_lds_dwordx4 v[238:239], off
	v_mfma_f32_16x16x32_bf16 v[52:55], v[128:131], v[198:201], v[52:55]
	v_mfma_f32_16x16x32_bf16 v[44:47], v[136:139], v[198:201], v[44:47]
	v_mfma_f32_16x16x32_bf16 v[36:39], v[128:131], v[206:209], v[36:39]
	v_mfma_f32_16x16x32_bf16 v[28:31], v[136:139], v[206:209], v[28:31]
	v_mfma_f32_16x16x32_bf16 v[20:23], v[128:131], v[228:231], v[20:23]
	v_mfma_f32_16x16x32_bf16 v[12:15], v[136:139], v[228:231], v[12:15]
	v_mfma_f32_16x16x32_bf16 v[60:63], v[132:135], v[194:197], v[60:63]
	v_mfma_f32_16x16x32_bf16 v[56:59], v[140:143], v[194:197], v[56:59]
	v_mfma_f32_16x16x32_bf16 v[52:55], v[132:135], v[202:205], v[52:55]
	v_mfma_f32_16x16x32_bf16 v[44:47], v[140:143], v[202:205], v[44:47]
	v_mfma_f32_16x16x32_bf16 v[36:39], v[132:135], v[224:227], v[36:39]
	v_mfma_f32_16x16x32_bf16 v[28:31], v[140:143], v[224:227], v[28:31]
	v_mfma_f32_16x16x32_bf16 v[20:23], v[132:135], v[232:235], v[20:23]
	v_mfma_f32_16x16x32_bf16 v[12:15], v[140:143], v[232:235], v[12:15]
	s_setprio 0
	s_setprio 1
	v_mfma_f32_16x16x32_bf16 v[48:51], v[156:159], v[178:181], v[48:51]
	v_mfma_f32_16x16x32_bf16 v[40:43], v[164:167], v[178:181], v[40:43]
	v_mfma_f32_16x16x32_bf16 v[32:35], v[156:159], v[198:201], v[32:35]
	v_mfma_f32_16x16x32_bf16 v[24:27], v[164:167], v[198:201], v[24:27]
	v_mfma_f32_16x16x32_bf16 v[16:19], v[156:159], v[206:209], v[16:19]
	v_mfma_f32_16x16x32_bf16 v[8:11], v[164:167], v[206:209], v[8:11]
	v_mfma_f32_16x16x32_bf16 v[4:7], v[156:159], v[228:231], v[4:7]
	v_mfma_f32_16x16x32_bf16 v[0:3], v[164:167], v[228:231], v[0:3]
	v_mfma_f32_16x16x32_bf16 v[48:51], v[160:163], v[194:197], v[48:51]
	v_mfma_f32_16x16x32_bf16 v[40:43], v[174:177], v[194:197], v[40:43]
	v_mfma_f32_16x16x32_bf16 v[32:35], v[160:163], v[202:205], v[32:35]
	v_mfma_f32_16x16x32_bf16 v[24:27], v[174:177], v[202:205], v[24:27]
	v_mfma_f32_16x16x32_bf16 v[16:19], v[160:163], v[224:227], v[16:19]
	v_mfma_f32_16x16x32_bf16 v[8:11], v[174:177], v[224:227], v[8:11]
	v_mfma_f32_16x16x32_bf16 v[4:7], v[160:163], v[232:235], v[4:7]
	v_mfma_f32_16x16x32_bf16 v[0:3], v[174:177], v[232:235], v[0:3]
	s_setprio 0
	s_barrier
	s_add_i32 s42, 0, 0x18000
	s_add_i32 s43, 0, 0x1c000
	v_add_u32_e32 v140, s42, v169
	v_add_u32_e32 v173, s43, v169
	ds_read_b128 v[128:131], v140
	ds_read_b128 v[132:135], v140 offset:1024
	ds_read_b128 v[136:139], v140 offset:2048
	ds_read_b128 v[140:143], v140 offset:3072
	ds_read_b128 v[156:159], v173
	ds_read_b128 v[160:163], v173 offset:1024
	ds_read_b128 v[164:167], v173 offset:2048
	ds_read_b128 v[174:177], v173 offset:3072
	s_add_u32 s28, s52, 0x80000
	s_addc_u32 s29, s53, 0
	s_mov_b32 m0, s26
	v_lshl_add_u64 v[240:241], s[28:29], 0, v[144:145]
	ds_read_b128 v[178:181], v172 offset:32768
	ds_read_b128 v[194:197], v172 offset:33792
	ds_read_b128 v[198:201], v172 offset:34816
	ds_read_b128 v[202:205], v172 offset:35840
	ds_read_b128 v[206:209], v172 offset:36864
	ds_read_b128 v[224:227], v172 offset:37888
	ds_read_b128 v[228:231], v172 offset:38912
	ds_read_b128 v[232:235], v172 offset:39936
	global_load_lds_dwordx4 v[240:241], off
	v_lshl_add_u64 v[240:241], s[28:29], 0, v[148:149]
	s_waitcnt vmcnt(7)
	s_waitcnt lgkmcnt(0)
	s_barrier
	s_setprio 1
	s_waitcnt lgkmcnt(0)
	v_mfma_f32_16x16x32_bf16 v[124:127], v[128:131], v[178:181], v[124:127]
	v_mfma_f32_16x16x32_bf16 v[120:123], v[136:139], v[178:181], v[120:123]
	s_mov_b32 m0, s27
	s_nop 0
	global_load_lds_dwordx4 v[240:241], off
	v_mfma_f32_16x16x32_bf16 v[116:119], v[128:131], v[198:201], v[116:119]
	v_mfma_f32_16x16x32_bf16 v[108:111], v[136:139], v[198:201], v[108:111]
	v_mfma_f32_16x16x32_bf16 v[100:103], v[128:131], v[206:209], v[100:103]
	v_mfma_f32_16x16x32_bf16 v[92:95], v[136:139], v[206:209], v[92:95]
	v_mfma_f32_16x16x32_bf16 v[84:87], v[128:131], v[228:231], v[84:87]
	v_mfma_f32_16x16x32_bf16 v[76:79], v[136:139], v[228:231], v[76:79]
	v_mfma_f32_16x16x32_bf16 v[124:127], v[132:135], v[194:197], v[124:127]
	v_mfma_f32_16x16x32_bf16 v[120:123], v[140:143], v[194:197], v[120:123]
	v_mfma_f32_16x16x32_bf16 v[116:119], v[132:135], v[202:205], v[116:119]
	v_mfma_f32_16x16x32_bf16 v[108:111], v[140:143], v[202:205], v[108:111]
	v_mfma_f32_16x16x32_bf16 v[100:103], v[132:135], v[224:227], v[100:103]
	v_mfma_f32_16x16x32_bf16 v[92:95], v[140:143], v[224:227], v[92:95]
	v_mfma_f32_16x16x32_bf16 v[84:87], v[132:135], v[232:235], v[84:87]
	v_mfma_f32_16x16x32_bf16 v[76:79], v[140:143], v[232:235], v[76:79]
	s_setprio 0
	s_setprio 1
	v_mfma_f32_16x16x32_bf16 v[112:115], v[156:159], v[178:181], v[112:115]
	v_mfma_f32_16x16x32_bf16 v[104:107], v[164:167], v[178:181], v[104:107]
	v_mfma_f32_16x16x32_bf16 v[96:99], v[156:159], v[198:201], v[96:99]
	v_mfma_f32_16x16x32_bf16 v[88:91], v[164:167], v[198:201], v[88:91]
	v_mfma_f32_16x16x32_bf16 v[80:83], v[156:159], v[206:209], v[80:83]
	v_mfma_f32_16x16x32_bf16 v[72:75], v[164:167], v[206:209], v[72:75]
	v_mfma_f32_16x16x32_bf16 v[68:71], v[156:159], v[228:231], v[68:71]
	v_mfma_f32_16x16x32_bf16 v[64:67], v[164:167], v[228:231], v[64:67]
	v_mfma_f32_16x16x32_bf16 v[112:115], v[160:163], v[194:197], v[112:115]
	v_mfma_f32_16x16x32_bf16 v[104:107], v[174:177], v[194:197], v[104:107]
	v_mfma_f32_16x16x32_bf16 v[96:99], v[160:163], v[202:205], v[96:99]
	v_mfma_f32_16x16x32_bf16 v[88:91], v[174:177], v[202:205], v[88:91]
	v_mfma_f32_16x16x32_bf16 v[80:83], v[160:163], v[224:227], v[80:83]
	v_mfma_f32_16x16x32_bf16 v[72:75], v[174:177], v[224:227], v[72:75]
	v_mfma_f32_16x16x32_bf16 v[68:71], v[160:163], v[232:235], v[68:71]
	v_mfma_f32_16x16x32_bf16 v[64:67], v[174:177], v[232:235], v[64:67]
	s_setprio 0
	s_barrier
	s_add_i32 s28, s42, s62
	v_lshl_add_u64 v[182:183], v[182:183], 0, s[68:69]
	s_mov_b32 m0, s28
	ds_read_b128 v[178:181], v172 offset:49152
	ds_read_b128 v[194:197], v172 offset:50176
	ds_read_b128 v[198:201], v172 offset:51200
	ds_read_b128 v[202:205], v172 offset:52224
	ds_read_b128 v[206:209], v172 offset:53248
	ds_read_b128 v[224:227], v172 offset:54272
	ds_read_b128 v[228:231], v172 offset:55296
	ds_read_b128 v[232:235], v172 offset:56320
	global_load_lds_dwordx4 v[182:183], off
	s_add_i32 m0, s28, 0x2000
	s_add_u32 s28, s50, 0x80080
	v_lshl_add_u64 v[182:183], v[210:211], 0, s[68:69]
	s_addc_u32 s29, s51, 0
	s_add_i32 s42, s43, s62
	global_load_lds_dwordx4 v[182:183], off
	v_lshl_add_u64 v[182:183], s[28:29], 0, v[146:147]
	s_mov_b32 m0, s42
	s_nop 0
	global_load_lds_dwordx4 v[182:183], off
	v_lshl_add_u64 v[182:183], s[28:29], 0, v[150:151]
	s_add_i32 m0, s42, 0x2000
	s_nop 0
	global_load_lds_dwordx4 v[182:183], off
	v_lshl_add_u64 v[182:183], v[236:237], 0, s[68:69]
	s_mov_b32 m0, s94
	s_nop 0
	global_load_lds_dwordx4 v[182:183], off
	v_lshl_add_u64 v[182:183], v[238:239], 0, s[68:69]
	s_waitcnt vmcnt(7)
	s_waitcnt lgkmcnt(0)
	s_barrier
	s_setprio 1
	s_waitcnt lgkmcnt(0)
	v_mfma_f32_16x16x32_bf16 v[60:63], v[128:131], v[178:181], v[60:63]
	v_mfma_f32_16x16x32_bf16 v[56:59], v[136:139], v[178:181], v[56:59]
	s_mov_b32 m0, s95
	s_nop 0
	global_load_lds_dwordx4 v[182:183], off
	v_mfma_f32_16x16x32_bf16 v[52:55], v[128:131], v[198:201], v[52:55]
	v_mfma_f32_16x16x32_bf16 v[44:47], v[136:139], v[198:201], v[44:47]
	v_mfma_f32_16x16x32_bf16 v[36:39], v[128:131], v[206:209], v[36:39]
	v_mfma_f32_16x16x32_bf16 v[28:31], v[136:139], v[206:209], v[28:31]
	v_mfma_f32_16x16x32_bf16 v[20:23], v[128:131], v[228:231], v[20:23]
	v_mfma_f32_16x16x32_bf16 v[12:15], v[136:139], v[228:231], v[12:15]
	v_mfma_f32_16x16x32_bf16 v[60:63], v[132:135], v[194:197], v[60:63]
	v_mfma_f32_16x16x32_bf16 v[56:59], v[140:143], v[194:197], v[56:59]
	v_mfma_f32_16x16x32_bf16 v[52:55], v[132:135], v[202:205], v[52:55]
	v_mfma_f32_16x16x32_bf16 v[44:47], v[140:143], v[202:205], v[44:47]
	v_mfma_f32_16x16x32_bf16 v[36:39], v[132:135], v[224:227], v[36:39]
	v_mfma_f32_16x16x32_bf16 v[28:31], v[140:143], v[224:227], v[28:31]
	v_mfma_f32_16x16x32_bf16 v[20:23], v[132:135], v[232:235], v[20:23]
	v_mfma_f32_16x16x32_bf16 v[12:15], v[140:143], v[232:235], v[12:15]
	s_setprio 0
	s_setprio 1
	v_mfma_f32_16x16x32_bf16 v[48:51], v[156:159], v[178:181], v[48:51]
	v_mfma_f32_16x16x32_bf16 v[40:43], v[164:167], v[178:181], v[40:43]
	v_mfma_f32_16x16x32_bf16 v[32:35], v[156:159], v[198:201], v[32:35]
	v_mfma_f32_16x16x32_bf16 v[24:27], v[164:167], v[198:201], v[24:27]
	v_mfma_f32_16x16x32_bf16 v[16:19], v[156:159], v[206:209], v[16:19]
	v_mfma_f32_16x16x32_bf16 v[8:11], v[164:167], v[206:209], v[8:11]
	v_mfma_f32_16x16x32_bf16 v[4:7], v[156:159], v[228:231], v[4:7]
	v_mfma_f32_16x16x32_bf16 v[0:3], v[164:167], v[228:231], v[0:3]
	v_mfma_f32_16x16x32_bf16 v[48:51], v[160:163], v[194:197], v[48:51]
	v_mfma_f32_16x16x32_bf16 v[40:43], v[174:177], v[194:197], v[40:43]
	v_mfma_f32_16x16x32_bf16 v[32:35], v[160:163], v[202:205], v[32:35]
	v_mfma_f32_16x16x32_bf16 v[24:27], v[174:177], v[202:205], v[24:27]
	v_mfma_f32_16x16x32_bf16 v[16:19], v[160:163], v[224:227], v[16:19]
	v_mfma_f32_16x16x32_bf16 v[8:11], v[174:177], v[224:227], v[8:11]
	v_mfma_f32_16x16x32_bf16 v[4:7], v[160:163], v[232:235], v[4:7]
	v_mfma_f32_16x16x32_bf16 v[0:3], v[174:177], v[232:235], v[0:3]
	s_setprio 0
	s_barrier
	s_add_i32 vcc_hi, vcc_hi, 2
	s_add_u32 s36, s36, 0x100
	s_addc_u32 s37, s37, 0
	s_add_u32 s78, s78, 0x100
	s_addc_u32 s79, s79, 0
	s_cmp_gt_u32 vcc_hi, 29
	s_cbranch_scc0 .LBB0_378
	s_and_b64 vcc, exec, s[14:15]
	s_cbranch_vccz .LBB0_381
	s_barrier

.LBB0_682:
	s_add_u32 s18, s16, 0x100
	s_addc_u32 s19, s17, 0
	s_add_u32 s28, s45, s16
	s_addc_u32 s29, s46, s17
	s_cmp_eq_u32 s47, 4
	s_cselect_b32 s36, 0, s18
	s_cselect_b32 s37, 0, s19
	s_cselect_b32 s30, s44, s28
	s_cselect_b32 s31, s9, s29
	s_add_u32 s36, s64, s36
	s_addc_u32 s37, s65, s37
	s_add_i32 s28, 0, 0x10000
	s_add_i32 s29, 0, 0x14000
	v_add_u32_e32 v168, s28, v154
	v_add_u32_e32 v194, s29, v154
	ds_read_b128 v[156:159], v168
	ds_read_b128 v[160:163], v168 offset:1024
	ds_read_b128 v[164:167], v168 offset:2048
	ds_read_b128 v[168:171], v168 offset:3072
	ds_read_b128 v[172:175], v194
	ds_read_b128 v[176:179], v194 offset:1024
	ds_read_b128 v[180:183], v194 offset:2048
	ds_read_b128 v[194:197], v194 offset:3072
	v_lshl_add_u64 v[210:211], v[150:151], 0, s[16:17]
	s_add_i32 m0, s20, 0xc000
	ds_read_b128 v[198:201], v155
	ds_read_b128 v[202:205], v155 offset:1024
	ds_read_b128 v[206:209], v155 offset:2048
	ds_read_b128 v[224:227], v155 offset:3072
	ds_read_b128 v[228:231], v155 offset:4096
	ds_read_b128 v[232:235], v155 offset:5120
	ds_read_b128 v[236:239], v155 offset:6144
	ds_read_b128 v[240:243], v155 offset:7168
	global_load_lds_dwordx4 v[210:211], off
	v_lshl_add_u64 v[210:211], v[152:153], 0, s[16:17]
	s_waitcnt vmcnt(7)
	s_waitcnt lgkmcnt(0)
	s_barrier
	s_setprio 1
	s_waitcnt lgkmcnt(0)
	v_mfma_f32_16x16x32_bf16 v[124:127], v[156:159], v[198:201], v[124:127]
	v_mfma_f32_16x16x32_bf16 v[120:123], v[164:167], v[198:201], v[120:123]
	s_add_i32 m0, s20, 0xe000
	s_nop 0
	global_load_lds_dwordx4 v[210:211], off
	v_mfma_f32_16x16x32_bf16 v[116:119], v[156:159], v[206:209], v[116:119]
	v_mfma_f32_16x16x32_bf16 v[108:111], v[164:167], v[206:209], v[108:111]
	v_mfma_f32_16x16x32_bf16 v[100:103], v[156:159], v[228:231], v[100:103]
	v_mfma_f32_16x16x32_bf16 v[92:95], v[164:167], v[228:231], v[92:95]
	v_mfma_f32_16x16x32_bf16 v[84:87], v[156:159], v[236:239], v[84:87]
	v_mfma_f32_16x16x32_bf16 v[76:79], v[164:167], v[236:239], v[76:79]
	v_mfma_f32_16x16x32_bf16 v[124:127], v[160:163], v[202:205], v[124:127]
	v_mfma_f32_16x16x32_bf16 v[120:123], v[168:171], v[202:205], v[120:123]
	v_mfma_f32_16x16x32_bf16 v[116:119], v[160:163], v[224:227], v[116:119]
	v_mfma_f32_16x16x32_bf16 v[108:111], v[168:171], v[224:227], v[108:111]
	v_mfma_f32_16x16x32_bf16 v[100:103], v[160:163], v[232:235], v[100:103]
	v_mfma_f32_16x16x32_bf16 v[92:95], v[168:171], v[232:235], v[92:95]
	v_mfma_f32_16x16x32_bf16 v[84:87], v[160:163], v[240:243], v[84:87]
	v_mfma_f32_16x16x32_bf16 v[76:79], v[168:171], v[240:243], v[76:79]
	s_setprio 0
	s_setprio 1
	v_mfma_f32_16x16x32_bf16 v[112:115], v[172:175], v[198:201], v[112:115]
	v_mfma_f32_16x16x32_bf16 v[104:107], v[180:183], v[198:201], v[104:107]
	v_mfma_f32_16x16x32_bf16 v[96:99], v[172:175], v[206:209], v[96:99]
	v_mfma_f32_16x16x32_bf16 v[88:91], v[180:183], v[206:209], v[88:91]
	v_mfma_f32_16x16x32_bf16 v[80:83], v[172:175], v[228:231], v[80:83]
	v_mfma_f32_16x16x32_bf16 v[72:75], v[180:183], v[228:231], v[72:75]
	v_mfma_f32_16x16x32_bf16 v[68:71], v[172:175], v[236:239], v[68:71]
	v_mfma_f32_16x16x32_bf16 v[64:67], v[180:183], v[236:239], v[64:67]
	v_mfma_f32_16x16x32_bf16 v[112:115], v[176:179], v[202:205], v[112:115]
	v_mfma_f32_16x16x32_bf16 v[104:107], v[194:197], v[202:205], v[104:107]
	v_mfma_f32_16x16x32_bf16 v[96:99], v[176:179], v[224:227], v[96:99]
	v_mfma_f32_16x16x32_bf16 v[88:91], v[194:197], v[224:227], v[88:91]
	v_mfma_f32_16x16x32_bf16 v[80:83], v[176:179], v[232:235], v[80:83]
	v_mfma_f32_16x16x32_bf16 v[72:75], v[194:197], v[232:235], v[72:75]
	v_mfma_f32_16x16x32_bf16 v[68:71], v[176:179], v[240:243], v[68:71]
	v_mfma_f32_16x16x32_bf16 v[64:67], v[194:197], v[240:243], v[64:67]
	s_setprio 0
	s_barrier
	s_add_i32 s16, s28, s4
	v_lshl_add_u64 v[210:211], s[30:31], 0, v[184:185]
	s_mov_b32 m0, s16
	ds_read_b128 v[198:201], v155 offset:16384
	ds_read_b128 v[202:205], v155 offset:17408
	ds_read_b128 v[206:209], v155 offset:18432
	ds_read_b128 v[224:227], v155 offset:19456
	ds_read_b128 v[228:231], v155 offset:20480
	ds_read_b128 v[232:235], v155 offset:21504
	ds_read_b128 v[236:239], v155 offset:22528
	ds_read_b128 v[240:243], v155 offset:23552
	global_load_lds_dwordx4 v[210:211], off
	s_add_i32 m0, s16, 0x2000
	s_add_u32 s16, s30, 0x20000
	v_lshl_add_u64 v[244:245], s[30:31], 0, v[128:129]
	s_addc_u32 s17, s31, 0
	s_add_i32 s28, s29, s4
	global_load_lds_dwordx4 v[244:245], off
	v_lshl_add_u64 v[246:247], s[16:17], 0, v[184:185]
	s_mov_b32 m0, s28
	v_lshl_add_u64 v[218:219], s[36:37], 0, v[130:131]
	global_load_lds_dwordx4 v[246:247], off
	v_lshl_add_u64 v[246:247], s[16:17], 0, v[128:129]
	s_add_i32 m0, s28, 0x2000
	s_nop 0
	global_load_lds_dwordx4 v[246:247], off
	v_lshl_add_u64 v[246:247], s[36:37], 0, v[132:133]
	s_mov_b32 m0, s20
	s_nop 0
	global_load_lds_dwordx4 v[246:247], off
	s_waitcnt vmcnt(7)
	s_waitcnt lgkmcnt(0)
	s_barrier
	s_setprio 1
	s_waitcnt lgkmcnt(0)
	v_mfma_f32_16x16x32_bf16 v[60:63], v[156:159], v[198:201], v[60:63]
	v_mfma_f32_16x16x32_bf16 v[56:59], v[164:167], v[198:201], v[56:59]
	s_mov_b32 m0, s21
	s_nop 0
	global_load_lds_dwordx4 v[218:219], off
	v_mfma_f32_16x16x32_bf16 v[52:55], v[156:159], v[206:209], v[52:55]
	v_mfma_f32_16x16x32_bf16 v[44:47], v[164:167], v[206:209], v[44:47]
	v_mfma_f32_16x16x32_bf16 v[36:39], v[156:159], v[228:231], v[36:39]
	v_mfma_f32_16x16x32_bf16 v[28:31], v[164:167], v[228:231], v[28:31]
	v_mfma_f32_16x16x32_bf16 v[20:23], v[156:159], v[236:239], v[20:23]
	v_mfma_f32_16x16x32_bf16 v[12:15], v[164:167], v[236:239], v[12:15]
	v_mfma_f32_16x16x32_bf16 v[60:63], v[160:163], v[202:205], v[60:63]
	v_mfma_f32_16x16x32_bf16 v[56:59], v[168:171], v[202:205], v[56:59]
	v_mfma_f32_16x16x32_bf16 v[52:55], v[160:163], v[224:227], v[52:55]
	v_mfma_f32_16x16x32_bf16 v[44:47], v[168:171], v[224:227], v[44:47]
	v_mfma_f32_16x16x32_bf16 v[36:39], v[160:163], v[232:235], v[36:39]
	v_mfma_f32_16x16x32_bf16 v[28:31], v[168:171], v[232:235], v[28:31]
	v_mfma_f32_16x16x32_bf16 v[20:23], v[160:163], v[240:243], v[20:23]
	v_mfma_f32_16x16x32_bf16 v[12:15], v[168:171], v[240:243], v[12:15]
	s_setprio 0
	s_setprio 1
	v_mfma_f32_16x16x32_bf16 v[48:51], v[172:175], v[198:201], v[48:51]
	v_mfma_f32_16x16x32_bf16 v[40:43], v[180:183], v[198:201], v[40:43]
	v_mfma_f32_16x16x32_bf16 v[32:35], v[172:175], v[206:209], v[32:35]
	v_mfma_f32_16x16x32_bf16 v[24:27], v[180:183], v[206:209], v[24:27]
	v_mfma_f32_16x16x32_bf16 v[16:19], v[172:175], v[228:231], v[16:19]
	v_mfma_f32_16x16x32_bf16 v[8:11], v[180:183], v[228:231], v[8:11]
	v_mfma_f32_16x16x32_bf16 v[4:7], v[172:175], v[236:239], v[4:7]
	v_mfma_f32_16x16x32_bf16 v[0:3], v[180:183], v[236:239], v[0:3]
	v_mfma_f32_16x16x32_bf16 v[48:51], v[176:179], v[202:205], v[48:51]
	v_mfma_f32_16x16x32_bf16 v[40:43], v[194:197], v[202:205], v[40:43]
	v_mfma_f32_16x16x32_bf16 v[32:35], v[176:179], v[224:227], v[32:35]
	v_mfma_f32_16x16x32_bf16 v[24:27], v[194:197], v[224:227], v[24:27]
	v_mfma_f32_16x16x32_bf16 v[16:19], v[176:179], v[232:235], v[16:19]
	v_mfma_f32_16x16x32_bf16 v[8:11], v[194:197], v[232:235], v[8:11]
	v_mfma_f32_16x16x32_bf16 v[4:7], v[176:179], v[240:243], v[4:7]
	v_mfma_f32_16x16x32_bf16 v[0:3], v[194:197], v[240:243], v[0:3]
	s_setprio 0
	s_barrier
	s_add_i32 s28, 0, 0x18000
	s_add_i32 s29, 0, 0x1c000
	v_add_u32_e32 v168, s28, v154
	v_add_u32_e32 v194, s29, v154
	ds_read_b128 v[156:159], v168
	ds_read_b128 v[160:163], v168 offset:1024
	ds_read_b128 v[164:167], v168 offset:2048
	ds_read_b128 v[168:171], v168 offset:3072
	ds_read_b128 v[172:175], v194
	ds_read_b128 v[176:179], v194 offset:1024
	ds_read_b128 v[180:183], v194 offset:2048
	ds_read_b128 v[194:197], v194 offset:3072
	s_add_u32 s16, s36, 0x20000
	s_addc_u32 s17, s37, 0
	s_mov_b32 m0, s26
	v_lshl_add_u64 v[216:217], s[16:17], 0, v[132:133]
	ds_read_b128 v[198:201], v155 offset:32768
	ds_read_b128 v[202:205], v155 offset:33792
	ds_read_b128 v[206:209], v155 offset:34816
	ds_read_b128 v[224:227], v155 offset:35840
	ds_read_b128 v[228:231], v155 offset:36864
	ds_read_b128 v[232:235], v155 offset:37888
	ds_read_b128 v[236:239], v155 offset:38912
	ds_read_b128 v[240:243], v155 offset:39936
	global_load_lds_dwordx4 v[216:217], off
	v_lshl_add_u64 v[216:217], s[16:17], 0, v[130:131]
	s_waitcnt vmcnt(7)
	s_waitcnt lgkmcnt(0)
	s_barrier
	s_setprio 1
	s_waitcnt lgkmcnt(0)
	v_mfma_f32_16x16x32_bf16 v[124:127], v[156:159], v[198:201], v[124:127]
	v_mfma_f32_16x16x32_bf16 v[120:123], v[164:167], v[198:201], v[120:123]
	s_mov_b32 m0, s27
	s_nop 0
	global_load_lds_dwordx4 v[216:217], off
	v_mfma_f32_16x16x32_bf16 v[116:119], v[156:159], v[206:209], v[116:119]
	v_mfma_f32_16x16x32_bf16 v[108:111], v[164:167], v[206:209], v[108:111]
	v_mfma_f32_16x16x32_bf16 v[100:103], v[156:159], v[228:231], v[100:103]
	v_mfma_f32_16x16x32_bf16 v[92:95], v[164:167], v[228:231], v[92:95]
	v_mfma_f32_16x16x32_bf16 v[84:87], v[156:159], v[236:239], v[84:87]
	v_mfma_f32_16x16x32_bf16 v[76:79], v[164:167], v[236:239], v[76:79]
	v_mfma_f32_16x16x32_bf16 v[124:127], v[160:163], v[202:205], v[124:127]
	v_mfma_f32_16x16x32_bf16 v[120:123], v[168:171], v[202:205], v[120:123]
	v_mfma_f32_16x16x32_bf16 v[116:119], v[160:163], v[224:227], v[116:119]
	v_mfma_f32_16x16x32_bf16 v[108:111], v[168:171], v[224:227], v[108:111]
	v_mfma_f32_16x16x32_bf16 v[100:103], v[160:163], v[232:235], v[100:103]
	v_mfma_f32_16x16x32_bf16 v[92:95], v[168:171], v[232:235], v[92:95]
	v_mfma_f32_16x16x32_bf16 v[84:87], v[160:163], v[240:243], v[84:87]
	v_mfma_f32_16x16x32_bf16 v[76:79], v[168:171], v[240:243], v[76:79]
	s_setprio 0
	s_setprio 1
	v_mfma_f32_16x16x32_bf16 v[112:115], v[172:175], v[198:201], v[112:115]
	v_mfma_f32_16x16x32_bf16 v[104:107], v[180:183], v[198:201], v[104:107]
	v_mfma_f32_16x16x32_bf16 v[96:99], v[172:175], v[206:209], v[96:99]
	v_mfma_f32_16x16x32_bf16 v[88:91], v[180:183], v[206:209], v[88:91]
	v_mfma_f32_16x16x32_bf16 v[80:83], v[172:175], v[228:231], v[80:83]
	v_mfma_f32_16x16x32_bf16 v[72:75], v[180:183], v[228:231], v[72:75]
	v_mfma_f32_16x16x32_bf16 v[68:71], v[172:175], v[236:239], v[68:71]
	v_mfma_f32_16x16x32_bf16 v[64:67], v[180:183], v[236:239], v[64:67]
	v_mfma_f32_16x16x32_bf16 v[112:115], v[176:179], v[202:205], v[112:115]
	v_mfma_f32_16x16x32_bf16 v[104:107], v[194:197], v[202:205], v[104:107]
	v_mfma_f32_16x16x32_bf16 v[96:99], v[176:179], v[224:227], v[96:99]
	v_mfma_f32_16x16x32_bf16 v[88:91], v[194:197], v[224:227], v[88:91]
	v_mfma_f32_16x16x32_bf16 v[80:83], v[176:179], v[232:235], v[80:83]
	v_mfma_f32_16x16x32_bf16 v[72:75], v[194:197], v[232:235], v[72:75]
	v_mfma_f32_16x16x32_bf16 v[68:71], v[176:179], v[240:243], v[68:71]
	v_mfma_f32_16x16x32_bf16 v[64:67], v[194:197], v[240:243], v[64:67]
	s_setprio 0
	s_barrier
	s_add_i32 s16, s28, s4
	v_lshl_add_u64 v[210:211], v[210:211], 0, s[68:69]
	s_mov_b32 m0, s16
	ds_read_b128 v[198:201], v155 offset:49152
	ds_read_b128 v[202:205], v155 offset:50176
	ds_read_b128 v[206:209], v155 offset:51200
	ds_read_b128 v[224:227], v155 offset:52224
	ds_read_b128 v[228:231], v155 offset:53248
	ds_read_b128 v[232:235], v155 offset:54272
	ds_read_b128 v[236:239], v155 offset:55296
	ds_read_b128 v[240:243], v155 offset:56320
	global_load_lds_dwordx4 v[210:211], off
	s_add_i32 m0, s16, 0x2000
	s_add_u32 s16, s30, 0x20080
	v_lshl_add_u64 v[210:211], v[244:245], 0, s[68:69]
	s_addc_u32 s17, s31, 0
	s_add_i32 s28, s29, s4
	global_load_lds_dwordx4 v[210:211], off
	v_lshl_add_u64 v[210:211], s[16:17], 0, v[184:185]
	s_mov_b32 m0, s28
	s_nop 0
	global_load_lds_dwordx4 v[210:211], off
	v_lshl_add_u64 v[210:211], s[16:17], 0, v[128:129]
	s_add_i32 m0, s28, 0x2000
	s_nop 0
	global_load_lds_dwordx4 v[210:211], off
	v_lshl_add_u64 v[210:211], v[246:247], 0, s[68:69]
	s_mov_b32 m0, s38
	s_nop 0
	global_load_lds_dwordx4 v[210:211], off
	v_lshl_add_u64 v[210:211], v[218:219], 0, s[68:69]
	s_waitcnt vmcnt(7)
	s_waitcnt lgkmcnt(0)
	s_barrier
	s_setprio 1
	s_waitcnt lgkmcnt(0)
	v_mfma_f32_16x16x32_bf16 v[60:63], v[156:159], v[198:201], v[60:63]
	v_mfma_f32_16x16x32_bf16 v[56:59], v[164:167], v[198:201], v[56:59]
	s_mov_b32 m0, s39
	s_nop 0
	global_load_lds_dwordx4 v[210:211], off
	v_mfma_f32_16x16x32_bf16 v[52:55], v[156:159], v[206:209], v[52:55]
	v_mfma_f32_16x16x32_bf16 v[44:47], v[164:167], v[206:209], v[44:47]
	v_mfma_f32_16x16x32_bf16 v[36:39], v[156:159], v[228:231], v[36:39]
	v_mfma_f32_16x16x32_bf16 v[28:31], v[164:167], v[228:231], v[28:31]
	v_mfma_f32_16x16x32_bf16 v[20:23], v[156:159], v[236:239], v[20:23]
	v_mfma_f32_16x16x32_bf16 v[12:15], v[164:167], v[236:239], v[12:15]
	v_mfma_f32_16x16x32_bf16 v[60:63], v[160:163], v[202:205], v[60:63]
	v_mfma_f32_16x16x32_bf16 v[56:59], v[168:171], v[202:205], v[56:59]
	v_mfma_f32_16x16x32_bf16 v[52:55], v[160:163], v[224:227], v[52:55]
	v_mfma_f32_16x16x32_bf16 v[44:47], v[168:171], v[224:227], v[44:47]
	v_mfma_f32_16x16x32_bf16 v[36:39], v[160:163], v[232:235], v[36:39]
	v_mfma_f32_16x16x32_bf16 v[28:31], v[168:171], v[232:235], v[28:31]
	v_mfma_f32_16x16x32_bf16 v[20:23], v[160:163], v[240:243], v[20:23]
	v_mfma_f32_16x16x32_bf16 v[12:15], v[168:171], v[240:243], v[12:15]
	s_setprio 0
	s_setprio 1
	v_mfma_f32_16x16x32_bf16 v[48:51], v[172:175], v[198:201], v[48:51]
	v_mfma_f32_16x16x32_bf16 v[40:43], v[180:183], v[198:201], v[40:43]
	v_mfma_f32_16x16x32_bf16 v[32:35], v[172:175], v[206:209], v[32:35]
	v_mfma_f32_16x16x32_bf16 v[24:27], v[180:183], v[206:209], v[24:27]
	v_mfma_f32_16x16x32_bf16 v[16:19], v[172:175], v[228:231], v[16:19]
	v_mfma_f32_16x16x32_bf16 v[8:11], v[180:183], v[228:231], v[8:11]
	v_mfma_f32_16x16x32_bf16 v[4:7], v[172:175], v[236:239], v[4:7]
	v_mfma_f32_16x16x32_bf16 v[0:3], v[180:183], v[236:239], v[0:3]
	v_mfma_f32_16x16x32_bf16 v[48:51], v[176:179], v[202:205], v[48:51]
	v_mfma_f32_16x16x32_bf16 v[40:43], v[194:197], v[202:205], v[40:43]
	v_mfma_f32_16x16x32_bf16 v[32:35], v[176:179], v[224:227], v[32:35]
	v_mfma_f32_16x16x32_bf16 v[24:27], v[194:197], v[224:227], v[24:27]
	v_mfma_f32_16x16x32_bf16 v[16:19], v[176:179], v[232:235], v[16:19]
	v_mfma_f32_16x16x32_bf16 v[8:11], v[194:197], v[232:235], v[8:11]
	v_mfma_f32_16x16x32_bf16 v[4:7], v[176:179], v[240:243], v[4:7]
	v_mfma_f32_16x16x32_bf16 v[0:3], v[194:197], v[240:243], v[0:3]
	s_setprio 0
	s_barrier
	s_add_i32 s47, s47, 2
	s_cmp_gt_u32 s47, 5
	s_mov_b64 s[16:17], s[18:19]
	s_cbranch_scc0 .LBB0_682
	s_and_b64 vcc, exec, s[6:7]
	s_cbranch_vccz .LBB0_685
	s_barrier

.LBB0_805:
	s_add_u32 s28, s30, 0xfff80080
	s_addc_u32 s29, s31, -1
	s_add_i32 s38, 0, 0x10000
	s_cmp_eq_u32 s78, 28
	s_cselect_b32 s45, s9, s29
	s_cselect_b32 s44, s11, s28
	s_cselect_b32 s41, s60, s63
	s_cselect_b32 s40, s61, s62
	s_add_i32 s39, 0, 0x14000
	v_add_u32_e32 v154, s38, v143
	v_add_u32_e32 v170, s39, v143
	ds_read_b128 v[138:141], v154
	ds_read_b128 v[146:149], v154 offset:1024
	ds_read_b128 v[150:153], v154 offset:2048
	ds_read_b128 v[154:157], v154 offset:3072
	ds_read_b128 v[158:161], v170
	ds_read_b128 v[162:165], v170 offset:1024
	ds_read_b128 v[166:169], v170 offset:2048
	ds_read_b128 v[170:173], v170 offset:3072
	v_lshl_add_u64 v[182:183], s[30:31], 0, v[134:135]
	s_add_i32 m0, s21, 0xc000
	ds_read_b128 v[174:177], v145
	ds_read_b128 v[178:181], v145 offset:1024
	ds_read_b128 v[194:197], v145 offset:2048
	ds_read_b128 v[198:201], v145 offset:3072
	ds_read_b128 v[202:205], v145 offset:4096
	ds_read_b128 v[206:209], v145 offset:5120
	ds_read_b128 v[224:227], v145 offset:6144
	ds_read_b128 v[228:231], v145 offset:7168
	global_load_lds_dwordx4 v[182:183], off
	v_lshl_add_u64 v[182:183], s[30:31], 0, v[136:137]
	s_waitcnt vmcnt(7)
	s_waitcnt lgkmcnt(0)
	s_barrier
	s_setprio 1
	s_waitcnt lgkmcnt(0)
	v_mfma_f32_16x16x32_bf16 v[124:127], v[138:141], v[174:177], v[124:127]
	v_mfma_f32_16x16x32_bf16 v[120:123], v[150:153], v[174:177], v[120:123]
	s_add_i32 m0, s21, 0xe000
	s_nop 0
	global_load_lds_dwordx4 v[182:183], off
	v_mfma_f32_16x16x32_bf16 v[116:119], v[138:141], v[194:197], v[116:119]
	v_mfma_f32_16x16x32_bf16 v[104:107], v[150:153], v[194:197], v[104:107]
	v_mfma_f32_16x16x32_bf16 v[100:103], v[138:141], v[202:205], v[100:103]
	v_mfma_f32_16x16x32_bf16 v[88:91], v[150:153], v[202:205], v[88:91]
	v_mfma_f32_16x16x32_bf16 v[84:87], v[138:141], v[224:227], v[84:87]
	v_mfma_f32_16x16x32_bf16 v[72:75], v[150:153], v[224:227], v[72:75]
	v_mfma_f32_16x16x32_bf16 v[124:127], v[146:149], v[178:181], v[124:127]
	v_mfma_f32_16x16x32_bf16 v[120:123], v[154:157], v[178:181], v[120:123]
	v_mfma_f32_16x16x32_bf16 v[116:119], v[146:149], v[198:201], v[116:119]
	v_mfma_f32_16x16x32_bf16 v[104:107], v[154:157], v[198:201], v[104:107]
	v_mfma_f32_16x16x32_bf16 v[100:103], v[146:149], v[206:209], v[100:103]
	v_mfma_f32_16x16x32_bf16 v[88:91], v[154:157], v[206:209], v[88:91]
	v_mfma_f32_16x16x32_bf16 v[84:87], v[146:149], v[228:231], v[84:87]
	v_mfma_f32_16x16x32_bf16 v[72:75], v[154:157], v[228:231], v[72:75]
	s_setprio 0
	s_setprio 1
	v_mfma_f32_16x16x32_bf16 v[112:115], v[158:161], v[174:177], v[112:115]
	v_mfma_f32_16x16x32_bf16 v[108:111], v[166:169], v[174:177], v[108:111]
	v_mfma_f32_16x16x32_bf16 v[96:99], v[158:161], v[194:197], v[96:99]
	v_mfma_f32_16x16x32_bf16 v[92:95], v[166:169], v[194:197], v[92:95]
	v_mfma_f32_16x16x32_bf16 v[80:83], v[158:161], v[202:205], v[80:83]
	v_mfma_f32_16x16x32_bf16 v[76:79], v[166:169], v[202:205], v[76:79]
	v_mfma_f32_16x16x32_bf16 v[68:71], v[158:161], v[224:227], v[68:71]
	v_mfma_f32_16x16x32_bf16 v[64:67], v[166:169], v[224:227], v[64:67]
	v_mfma_f32_16x16x32_bf16 v[112:115], v[162:165], v[178:181], v[112:115]
	v_mfma_f32_16x16x32_bf16 v[108:111], v[170:173], v[178:181], v[108:111]
	v_mfma_f32_16x16x32_bf16 v[96:99], v[162:165], v[198:201], v[96:99]
	v_mfma_f32_16x16x32_bf16 v[92:95], v[170:173], v[198:201], v[92:95]
	v_mfma_f32_16x16x32_bf16 v[80:83], v[162:165], v[206:209], v[80:83]
	v_mfma_f32_16x16x32_bf16 v[76:79], v[170:173], v[206:209], v[76:79]
	v_mfma_f32_16x16x32_bf16 v[68:71], v[162:165], v[228:231], v[68:71]
	v_mfma_f32_16x16x32_bf16 v[64:67], v[170:173], v[228:231], v[64:67]
	s_setprio 0
	s_barrier
	s_add_i32 s28, s38, s20
	v_lshl_add_u64 v[182:183], s[40:41], 0, v[184:185]
	s_mov_b32 m0, s28
	ds_read_b128 v[174:177], v145 offset:16384
	ds_read_b128 v[178:181], v145 offset:17408
	ds_read_b128 v[194:197], v145 offset:18432
	ds_read_b128 v[198:201], v145 offset:19456
	ds_read_b128 v[202:205], v145 offset:20480
	ds_read_b128 v[206:209], v145 offset:21504
	ds_read_b128 v[224:227], v145 offset:22528
	ds_read_b128 v[228:231], v145 offset:23552
	global_load_lds_dwordx4 v[182:183], off
	s_add_i32 m0, s28, 0x2000
	s_add_u32 s28, s40, 0x80000
	v_lshl_add_u64 v[210:211], s[40:41], 0, v[128:129]
	s_addc_u32 s29, s41, 0
	s_add_i32 s38, s39, s20
	global_load_lds_dwordx4 v[210:211], off
	v_lshl_add_u64 v[216:217], s[28:29], 0, v[184:185]
	s_mov_b32 m0, s38
	v_lshl_add_u64 v[218:219], s[44:45], 0, v[130:131]
	global_load_lds_dwordx4 v[216:217], off
	v_lshl_add_u64 v[216:217], s[28:29], 0, v[128:129]
	s_add_i32 m0, s38, 0x2000
	s_nop 0
	global_load_lds_dwordx4 v[216:217], off
	v_lshl_add_u64 v[216:217], s[44:45], 0, v[132:133]
	s_mov_b32 m0, s21
	s_nop 0
	global_load_lds_dwordx4 v[216:217], off
	s_waitcnt vmcnt(7)
	s_waitcnt lgkmcnt(0)
	s_barrier
	s_setprio 1
	s_waitcnt lgkmcnt(0)
	v_mfma_f32_16x16x32_bf16 v[60:63], v[138:141], v[174:177], v[60:63]
	v_mfma_f32_16x16x32_bf16 v[56:59], v[150:153], v[174:177], v[56:59]
	s_mov_b32 m0, s46
	s_nop 0
	global_load_lds_dwordx4 v[218:219], off
	v_mfma_f32_16x16x32_bf16 v[52:55], v[138:141], v[194:197], v[52:55]
	v_mfma_f32_16x16x32_bf16 v[40:43], v[150:153], v[194:197], v[40:43]
	v_mfma_f32_16x16x32_bf16 v[36:39], v[138:141], v[202:205], v[36:39]
	v_mfma_f32_16x16x32_bf16 v[24:27], v[150:153], v[202:205], v[24:27]
	v_mfma_f32_16x16x32_bf16 v[20:23], v[138:141], v[224:227], v[20:23]
	v_mfma_f32_16x16x32_bf16 v[8:11], v[150:153], v[224:227], v[8:11]
	v_mfma_f32_16x16x32_bf16 v[60:63], v[146:149], v[178:181], v[60:63]
	v_mfma_f32_16x16x32_bf16 v[56:59], v[154:157], v[178:181], v[56:59]
	v_mfma_f32_16x16x32_bf16 v[52:55], v[146:149], v[198:201], v[52:55]
	v_mfma_f32_16x16x32_bf16 v[40:43], v[154:157], v[198:201], v[40:43]
	v_mfma_f32_16x16x32_bf16 v[36:39], v[146:149], v[206:209], v[36:39]
	v_mfma_f32_16x16x32_bf16 v[24:27], v[154:157], v[206:209], v[24:27]
	v_mfma_f32_16x16x32_bf16 v[20:23], v[146:149], v[228:231], v[20:23]
	v_mfma_f32_16x16x32_bf16 v[8:11], v[154:157], v[228:231], v[8:11]
	s_setprio 0
	s_setprio 1
	v_mfma_f32_16x16x32_bf16 v[48:51], v[158:161], v[174:177], v[48:51]
	v_mfma_f32_16x16x32_bf16 v[44:47], v[166:169], v[174:177], v[44:47]
	v_mfma_f32_16x16x32_bf16 v[32:35], v[158:161], v[194:197], v[32:35]
	v_mfma_f32_16x16x32_bf16 v[28:31], v[166:169], v[194:197], v[28:31]
	v_mfma_f32_16x16x32_bf16 v[16:19], v[158:161], v[202:205], v[16:19]
	v_mfma_f32_16x16x32_bf16 v[12:15], v[166:169], v[202:205], v[12:15]
	v_mfma_f32_16x16x32_bf16 v[4:7], v[158:161], v[224:227], v[4:7]
	v_mfma_f32_16x16x32_bf16 v[0:3], v[166:169], v[224:227], v[0:3]
	v_mfma_f32_16x16x32_bf16 v[48:51], v[162:165], v[178:181], v[48:51]
	v_mfma_f32_16x16x32_bf16 v[44:47], v[170:173], v[178:181], v[44:47]
	v_mfma_f32_16x16x32_bf16 v[32:35], v[162:165], v[198:201], v[32:35]
	v_mfma_f32_16x16x32_bf16 v[28:31], v[170:173], v[198:201], v[28:31]
	v_mfma_f32_16x16x32_bf16 v[16:19], v[162:165], v[206:209], v[16:19]
	v_mfma_f32_16x16x32_bf16 v[12:15], v[170:173], v[206:209], v[12:15]
	v_mfma_f32_16x16x32_bf16 v[4:7], v[162:165], v[228:231], v[4:7]
	v_mfma_f32_16x16x32_bf16 v[0:3], v[170:173], v[228:231], v[0:3]
	s_setprio 0
	s_barrier
	s_add_i32 s38, 0, 0x18000
	s_add_i32 s39, 0, 0x1c000
	v_add_u32_e32 v154, s38, v143
	v_add_u32_e32 v170, s39, v143
	ds_read_b128 v[138:141], v154
	ds_read_b128 v[146:149], v154 offset:1024
	ds_read_b128 v[150:153], v154 offset:2048
	ds_read_b128 v[154:157], v154 offset:3072
	ds_read_b128 v[158:161], v170
	ds_read_b128 v[162:165], v170 offset:1024
	ds_read_b128 v[166:169], v170 offset:2048
	ds_read_b128 v[170:173], v170 offset:3072
	s_add_u32 s28, s44, 0x80000
	s_addc_u32 s29, s45, 0
	s_mov_b32 m0, s47
	v_lshl_add_u64 v[232:233], s[28:29], 0, v[132:133]
	ds_read_b128 v[174:177], v145 offset:32768
	ds_read_b128 v[178:181], v145 offset:33792
	ds_read_b128 v[194:197], v145 offset:34816
	ds_read_b128 v[198:201], v145 offset:35840
	ds_read_b128 v[202:205], v145 offset:36864
	ds_read_b128 v[206:209], v145 offset:37888
	ds_read_b128 v[224:227], v145 offset:38912
	ds_read_b128 v[228:231], v145 offset:39936
	global_load_lds_dwordx4 v[232:233], off
	v_lshl_add_u64 v[232:233], s[28:29], 0, v[130:131]
	s_waitcnt vmcnt(7)
	s_waitcnt lgkmcnt(0)
	s_barrier
	s_setprio 1
	s_waitcnt lgkmcnt(0)
	v_mfma_f32_16x16x32_bf16 v[124:127], v[138:141], v[174:177], v[124:127]
	v_mfma_f32_16x16x32_bf16 v[120:123], v[150:153], v[174:177], v[120:123]
	s_mov_b32 m0, s50
	s_nop 0
	global_load_lds_dwordx4 v[232:233], off
	v_mfma_f32_16x16x32_bf16 v[116:119], v[138:141], v[194:197], v[116:119]
	v_mfma_f32_16x16x32_bf16 v[104:107], v[150:153], v[194:197], v[104:107]
	v_mfma_f32_16x16x32_bf16 v[100:103], v[138:141], v[202:205], v[100:103]
	v_mfma_f32_16x16x32_bf16 v[88:91], v[150:153], v[202:205], v[88:91]
	v_mfma_f32_16x16x32_bf16 v[84:87], v[138:141], v[224:227], v[84:87]
	v_mfma_f32_16x16x32_bf16 v[72:75], v[150:153], v[224:227], v[72:75]
	v_mfma_f32_16x16x32_bf16 v[124:127], v[146:149], v[178:181], v[124:127]
	v_mfma_f32_16x16x32_bf16 v[120:123], v[154:157], v[178:181], v[120:123]
	v_mfma_f32_16x16x32_bf16 v[116:119], v[146:149], v[198:201], v[116:119]
	v_mfma_f32_16x16x32_bf16 v[104:107], v[154:157], v[198:201], v[104:107]
	v_mfma_f32_16x16x32_bf16 v[100:103], v[146:149], v[206:209], v[100:103]
	v_mfma_f32_16x16x32_bf16 v[88:91], v[154:157], v[206:209], v[88:91]
	v_mfma_f32_16x16x32_bf16 v[84:87], v[146:149], v[228:231], v[84:87]
	v_mfma_f32_16x16x32_bf16 v[72:75], v[154:157], v[228:231], v[72:75]
	s_setprio 0
	s_setprio 1
	v_mfma_f32_16x16x32_bf16 v[112:115], v[158:161], v[174:177], v[112:115]
	v_mfma_f32_16x16x32_bf16 v[108:111], v[166:169], v[174:177], v[108:111]
	v_mfma_f32_16x16x32_bf16 v[96:99], v[158:161], v[194:197], v[96:99]
	v_mfma_f32_16x16x32_bf16 v[92:95], v[166:169], v[194:197], v[92:95]
	v_mfma_f32_16x16x32_bf16 v[80:83], v[158:161], v[202:205], v[80:83]
	v_mfma_f32_16x16x32_bf16 v[76:79], v[166:169], v[202:205], v[76:79]
	v_mfma_f32_16x16x32_bf16 v[68:71], v[158:161], v[224:227], v[68:71]
	v_mfma_f32_16x16x32_bf16 v[64:67], v[166:169], v[224:227], v[64:67]
	v_mfma_f32_16x16x32_bf16 v[112:115], v[162:165], v[178:181], v[112:115]
	v_mfma_f32_16x16x32_bf16 v[108:111], v[170:173], v[178:181], v[108:111]
	v_mfma_f32_16x16x32_bf16 v[96:99], v[162:165], v[198:201], v[96:99]
	v_mfma_f32_16x16x32_bf16 v[92:95], v[170:173], v[198:201], v[92:95]
	v_mfma_f32_16x16x32_bf16 v[80:83], v[162:165], v[206:209], v[80:83]
	v_mfma_f32_16x16x32_bf16 v[76:79], v[170:173], v[206:209], v[76:79]
	v_mfma_f32_16x16x32_bf16 v[68:71], v[162:165], v[228:231], v[68:71]
	v_mfma_f32_16x16x32_bf16 v[64:67], v[170:173], v[228:231], v[64:67]
	s_setprio 0
	s_barrier
	s_add_i32 s28, s38, s20
	v_lshl_add_u64 v[182:183], v[182:183], 0, s[68:69]
	s_mov_b32 m0, s28
	ds_read_b128 v[174:177], v145 offset:49152
	ds_read_b128 v[178:181], v145 offset:50176
	ds_read_b128 v[194:197], v145 offset:51200
	ds_read_b128 v[198:201], v145 offset:52224
	ds_read_b128 v[202:205], v145 offset:53248
	ds_read_b128 v[206:209], v145 offset:54272
	ds_read_b128 v[224:227], v145 offset:55296
	ds_read_b128 v[228:231], v145 offset:56320
	global_load_lds_dwordx4 v[182:183], off
	s_add_i32 m0, s28, 0x2000
	s_add_u32 s28, s40, 0x80080
	v_lshl_add_u64 v[182:183], v[210:211], 0, s[68:69]
	s_addc_u32 s29, s41, 0
	s_add_i32 s38, s39, s20
	global_load_lds_dwordx4 v[182:183], off
	v_lshl_add_u64 v[182:183], s[28:29], 0, v[184:185]
	s_mov_b32 m0, s38
	s_nop 0
	global_load_lds_dwordx4 v[182:183], off
	v_lshl_add_u64 v[182:183], s[28:29], 0, v[128:129]
	s_add_i32 m0, s38, 0x2000
	s_nop 0
	global_load_lds_dwordx4 v[182:183], off
	v_lshl_add_u64 v[182:183], v[216:217], 0, s[68:69]
	s_mov_b32 m0, s51
	s_nop 0
	global_load_lds_dwordx4 v[182:183], off
	v_lshl_add_u64 v[182:183], v[218:219], 0, s[68:69]
	s_waitcnt vmcnt(7)
	s_waitcnt lgkmcnt(0)
	s_barrier
	s_setprio 1
	s_waitcnt lgkmcnt(0)
	v_mfma_f32_16x16x32_bf16 v[60:63], v[138:141], v[174:177], v[60:63]
	v_mfma_f32_16x16x32_bf16 v[56:59], v[150:153], v[174:177], v[56:59]
	s_mov_b32 m0, s52
	s_nop 0
	global_load_lds_dwordx4 v[182:183], off
	v_mfma_f32_16x16x32_bf16 v[52:55], v[138:141], v[194:197], v[52:55]
	v_mfma_f32_16x16x32_bf16 v[40:43], v[150:153], v[194:197], v[40:43]
	v_mfma_f32_16x16x32_bf16 v[36:39], v[138:141], v[202:205], v[36:39]
	v_mfma_f32_16x16x32_bf16 v[24:27], v[150:153], v[202:205], v[24:27]
	v_mfma_f32_16x16x32_bf16 v[20:23], v[138:141], v[224:227], v[20:23]
	v_mfma_f32_16x16x32_bf16 v[8:11], v[150:153], v[224:227], v[8:11]
	v_mfma_f32_16x16x32_bf16 v[60:63], v[146:149], v[178:181], v[60:63]
	v_mfma_f32_16x16x32_bf16 v[56:59], v[154:157], v[178:181], v[56:59]
	v_mfma_f32_16x16x32_bf16 v[52:55], v[146:149], v[198:201], v[52:55]
	v_mfma_f32_16x16x32_bf16 v[40:43], v[154:157], v[198:201], v[40:43]
	v_mfma_f32_16x16x32_bf16 v[36:39], v[146:149], v[206:209], v[36:39]
	v_mfma_f32_16x16x32_bf16 v[24:27], v[154:157], v[206:209], v[24:27]
	v_mfma_f32_16x16x32_bf16 v[20:23], v[146:149], v[228:231], v[20:23]
	v_mfma_f32_16x16x32_bf16 v[8:11], v[154:157], v[228:231], v[8:11]
	s_setprio 0
	s_setprio 1
	v_mfma_f32_16x16x32_bf16 v[48:51], v[158:161], v[174:177], v[48:51]
	v_mfma_f32_16x16x32_bf16 v[44:47], v[166:169], v[174:177], v[44:47]
	v_mfma_f32_16x16x32_bf16 v[32:35], v[158:161], v[194:197], v[32:35]
	v_mfma_f32_16x16x32_bf16 v[28:31], v[166:169], v[194:197], v[28:31]
	v_mfma_f32_16x16x32_bf16 v[16:19], v[158:161], v[202:205], v[16:19]
	v_mfma_f32_16x16x32_bf16 v[12:15], v[166:169], v[202:205], v[12:15]
	v_mfma_f32_16x16x32_bf16 v[4:7], v[158:161], v[224:227], v[4:7]
	v_mfma_f32_16x16x32_bf16 v[0:3], v[166:169], v[224:227], v[0:3]
	v_mfma_f32_16x16x32_bf16 v[48:51], v[162:165], v[178:181], v[48:51]
	v_mfma_f32_16x16x32_bf16 v[44:47], v[170:173], v[178:181], v[44:47]
	v_mfma_f32_16x16x32_bf16 v[32:35], v[162:165], v[198:201], v[32:35]
	v_mfma_f32_16x16x32_bf16 v[28:31], v[170:173], v[198:201], v[28:31]
	v_mfma_f32_16x16x32_bf16 v[16:19], v[162:165], v[206:209], v[16:19]
	v_mfma_f32_16x16x32_bf16 v[12:15], v[170:173], v[206:209], v[12:15]
	v_mfma_f32_16x16x32_bf16 v[4:7], v[162:165], v[228:231], v[4:7]
	v_mfma_f32_16x16x32_bf16 v[0:3], v[170:173], v[228:231], v[0:3]
	s_setprio 0
	s_barrier
	s_add_i32 s78, s78, 2
	s_add_u32 s30, s30, 0x100
	s_addc_u32 s31, s31, 0
	s_add_u32 s62, s62, 0x100
	s_addc_u32 s63, s63, 0
	s_cmp_gt_u32 s78, 29
	s_cbranch_scc0 .LBB0_805
	s_and_b64 vcc, exec, s[6:7]
	s_cbranch_vccz .LBB0_808
	s_barrier

.LBB0_842:
	s_add_u32 s28, s30, 0xfffc0080
	s_addc_u32 s29, s31, -1
	s_add_i32 s42, 0, 0x10000
	s_cmp_eq_u32 s60, 12
	s_cselect_b32 s45, s9, s29
	s_cselect_b32 s44, s11, s28
	s_cselect_b32 s41, s36, s59
	s_cselect_b32 s40, s37, s58
	s_add_i32 s43, 0, 0x14000
	v_add_u32_e32 v154, s42, v147
	v_add_u32_e32 v170, s43, v147
	ds_read_b128 v[138:141], v154
	ds_read_b128 v[142:145], v154 offset:1024
	ds_read_b128 v[150:153], v154 offset:2048
	ds_read_b128 v[154:157], v154 offset:3072
	ds_read_b128 v[158:161], v170
	ds_read_b128 v[162:165], v170 offset:1024
	ds_read_b128 v[166:169], v170 offset:2048
	ds_read_b128 v[170:173], v170 offset:3072
	v_lshl_add_u64 v[182:183], s[30:31], 0, v[134:135]
	s_add_i32 m0, s21, 0xc000
	ds_read_b128 v[174:177], v149
	ds_read_b128 v[178:181], v149 offset:1024
	ds_read_b128 v[194:197], v149 offset:2048
	ds_read_b128 v[198:201], v149 offset:3072
	ds_read_b128 v[202:205], v149 offset:4096
	ds_read_b128 v[206:209], v149 offset:5120
	ds_read_b128 v[224:227], v149 offset:6144
	ds_read_b128 v[228:231], v149 offset:7168
	global_load_lds_dwordx4 v[182:183], off
	v_lshl_add_u64 v[182:183], s[30:31], 0, v[136:137]
	s_waitcnt vmcnt(7)
	s_waitcnt lgkmcnt(0)
	s_barrier
	s_setprio 1
	s_waitcnt lgkmcnt(0)
	v_mfma_f32_16x16x32_bf16 v[124:127], v[138:141], v[174:177], v[124:127]
	v_mfma_f32_16x16x32_bf16 v[120:123], v[150:153], v[174:177], v[120:123]
	s_add_i32 m0, s21, 0xe000
	s_nop 0
	global_load_lds_dwordx4 v[182:183], off
	v_mfma_f32_16x16x32_bf16 v[108:111], v[138:141], v[194:197], v[108:111]
	v_mfma_f32_16x16x32_bf16 v[104:107], v[150:153], v[194:197], v[104:107]
	v_mfma_f32_16x16x32_bf16 v[92:95], v[138:141], v[202:205], v[92:95]
	v_mfma_f32_16x16x32_bf16 v[88:91], v[150:153], v[202:205], v[88:91]
	v_mfma_f32_16x16x32_bf16 v[76:79], v[138:141], v[224:227], v[76:79]
	v_mfma_f32_16x16x32_bf16 v[72:75], v[150:153], v[224:227], v[72:75]
	v_mfma_f32_16x16x32_bf16 v[124:127], v[142:145], v[178:181], v[124:127]
	v_mfma_f32_16x16x32_bf16 v[120:123], v[154:157], v[178:181], v[120:123]
	v_mfma_f32_16x16x32_bf16 v[108:111], v[142:145], v[198:201], v[108:111]
	v_mfma_f32_16x16x32_bf16 v[104:107], v[154:157], v[198:201], v[104:107]
	v_mfma_f32_16x16x32_bf16 v[92:95], v[142:145], v[206:209], v[92:95]
	v_mfma_f32_16x16x32_bf16 v[88:91], v[154:157], v[206:209], v[88:91]
	v_mfma_f32_16x16x32_bf16 v[76:79], v[142:145], v[228:231], v[76:79]
	v_mfma_f32_16x16x32_bf16 v[72:75], v[154:157], v[228:231], v[72:75]
	s_setprio 0
	s_setprio 1
	v_mfma_f32_16x16x32_bf16 v[116:119], v[158:161], v[174:177], v[116:119]
	v_mfma_f32_16x16x32_bf16 v[112:115], v[166:169], v[174:177], v[112:115]
	v_mfma_f32_16x16x32_bf16 v[100:103], v[158:161], v[194:197], v[100:103]
	v_mfma_f32_16x16x32_bf16 v[96:99], v[166:169], v[194:197], v[96:99]
	v_mfma_f32_16x16x32_bf16 v[84:87], v[158:161], v[202:205], v[84:87]
	v_mfma_f32_16x16x32_bf16 v[80:83], v[166:169], v[202:205], v[80:83]
	v_mfma_f32_16x16x32_bf16 v[68:71], v[158:161], v[224:227], v[68:71]
	v_mfma_f32_16x16x32_bf16 v[64:67], v[166:169], v[224:227], v[64:67]
	v_mfma_f32_16x16x32_bf16 v[116:119], v[162:165], v[178:181], v[116:119]
	v_mfma_f32_16x16x32_bf16 v[112:115], v[170:173], v[178:181], v[112:115]
	v_mfma_f32_16x16x32_bf16 v[100:103], v[162:165], v[198:201], v[100:103]
	v_mfma_f32_16x16x32_bf16 v[96:99], v[170:173], v[198:201], v[96:99]
	v_mfma_f32_16x16x32_bf16 v[84:87], v[162:165], v[206:209], v[84:87]
	v_mfma_f32_16x16x32_bf16 v[80:83], v[170:173], v[206:209], v[80:83]
	v_mfma_f32_16x16x32_bf16 v[68:71], v[162:165], v[228:231], v[68:71]
	v_mfma_f32_16x16x32_bf16 v[64:67], v[170:173], v[228:231], v[64:67]
	s_setprio 0
	s_barrier
	s_add_i32 s28, s42, s20
	v_lshl_add_u64 v[182:183], s[40:41], 0, v[184:185]
	s_mov_b32 m0, s28
	ds_read_b128 v[174:177], v149 offset:16384
	ds_read_b128 v[178:181], v149 offset:17408
	ds_read_b128 v[194:197], v149 offset:18432
	ds_read_b128 v[198:201], v149 offset:19456
	ds_read_b128 v[202:205], v149 offset:20480
	ds_read_b128 v[206:209], v149 offset:21504
	ds_read_b128 v[224:227], v149 offset:22528
	ds_read_b128 v[228:231], v149 offset:23552
	global_load_lds_dwordx4 v[182:183], off
	s_add_i32 m0, s28, 0x2000
	s_add_u32 s28, s40, 0x40000
	v_lshl_add_u64 v[210:211], s[40:41], 0, v[128:129]
	s_addc_u32 s29, s41, 0
	s_add_i32 s42, s43, s20
	global_load_lds_dwordx4 v[210:211], off
	v_lshl_add_u64 v[216:217], s[28:29], 0, v[184:185]
	s_mov_b32 m0, s42
	v_lshl_add_u64 v[218:219], s[44:45], 0, v[130:131]
	global_load_lds_dwordx4 v[216:217], off
	v_lshl_add_u64 v[216:217], s[28:29], 0, v[128:129]
	s_add_i32 m0, s42, 0x2000
	s_nop 0
	global_load_lds_dwordx4 v[216:217], off
	v_lshl_add_u64 v[216:217], s[44:45], 0, v[132:133]
	s_mov_b32 m0, s21
	s_nop 0
	global_load_lds_dwordx4 v[216:217], off
	s_waitcnt vmcnt(7)
	s_waitcnt lgkmcnt(0)
	s_barrier
	s_setprio 1
	s_waitcnt lgkmcnt(0)
	v_mfma_f32_16x16x32_bf16 v[60:63], v[138:141], v[174:177], v[60:63]
	v_mfma_f32_16x16x32_bf16 v[56:59], v[150:153], v[174:177], v[56:59]
	s_mov_b32 m0, s26
	s_nop 0
	global_load_lds_dwordx4 v[218:219], off
	v_mfma_f32_16x16x32_bf16 v[44:47], v[138:141], v[194:197], v[44:47]
	v_mfma_f32_16x16x32_bf16 v[40:43], v[150:153], v[194:197], v[40:43]
	v_mfma_f32_16x16x32_bf16 v[28:31], v[138:141], v[202:205], v[28:31]
	v_mfma_f32_16x16x32_bf16 v[24:27], v[150:153], v[202:205], v[24:27]
	v_mfma_f32_16x16x32_bf16 v[12:15], v[138:141], v[224:227], v[12:15]
	v_mfma_f32_16x16x32_bf16 v[8:11], v[150:153], v[224:227], v[8:11]
	v_mfma_f32_16x16x32_bf16 v[60:63], v[142:145], v[178:181], v[60:63]
	v_mfma_f32_16x16x32_bf16 v[56:59], v[154:157], v[178:181], v[56:59]
	v_mfma_f32_16x16x32_bf16 v[44:47], v[142:145], v[198:201], v[44:47]
	v_mfma_f32_16x16x32_bf16 v[40:43], v[154:157], v[198:201], v[40:43]
	v_mfma_f32_16x16x32_bf16 v[28:31], v[142:145], v[206:209], v[28:31]
	v_mfma_f32_16x16x32_bf16 v[24:27], v[154:157], v[206:209], v[24:27]
	v_mfma_f32_16x16x32_bf16 v[12:15], v[142:145], v[228:231], v[12:15]
	v_mfma_f32_16x16x32_bf16 v[8:11], v[154:157], v[228:231], v[8:11]
	s_setprio 0
	s_setprio 1
	v_mfma_f32_16x16x32_bf16 v[52:55], v[158:161], v[174:177], v[52:55]
	v_mfma_f32_16x16x32_bf16 v[48:51], v[166:169], v[174:177], v[48:51]
	v_mfma_f32_16x16x32_bf16 v[36:39], v[158:161], v[194:197], v[36:39]
	v_mfma_f32_16x16x32_bf16 v[32:35], v[166:169], v[194:197], v[32:35]
	v_mfma_f32_16x16x32_bf16 v[20:23], v[158:161], v[202:205], v[20:23]
	v_mfma_f32_16x16x32_bf16 v[16:19], v[166:169], v[202:205], v[16:19]
	v_mfma_f32_16x16x32_bf16 v[4:7], v[158:161], v[224:227], v[4:7]
	v_mfma_f32_16x16x32_bf16 v[0:3], v[166:169], v[224:227], v[0:3]
	v_mfma_f32_16x16x32_bf16 v[52:55], v[162:165], v[178:181], v[52:55]
	v_mfma_f32_16x16x32_bf16 v[48:51], v[170:173], v[178:181], v[48:51]
	v_mfma_f32_16x16x32_bf16 v[36:39], v[162:165], v[198:201], v[36:39]
	v_mfma_f32_16x16x32_bf16 v[32:35], v[170:173], v[198:201], v[32:35]
	v_mfma_f32_16x16x32_bf16 v[20:23], v[162:165], v[206:209], v[20:23]
	v_mfma_f32_16x16x32_bf16 v[16:19], v[170:173], v[206:209], v[16:19]
	v_mfma_f32_16x16x32_bf16 v[4:7], v[162:165], v[228:231], v[4:7]
	v_mfma_f32_16x16x32_bf16 v[0:3], v[170:173], v[228:231], v[0:3]
	s_setprio 0
	s_barrier
	s_add_i32 s42, 0, 0x18000
	s_add_i32 s43, 0, 0x1c000
	v_add_u32_e32 v154, s42, v147
	v_add_u32_e32 v170, s43, v147
	ds_read_b128 v[138:141], v154
	ds_read_b128 v[142:145], v154 offset:1024
	ds_read_b128 v[150:153], v154 offset:2048
	ds_read_b128 v[154:157], v154 offset:3072
	ds_read_b128 v[158:161], v170
	ds_read_b128 v[162:165], v170 offset:1024
	ds_read_b128 v[166:169], v170 offset:2048
	ds_read_b128 v[170:173], v170 offset:3072
	s_add_u32 s28, s44, 0x40000
	s_addc_u32 s29, s45, 0
	s_mov_b32 m0, s27
	v_lshl_add_u64 v[232:233], s[28:29], 0, v[132:133]
	ds_read_b128 v[174:177], v149 offset:32768
	ds_read_b128 v[178:181], v149 offset:33792
	ds_read_b128 v[194:197], v149 offset:34816
	ds_read_b128 v[198:201], v149 offset:35840
	ds_read_b128 v[202:205], v149 offset:36864
	ds_read_b128 v[206:209], v149 offset:37888
	ds_read_b128 v[224:227], v149 offset:38912
	ds_read_b128 v[228:231], v149 offset:39936
	global_load_lds_dwordx4 v[232:233], off
	v_lshl_add_u64 v[232:233], s[28:29], 0, v[130:131]
	s_waitcnt vmcnt(7)
	s_waitcnt lgkmcnt(0)
	s_barrier
	s_setprio 1
	s_waitcnt lgkmcnt(0)
	v_mfma_f32_16x16x32_bf16 v[124:127], v[138:141], v[174:177], v[124:127]
	v_mfma_f32_16x16x32_bf16 v[120:123], v[150:153], v[174:177], v[120:123]
	s_mov_b32 m0, s46
	s_nop 0
	global_load_lds_dwordx4 v[232:233], off
	v_mfma_f32_16x16x32_bf16 v[108:111], v[138:141], v[194:197], v[108:111]
	v_mfma_f32_16x16x32_bf16 v[104:107], v[150:153], v[194:197], v[104:107]
	v_mfma_f32_16x16x32_bf16 v[92:95], v[138:141], v[202:205], v[92:95]
	v_mfma_f32_16x16x32_bf16 v[88:91], v[150:153], v[202:205], v[88:91]
	v_mfma_f32_16x16x32_bf16 v[76:79], v[138:141], v[224:227], v[76:79]
	v_mfma_f32_16x16x32_bf16 v[72:75], v[150:153], v[224:227], v[72:75]
	v_mfma_f32_16x16x32_bf16 v[124:127], v[142:145], v[178:181], v[124:127]
	v_mfma_f32_16x16x32_bf16 v[120:123], v[154:157], v[178:181], v[120:123]
	v_mfma_f32_16x16x32_bf16 v[108:111], v[142:145], v[198:201], v[108:111]
	v_mfma_f32_16x16x32_bf16 v[104:107], v[154:157], v[198:201], v[104:107]
	v_mfma_f32_16x16x32_bf16 v[92:95], v[142:145], v[206:209], v[92:95]
	v_mfma_f32_16x16x32_bf16 v[88:91], v[154:157], v[206:209], v[88:91]
	v_mfma_f32_16x16x32_bf16 v[76:79], v[142:145], v[228:231], v[76:79]
	v_mfma_f32_16x16x32_bf16 v[72:75], v[154:157], v[228:231], v[72:75]
	s_setprio 0
	s_setprio 1
	v_mfma_f32_16x16x32_bf16 v[116:119], v[158:161], v[174:177], v[116:119]
	v_mfma_f32_16x16x32_bf16 v[112:115], v[166:169], v[174:177], v[112:115]
	v_mfma_f32_16x16x32_bf16 v[100:103], v[158:161], v[194:197], v[100:103]
	v_mfma_f32_16x16x32_bf16 v[96:99], v[166:169], v[194:197], v[96:99]
	v_mfma_f32_16x16x32_bf16 v[84:87], v[158:161], v[202:205], v[84:87]
	v_mfma_f32_16x16x32_bf16 v[80:83], v[166:169], v[202:205], v[80:83]
	v_mfma_f32_16x16x32_bf16 v[68:71], v[158:161], v[224:227], v[68:71]
	v_mfma_f32_16x16x32_bf16 v[64:67], v[166:169], v[224:227], v[64:67]
	v_mfma_f32_16x16x32_bf16 v[116:119], v[162:165], v[178:181], v[116:119]
	v_mfma_f32_16x16x32_bf16 v[112:115], v[170:173], v[178:181], v[112:115]
	v_mfma_f32_16x16x32_bf16 v[100:103], v[162:165], v[198:201], v[100:103]
	v_mfma_f32_16x16x32_bf16 v[96:99], v[170:173], v[198:201], v[96:99]
	v_mfma_f32_16x16x32_bf16 v[84:87], v[162:165], v[206:209], v[84:87]
	v_mfma_f32_16x16x32_bf16 v[80:83], v[170:173], v[206:209], v[80:83]
	v_mfma_f32_16x16x32_bf16 v[68:71], v[162:165], v[228:231], v[68:71]
	v_mfma_f32_16x16x32_bf16 v[64:67], v[170:173], v[228:231], v[64:67]
	s_setprio 0
	s_barrier
	s_add_i32 s28, s42, s20
	v_lshl_add_u64 v[182:183], v[182:183], 0, s[68:69]
	s_mov_b32 m0, s28
	ds_read_b128 v[174:177], v149 offset:49152
	ds_read_b128 v[178:181], v149 offset:50176
	ds_read_b128 v[194:197], v149 offset:51200
	ds_read_b128 v[198:201], v149 offset:52224
	ds_read_b128 v[202:205], v149 offset:53248
	ds_read_b128 v[206:209], v149 offset:54272
	ds_read_b128 v[224:227], v149 offset:55296
	ds_read_b128 v[228:231], v149 offset:56320
	global_load_lds_dwordx4 v[182:183], off
	s_add_i32 m0, s28, 0x2000
	s_add_u32 s28, s40, 0x40080
	v_lshl_add_u64 v[182:183], v[210:211], 0, s[68:69]
	s_addc_u32 s29, s41, 0
	s_add_i32 s40, s43, s20
	global_load_lds_dwordx4 v[182:183], off
	v_lshl_add_u64 v[182:183], s[28:29], 0, v[184:185]
	s_mov_b32 m0, s40
	s_nop 0
	global_load_lds_dwordx4 v[182:183], off
	v_lshl_add_u64 v[182:183], s[28:29], 0, v[128:129]
	s_add_i32 m0, s40, 0x2000
	s_nop 0
	global_load_lds_dwordx4 v[182:183], off
	v_lshl_add_u64 v[182:183], v[216:217], 0, s[68:69]
	s_mov_b32 m0, s47
	s_nop 0
	global_load_lds_dwordx4 v[182:183], off
	v_lshl_add_u64 v[182:183], v[218:219], 0, s[68:69]
	s_waitcnt vmcnt(7)
	s_waitcnt lgkmcnt(0)
	s_barrier
	s_setprio 1
	s_waitcnt lgkmcnt(0)
	v_mfma_f32_16x16x32_bf16 v[60:63], v[138:141], v[174:177], v[60:63]
	v_mfma_f32_16x16x32_bf16 v[56:59], v[150:153], v[174:177], v[56:59]
	s_mov_b32 m0, s50
	s_nop 0
	global_load_lds_dwordx4 v[182:183], off
	v_mfma_f32_16x16x32_bf16 v[44:47], v[138:141], v[194:197], v[44:47]
	v_mfma_f32_16x16x32_bf16 v[40:43], v[150:153], v[194:197], v[40:43]
	v_mfma_f32_16x16x32_bf16 v[28:31], v[138:141], v[202:205], v[28:31]
	v_mfma_f32_16x16x32_bf16 v[24:27], v[150:153], v[202:205], v[24:27]
	v_mfma_f32_16x16x32_bf16 v[12:15], v[138:141], v[224:227], v[12:15]
	v_mfma_f32_16x16x32_bf16 v[8:11], v[150:153], v[224:227], v[8:11]
	v_mfma_f32_16x16x32_bf16 v[60:63], v[142:145], v[178:181], v[60:63]
	v_mfma_f32_16x16x32_bf16 v[56:59], v[154:157], v[178:181], v[56:59]
	v_mfma_f32_16x16x32_bf16 v[44:47], v[142:145], v[198:201], v[44:47]
	v_mfma_f32_16x16x32_bf16 v[40:43], v[154:157], v[198:201], v[40:43]
	v_mfma_f32_16x16x32_bf16 v[28:31], v[142:145], v[206:209], v[28:31]
	v_mfma_f32_16x16x32_bf16 v[24:27], v[154:157], v[206:209], v[24:27]
	v_mfma_f32_16x16x32_bf16 v[12:15], v[142:145], v[228:231], v[12:15]
	v_mfma_f32_16x16x32_bf16 v[8:11], v[154:157], v[228:231], v[8:11]
	s_setprio 0
	s_setprio 1
	v_mfma_f32_16x16x32_bf16 v[52:55], v[158:161], v[174:177], v[52:55]
	v_mfma_f32_16x16x32_bf16 v[48:51], v[166:169], v[174:177], v[48:51]
	v_mfma_f32_16x16x32_bf16 v[36:39], v[158:161], v[194:197], v[36:39]
	v_mfma_f32_16x16x32_bf16 v[32:35], v[166:169], v[194:197], v[32:35]
	v_mfma_f32_16x16x32_bf16 v[20:23], v[158:161], v[202:205], v[20:23]
	v_mfma_f32_16x16x32_bf16 v[16:19], v[166:169], v[202:205], v[16:19]
	v_mfma_f32_16x16x32_bf16 v[4:7], v[158:161], v[224:227], v[4:7]
	v_mfma_f32_16x16x32_bf16 v[0:3], v[166:169], v[224:227], v[0:3]
	v_mfma_f32_16x16x32_bf16 v[52:55], v[162:165], v[178:181], v[52:55]
	v_mfma_f32_16x16x32_bf16 v[48:51], v[170:173], v[178:181], v[48:51]
	v_mfma_f32_16x16x32_bf16 v[36:39], v[162:165], v[198:201], v[36:39]
	v_mfma_f32_16x16x32_bf16 v[32:35], v[170:173], v[198:201], v[32:35]
	v_mfma_f32_16x16x32_bf16 v[20:23], v[162:165], v[206:209], v[20:23]
	v_mfma_f32_16x16x32_bf16 v[16:19], v[170:173], v[206:209], v[16:19]
	v_mfma_f32_16x16x32_bf16 v[4:7], v[162:165], v[228:231], v[4:7]
	v_mfma_f32_16x16x32_bf16 v[0:3], v[170:173], v[228:231], v[0:3]
	s_setprio 0
	s_barrier
	s_add_i32 s60, s60, 2
	s_add_u32 s30, s30, 0x100
	s_addc_u32 s31, s31, 0
	s_add_u32 s58, s58, 0x100
	s_addc_u32 s59, s59, 0
	s_cmp_gt_u32 s60, 13
	s_cbranch_scc0 .LBB0_842
	s_and_b64 vcc, exec, s[6:7]
	s_cbranch_vccz .LBB0_845
	s_barrier

.LBB0_991:
	s_add_u32 s28, s40, 0xfff80080
	s_addc_u32 s29, s41, -1
	s_add_i32 s48, 0, 0x10000
	s_cmp_eq_u32 s79, 28
	s_cselect_b32 s45, s11, s29
	s_cselect_b32 s44, s13, s28
	s_cselect_b32 s43, s60, s63
	s_cselect_b32 s42, s61, s62
	s_add_i32 s49, 0, 0x14000
	s_waitcnt vmcnt(0)
	v_add_u32_e32 v60, s48, v169
	v_add_u32_e32 v166, s49, v169
	ds_read_b128 v[40:43], v60
	ds_read_b128 v[44:47], v60 offset:1024
	ds_read_b128 v[56:59], v60 offset:2048
	ds_read_b128 v[60:63], v60 offset:3072
	ds_read_b128 v[144:147], v166
	ds_read_b128 v[148:151], v166 offset:1024
	ds_read_b128 v[162:165], v166 offset:2048
	ds_read_b128 v[172:175], v166 offset:3072
	v_lshl_add_u64 v[166:167], s[40:41], 0, v[158:159]
	s_add_i32 m0, s26, 0xc000
	ds_read_b128 v[176:179], v171
	ds_read_b128 v[180:183], v171 offset:1024
	ds_read_b128 v[194:197], v171 offset:2048
	ds_read_b128 v[198:201], v171 offset:3072
	ds_read_b128 v[202:205], v171 offset:4096
	ds_read_b128 v[206:209], v171 offset:5120
	ds_read_b128 v[224:227], v171 offset:6144
	ds_read_b128 v[228:231], v171 offset:7168
	global_load_lds_dwordx4 v[166:167], off
	v_lshl_add_u64 v[166:167], s[40:41], 0, v[160:161]
	s_waitcnt vmcnt(7)
	s_waitcnt lgkmcnt(0)
	s_barrier
	s_setprio 1
	s_waitcnt lgkmcnt(0)
	v_mfma_f32_16x16x32_bf16 v[140:143], v[40:43], v[176:179], v[140:143]
	v_mfma_f32_16x16x32_bf16 v[136:139], v[56:59], v[176:179], v[136:139]
	s_add_i32 m0, s26, 0xe000
	s_nop 0
	global_load_lds_dwordx4 v[166:167], off
	v_mfma_f32_16x16x32_bf16 v[124:127], v[40:43], v[194:197], v[124:127]
	v_mfma_f32_16x16x32_bf16 v[120:123], v[56:59], v[194:197], v[120:123]
	v_mfma_f32_16x16x32_bf16 v[108:111], v[40:43], v[202:205], v[108:111]
	v_mfma_f32_16x16x32_bf16 v[104:107], v[56:59], v[202:205], v[104:107]
	v_mfma_f32_16x16x32_bf16 v[92:95], v[40:43], v[224:227], v[92:95]
	v_mfma_f32_16x16x32_bf16 v[88:91], v[56:59], v[224:227], v[88:91]
	v_mfma_f32_16x16x32_bf16 v[140:143], v[44:47], v[180:183], v[140:143]
	v_mfma_f32_16x16x32_bf16 v[136:139], v[60:63], v[180:183], v[136:139]
	v_mfma_f32_16x16x32_bf16 v[124:127], v[44:47], v[198:201], v[124:127]
	v_mfma_f32_16x16x32_bf16 v[120:123], v[60:63], v[198:201], v[120:123]
	v_mfma_f32_16x16x32_bf16 v[108:111], v[44:47], v[206:209], v[108:111]
	v_mfma_f32_16x16x32_bf16 v[104:107], v[60:63], v[206:209], v[104:107]
	v_mfma_f32_16x16x32_bf16 v[92:95], v[44:47], v[228:231], v[92:95]
	v_mfma_f32_16x16x32_bf16 v[88:91], v[60:63], v[228:231], v[88:91]
	s_setprio 0
	s_setprio 1
	v_mfma_f32_16x16x32_bf16 v[132:135], v[144:147], v[176:179], v[132:135]
	v_mfma_f32_16x16x32_bf16 v[128:131], v[162:165], v[176:179], v[128:131]
	v_mfma_f32_16x16x32_bf16 v[116:119], v[144:147], v[194:197], v[116:119]
	v_mfma_f32_16x16x32_bf16 v[112:115], v[162:165], v[194:197], v[112:115]
	v_mfma_f32_16x16x32_bf16 v[100:103], v[144:147], v[202:205], v[100:103]
	v_mfma_f32_16x16x32_bf16 v[96:99], v[162:165], v[202:205], v[96:99]
	v_mfma_f32_16x16x32_bf16 v[84:87], v[144:147], v[224:227], v[84:87]
	v_mfma_f32_16x16x32_bf16 v[80:83], v[162:165], v[224:227], v[80:83]
	v_mfma_f32_16x16x32_bf16 v[132:135], v[148:151], v[180:183], v[132:135]
	v_mfma_f32_16x16x32_bf16 v[128:131], v[172:175], v[180:183], v[128:131]
	v_mfma_f32_16x16x32_bf16 v[116:119], v[148:151], v[198:201], v[116:119]
	v_mfma_f32_16x16x32_bf16 v[112:115], v[172:175], v[198:201], v[112:115]
	v_mfma_f32_16x16x32_bf16 v[100:103], v[148:151], v[206:209], v[100:103]
	v_mfma_f32_16x16x32_bf16 v[96:99], v[172:175], v[206:209], v[96:99]
	v_mfma_f32_16x16x32_bf16 v[84:87], v[148:151], v[228:231], v[84:87]
	v_mfma_f32_16x16x32_bf16 v[80:83], v[172:175], v[228:231], v[80:83]
	s_setprio 0
	s_barrier
	s_add_i32 s28, s48, s46
	v_lshl_add_u64 v[166:167], s[42:43], 0, v[184:185]
	s_mov_b32 m0, s28
	ds_read_b128 v[176:179], v171 offset:16384
	ds_read_b128 v[180:183], v171 offset:17408
	ds_read_b128 v[194:197], v171 offset:18432
	ds_read_b128 v[198:201], v171 offset:19456
	ds_read_b128 v[202:205], v171 offset:20480
	ds_read_b128 v[206:209], v171 offset:21504
	ds_read_b128 v[224:227], v171 offset:22528
	ds_read_b128 v[228:231], v171 offset:23552
	global_load_lds_dwordx4 v[166:167], off
	s_add_i32 m0, s28, 0x2000
	s_add_u32 s28, s42, 0x80000
	v_lshl_add_u64 v[210:211], s[42:43], 0, v[152:153]
	s_addc_u32 s29, s43, 0
	s_add_i32 s48, s49, s46
	global_load_lds_dwordx4 v[210:211], off
	v_lshl_add_u64 v[216:217], s[28:29], 0, v[184:185]
	s_mov_b32 m0, s48
	v_lshl_add_u64 v[218:219], s[44:45], 0, v[154:155]
	global_load_lds_dwordx4 v[216:217], off
	v_lshl_add_u64 v[216:217], s[28:29], 0, v[152:153]
	s_add_i32 m0, s48, 0x2000
	s_nop 0
	global_load_lds_dwordx4 v[216:217], off
	v_lshl_add_u64 v[216:217], s[44:45], 0, v[156:157]
	s_mov_b32 m0, s26
	s_nop 0
	global_load_lds_dwordx4 v[216:217], off
	s_waitcnt vmcnt(7)
	s_waitcnt lgkmcnt(0)
	s_barrier
	s_setprio 1
	s_waitcnt lgkmcnt(0)
	v_mfma_f32_16x16x32_bf16 v[76:79], v[40:43], v[176:179], v[76:79]
	v_mfma_f32_16x16x32_bf16 v[72:75], v[56:59], v[176:179], v[72:75]
	s_mov_b32 m0, s27
	s_nop 0
	global_load_lds_dwordx4 v[218:219], off
	v_mfma_f32_16x16x32_bf16 v[52:55], v[40:43], v[194:197], v[52:55]
	v_mfma_f32_16x16x32_bf16 v[48:51], v[56:59], v[194:197], v[48:51]
	v_mfma_f32_16x16x32_bf16 v[28:31], v[40:43], v[202:205], v[28:31]
	v_mfma_f32_16x16x32_bf16 v[24:27], v[56:59], v[202:205], v[24:27]
	v_mfma_f32_16x16x32_bf16 v[12:15], v[40:43], v[224:227], v[12:15]
	v_mfma_f32_16x16x32_bf16 v[8:11], v[56:59], v[224:227], v[8:11]
	v_mfma_f32_16x16x32_bf16 v[76:79], v[44:47], v[180:183], v[76:79]
	v_mfma_f32_16x16x32_bf16 v[72:75], v[60:63], v[180:183], v[72:75]
	v_mfma_f32_16x16x32_bf16 v[52:55], v[44:47], v[198:201], v[52:55]
	v_mfma_f32_16x16x32_bf16 v[48:51], v[60:63], v[198:201], v[48:51]
	v_mfma_f32_16x16x32_bf16 v[28:31], v[44:47], v[206:209], v[28:31]
	v_mfma_f32_16x16x32_bf16 v[24:27], v[60:63], v[206:209], v[24:27]
	v_mfma_f32_16x16x32_bf16 v[12:15], v[44:47], v[228:231], v[12:15]
	v_mfma_f32_16x16x32_bf16 v[8:11], v[60:63], v[228:231], v[8:11]
	s_setprio 0
	s_setprio 1
	v_mfma_f32_16x16x32_bf16 v[36:39], v[144:147], v[194:197], v[36:39]
	v_mfma_f32_16x16x32_bf16 v[32:35], v[162:165], v[194:197], v[32:35]
	v_mfma_f32_16x16x32_bf16 v[20:23], v[144:147], v[202:205], v[20:23]
	v_mfma_f32_16x16x32_bf16 v[16:19], v[162:165], v[202:205], v[16:19]
	v_mfma_f32_16x16x32_bf16 v[4:7], v[144:147], v[224:227], v[4:7]
	v_mfma_f32_16x16x32_bf16 v[0:3], v[162:165], v[224:227], v[0:3]
	v_mfma_f32_16x16x32_bf16 v[40:43], v[144:147], v[176:179], v[68:71]
	v_mfma_f32_16x16x32_bf16 v[44:47], v[162:165], v[176:179], v[64:67]
	v_mfma_f32_16x16x32_bf16 v[36:39], v[148:151], v[198:201], v[36:39]
	v_mfma_f32_16x16x32_bf16 v[32:35], v[172:175], v[198:201], v[32:35]
	v_mfma_f32_16x16x32_bf16 v[20:23], v[148:151], v[206:209], v[20:23]
	v_mfma_f32_16x16x32_bf16 v[16:19], v[172:175], v[206:209], v[16:19]
	v_mfma_f32_16x16x32_bf16 v[4:7], v[148:151], v[228:231], v[4:7]
	v_mfma_f32_16x16x32_bf16 v[0:3], v[172:175], v[228:231], v[0:3]
	v_mfma_f32_16x16x32_bf16 v[40:43], v[148:151], v[180:183], v[40:43]
	v_mfma_f32_16x16x32_bf16 v[44:47], v[172:175], v[180:183], v[44:47]
	s_setprio 0
	s_barrier
	s_add_i32 s48, 0, 0x18000
	s_add_i32 s49, 0, 0x1c000
	v_add_u32_e32 v68, s48, v169
	v_add_u32_e32 v172, s49, v169
	ds_read_b128 v[56:59], v68
	ds_read_b128 v[60:63], v68 offset:1024
	ds_read_b128 v[64:67], v68 offset:2048
	ds_read_b128 v[68:71], v68 offset:3072
	ds_read_b128 v[144:147], v172
	ds_read_b128 v[148:151], v172 offset:1024
	ds_read_b128 v[162:165], v172 offset:2048
	ds_read_b128 v[172:175], v172 offset:3072
	s_add_u32 s28, s44, 0x80000
	s_addc_u32 s29, s45, 0
	s_mov_b32 m0, s47
	v_lshl_add_u64 v[232:233], s[28:29], 0, v[156:157]
	ds_read_b128 v[176:179], v171 offset:32768
	ds_read_b128 v[180:183], v171 offset:33792
	ds_read_b128 v[194:197], v171 offset:34816
	ds_read_b128 v[198:201], v171 offset:35840
	ds_read_b128 v[202:205], v171 offset:36864
	ds_read_b128 v[206:209], v171 offset:37888
	ds_read_b128 v[224:227], v171 offset:38912
	ds_read_b128 v[228:231], v171 offset:39936
	global_load_lds_dwordx4 v[232:233], off
	v_lshl_add_u64 v[232:233], s[28:29], 0, v[154:155]
	s_waitcnt vmcnt(7)
	s_waitcnt lgkmcnt(0)
	s_barrier
	s_setprio 1
	s_waitcnt lgkmcnt(0)
	v_mfma_f32_16x16x32_bf16 v[140:143], v[56:59], v[176:179], v[140:143]
	v_mfma_f32_16x16x32_bf16 v[136:139], v[64:67], v[176:179], v[136:139]
	s_mov_b32 m0, s50
	s_nop 0
	global_load_lds_dwordx4 v[232:233], off
	v_mfma_f32_16x16x32_bf16 v[124:127], v[56:59], v[194:197], v[124:127]
	v_mfma_f32_16x16x32_bf16 v[120:123], v[64:67], v[194:197], v[120:123]
	v_mfma_f32_16x16x32_bf16 v[108:111], v[56:59], v[202:205], v[108:111]
	v_mfma_f32_16x16x32_bf16 v[104:107], v[64:67], v[202:205], v[104:107]
	v_mfma_f32_16x16x32_bf16 v[92:95], v[56:59], v[224:227], v[92:95]
	v_mfma_f32_16x16x32_bf16 v[88:91], v[64:67], v[224:227], v[88:91]
	v_mfma_f32_16x16x32_bf16 v[140:143], v[60:63], v[180:183], v[140:143]
	v_mfma_f32_16x16x32_bf16 v[136:139], v[68:71], v[180:183], v[136:139]
	v_mfma_f32_16x16x32_bf16 v[124:127], v[60:63], v[198:201], v[124:127]
	v_mfma_f32_16x16x32_bf16 v[120:123], v[68:71], v[198:201], v[120:123]
	v_mfma_f32_16x16x32_bf16 v[108:111], v[60:63], v[206:209], v[108:111]
	v_mfma_f32_16x16x32_bf16 v[104:107], v[68:71], v[206:209], v[104:107]
	v_mfma_f32_16x16x32_bf16 v[92:95], v[60:63], v[228:231], v[92:95]
	v_mfma_f32_16x16x32_bf16 v[88:91], v[68:71], v[228:231], v[88:91]
	s_setprio 0
	s_setprio 1
	v_mfma_f32_16x16x32_bf16 v[132:135], v[144:147], v[176:179], v[132:135]
	v_mfma_f32_16x16x32_bf16 v[128:131], v[162:165], v[176:179], v[128:131]
	v_mfma_f32_16x16x32_bf16 v[116:119], v[144:147], v[194:197], v[116:119]
	v_mfma_f32_16x16x32_bf16 v[112:115], v[162:165], v[194:197], v[112:115]
	v_mfma_f32_16x16x32_bf16 v[100:103], v[144:147], v[202:205], v[100:103]
	v_mfma_f32_16x16x32_bf16 v[96:99], v[162:165], v[202:205], v[96:99]
	v_mfma_f32_16x16x32_bf16 v[84:87], v[144:147], v[224:227], v[84:87]
	v_mfma_f32_16x16x32_bf16 v[80:83], v[162:165], v[224:227], v[80:83]
	v_mfma_f32_16x16x32_bf16 v[132:135], v[148:151], v[180:183], v[132:135]
	v_mfma_f32_16x16x32_bf16 v[128:131], v[172:175], v[180:183], v[128:131]
	v_mfma_f32_16x16x32_bf16 v[116:119], v[148:151], v[198:201], v[116:119]
	v_mfma_f32_16x16x32_bf16 v[112:115], v[172:175], v[198:201], v[112:115]
	v_mfma_f32_16x16x32_bf16 v[100:103], v[148:151], v[206:209], v[100:103]
	v_mfma_f32_16x16x32_bf16 v[96:99], v[172:175], v[206:209], v[96:99]
	v_mfma_f32_16x16x32_bf16 v[84:87], v[148:151], v[228:231], v[84:87]
	v_mfma_f32_16x16x32_bf16 v[80:83], v[172:175], v[228:231], v[80:83]
	s_setprio 0
	s_barrier
	s_add_i32 s28, s48, s46
	v_lshl_add_u64 v[166:167], v[166:167], 0, s[68:69]
	s_mov_b32 m0, s28
	ds_read_b128 v[176:179], v171 offset:49152
	ds_read_b128 v[180:183], v171 offset:50176
	ds_read_b128 v[194:197], v171 offset:51200
	ds_read_b128 v[198:201], v171 offset:52224
	ds_read_b128 v[202:205], v171 offset:53248
	ds_read_b128 v[206:209], v171 offset:54272
	ds_read_b128 v[224:227], v171 offset:55296
	ds_read_b128 v[228:231], v171 offset:56320
	global_load_lds_dwordx4 v[166:167], off
	s_add_i32 m0, s28, 0x2000
	s_add_u32 s28, s42, 0x80080
	v_lshl_add_u64 v[166:167], v[210:211], 0, s[68:69]
	s_addc_u32 s29, s43, 0
	s_add_i32 s42, s49, s46
	global_load_lds_dwordx4 v[166:167], off
	v_lshl_add_u64 v[166:167], s[28:29], 0, v[184:185]
	s_mov_b32 m0, s42
	s_nop 0
	global_load_lds_dwordx4 v[166:167], off
	v_lshl_add_u64 v[166:167], s[28:29], 0, v[152:153]
	s_add_i32 m0, s42, 0x2000
	s_nop 0
	global_load_lds_dwordx4 v[166:167], off
	v_lshl_add_u64 v[166:167], v[216:217], 0, s[68:69]
	s_mov_b32 m0, s53
	s_nop 0
	global_load_lds_dwordx4 v[166:167], off
	v_lshl_add_u64 v[166:167], v[218:219], 0, s[68:69]
	s_waitcnt vmcnt(7)
	s_waitcnt lgkmcnt(0)
	s_barrier
	s_setprio 1
	s_waitcnt lgkmcnt(0)
	v_mfma_f32_16x16x32_bf16 v[76:79], v[56:59], v[176:179], v[76:79]
	v_mfma_f32_16x16x32_bf16 v[72:75], v[64:67], v[176:179], v[72:75]
	s_mov_b32 m0, s58
	s_nop 0
	global_load_lds_dwordx4 v[166:167], off
	v_mfma_f32_16x16x32_bf16 v[52:55], v[56:59], v[194:197], v[52:55]
	v_mfma_f32_16x16x32_bf16 v[48:51], v[64:67], v[194:197], v[48:51]
	v_mfma_f32_16x16x32_bf16 v[28:31], v[56:59], v[202:205], v[28:31]
	v_mfma_f32_16x16x32_bf16 v[24:27], v[64:67], v[202:205], v[24:27]
	v_mfma_f32_16x16x32_bf16 v[12:15], v[56:59], v[224:227], v[12:15]
	v_mfma_f32_16x16x32_bf16 v[8:11], v[64:67], v[224:227], v[8:11]
	v_mfma_f32_16x16x32_bf16 v[76:79], v[60:63], v[180:183], v[76:79]
	v_mfma_f32_16x16x32_bf16 v[72:75], v[68:71], v[180:183], v[72:75]
	v_mfma_f32_16x16x32_bf16 v[52:55], v[60:63], v[198:201], v[52:55]
	v_mfma_f32_16x16x32_bf16 v[48:51], v[68:71], v[198:201], v[48:51]
	v_mfma_f32_16x16x32_bf16 v[28:31], v[60:63], v[206:209], v[28:31]
	v_mfma_f32_16x16x32_bf16 v[24:27], v[68:71], v[206:209], v[24:27]
	v_mfma_f32_16x16x32_bf16 v[12:15], v[60:63], v[228:231], v[12:15]
	v_mfma_f32_16x16x32_bf16 v[8:11], v[68:71], v[228:231], v[8:11]
	s_setprio 0
	s_setprio 1
	v_mfma_f32_16x16x32_bf16 v[40:43], v[144:147], v[176:179], v[40:43]
	v_mfma_f32_16x16x32_bf16 v[68:71], v[148:151], v[180:183], v[40:43]
	v_mfma_f32_16x16x32_bf16 v[40:43], v[162:165], v[176:179], v[44:47]
	v_mfma_f32_16x16x32_bf16 v[36:39], v[144:147], v[194:197], v[36:39]
	v_mfma_f32_16x16x32_bf16 v[32:35], v[162:165], v[194:197], v[32:35]
	v_mfma_f32_16x16x32_bf16 v[20:23], v[144:147], v[202:205], v[20:23]
	v_mfma_f32_16x16x32_bf16 v[16:19], v[162:165], v[202:205], v[16:19]
	v_mfma_f32_16x16x32_bf16 v[4:7], v[144:147], v[224:227], v[4:7]
	v_mfma_f32_16x16x32_bf16 v[0:3], v[162:165], v[224:227], v[0:3]
	v_mfma_f32_16x16x32_bf16 v[64:67], v[172:175], v[180:183], v[40:43]
	v_mfma_f32_16x16x32_bf16 v[36:39], v[148:151], v[198:201], v[36:39]
	v_mfma_f32_16x16x32_bf16 v[32:35], v[172:175], v[198:201], v[32:35]
	v_mfma_f32_16x16x32_bf16 v[20:23], v[148:151], v[206:209], v[20:23]
	v_mfma_f32_16x16x32_bf16 v[16:19], v[172:175], v[206:209], v[16:19]
	v_mfma_f32_16x16x32_bf16 v[4:7], v[148:151], v[228:231], v[4:7]
	v_mfma_f32_16x16x32_bf16 v[0:3], v[172:175], v[228:231], v[0:3]
	s_setprio 0
	s_barrier
	s_add_i32 s79, s79, 2
	s_add_u32 s40, s40, 0x100
	s_addc_u32 s41, s41, 0
	s_add_u32 s62, s62, 0x100
	s_addc_u32 s63, s63, 0
	s_cmp_gt_u32 s79, 29
	s_cbranch_scc0 .LBB0_991
	s_and_b64 vcc, exec, s[8:9]
	s_cbranch_vccz .LBB0_994
	s_barrier

.LBB0_1419:
	s_add_u32 s28, s24, 0xfff80080
	s_addc_u32 s29, s25, -1
	s_add_i32 s48, 0, 0x10000
	s_cmp_eq_u32 s17, 28
	s_cselect_b32 s31, s9, s29
	s_cselect_b32 s30, s11, s28
	s_cselect_b64 vcc, -1, 0
	s_add_i32 s28, 0, 0x14000
	v_add_u32_e32 v164, s48, v147
	v_add_u32_e32 v180, s28, v147
	ds_read_b128 v[152:155], v164
	ds_read_b128 v[156:159], v164 offset:1024
	ds_read_b128 v[160:163], v164 offset:2048
	ds_read_b128 v[164:167], v164 offset:3072
	ds_read_b128 v[168:171], v180
	ds_read_b128 v[172:175], v180 offset:1024
	ds_read_b128 v[176:179], v180 offset:2048
	ds_read_b128 v[180:183], v180 offset:3072
	v_cndmask_b32_e32 v211, v145, v150, vcc
	v_cndmask_b32_e32 v210, v144, v151, vcc
	v_lshl_add_u64 v[216:217], s[24:25], 0, v[136:137]
	s_add_i32 m0, s19, 0xc000
	ds_read_b128 v[194:197], v149
	ds_read_b128 v[198:201], v149 offset:1024
	ds_read_b128 v[202:205], v149 offset:2048
	ds_read_b128 v[206:209], v149 offset:3072
	ds_read_b128 v[224:227], v149 offset:4096
	ds_read_b128 v[228:231], v149 offset:5120
	ds_read_b128 v[232:235], v149 offset:6144
	ds_read_b128 v[236:239], v149 offset:7168
	global_load_lds_dwordx4 v[216:217], off
	v_lshl_add_u64 v[216:217], s[24:25], 0, v[138:139]
	s_waitcnt vmcnt(7)
	s_waitcnt lgkmcnt(0)
	s_barrier
	s_setprio 1
	s_waitcnt lgkmcnt(0)
	v_mfma_f32_16x16x32_bf16 v[124:127], v[152:155], v[194:197], v[124:127]
	v_mfma_f32_16x16x32_bf16 v[116:119], v[160:163], v[194:197], v[116:119]
	s_add_i32 m0, s19, 0xe000
	s_nop 0
	global_load_lds_dwordx4 v[216:217], off
	v_mfma_f32_16x16x32_bf16 v[108:111], v[152:155], v[202:205], v[108:111]
	v_mfma_f32_16x16x32_bf16 v[100:103], v[160:163], v[202:205], v[100:103]
	v_mfma_f32_16x16x32_bf16 v[92:95], v[152:155], v[224:227], v[92:95]
	v_mfma_f32_16x16x32_bf16 v[84:87], v[160:163], v[224:227], v[84:87]
	v_mfma_f32_16x16x32_bf16 v[76:79], v[152:155], v[232:235], v[76:79]
	v_mfma_f32_16x16x32_bf16 v[68:71], v[160:163], v[232:235], v[68:71]
	v_mfma_f32_16x16x32_bf16 v[124:127], v[156:159], v[198:201], v[124:127]
	v_mfma_f32_16x16x32_bf16 v[116:119], v[164:167], v[198:201], v[116:119]
	v_mfma_f32_16x16x32_bf16 v[108:111], v[156:159], v[206:209], v[108:111]
	v_mfma_f32_16x16x32_bf16 v[100:103], v[164:167], v[206:209], v[100:103]
	v_mfma_f32_16x16x32_bf16 v[92:95], v[156:159], v[228:231], v[92:95]
	v_mfma_f32_16x16x32_bf16 v[84:87], v[164:167], v[228:231], v[84:87]
	v_mfma_f32_16x16x32_bf16 v[76:79], v[156:159], v[236:239], v[76:79]
	v_mfma_f32_16x16x32_bf16 v[68:71], v[164:167], v[236:239], v[68:71]
	s_setprio 0
	s_setprio 1
	v_mfma_f32_16x16x32_bf16 v[120:123], v[168:171], v[194:197], v[120:123]
	v_mfma_f32_16x16x32_bf16 v[112:115], v[176:179], v[194:197], v[112:115]
	v_mfma_f32_16x16x32_bf16 v[104:107], v[168:171], v[202:205], v[104:107]
	v_mfma_f32_16x16x32_bf16 v[96:99], v[176:179], v[202:205], v[96:99]
	v_mfma_f32_16x16x32_bf16 v[88:91], v[168:171], v[224:227], v[88:91]
	v_mfma_f32_16x16x32_bf16 v[80:83], v[176:179], v[224:227], v[80:83]
	v_mfma_f32_16x16x32_bf16 v[72:75], v[168:171], v[232:235], v[72:75]
	v_mfma_f32_16x16x32_bf16 v[64:67], v[176:179], v[232:235], v[64:67]
	v_mfma_f32_16x16x32_bf16 v[120:123], v[172:175], v[198:201], v[120:123]
	v_mfma_f32_16x16x32_bf16 v[112:115], v[180:183], v[198:201], v[112:115]
	v_mfma_f32_16x16x32_bf16 v[104:107], v[172:175], v[206:209], v[104:107]
	v_mfma_f32_16x16x32_bf16 v[96:99], v[180:183], v[206:209], v[96:99]
	v_mfma_f32_16x16x32_bf16 v[88:91], v[172:175], v[228:231], v[88:91]
	v_mfma_f32_16x16x32_bf16 v[80:83], v[180:183], v[228:231], v[80:83]
	v_mfma_f32_16x16x32_bf16 v[72:75], v[172:175], v[236:239], v[72:75]
	v_mfma_f32_16x16x32_bf16 v[64:67], v[180:183], v[236:239], v[64:67]
	s_setprio 0
	s_barrier
	s_add_i32 s29, s48, s50
	v_lshl_add_u64 v[216:217], v[210:211], 0, v[130:131]
	s_mov_b32 m0, s29
	ds_read_b128 v[194:197], v149 offset:16384
	ds_read_b128 v[198:201], v149 offset:17408
	ds_read_b128 v[202:205], v149 offset:18432
	ds_read_b128 v[206:209], v149 offset:19456
	ds_read_b128 v[224:227], v149 offset:20480
	ds_read_b128 v[228:231], v149 offset:21504
	ds_read_b128 v[232:235], v149 offset:22528
	ds_read_b128 v[236:239], v149 offset:23552
	global_load_lds_dwordx4 v[216:217], off
	v_lshl_add_u64 v[218:219], v[210:211], 0, v[134:135]
	s_add_i32 m0, s29, 0x2000
	v_lshl_add_u64 v[220:221], v[210:211], 0, s[72:73]
	s_add_i32 s28, s28, s50
	global_load_lds_dwordx4 v[218:219], off
	v_lshl_add_u64 v[240:241], v[220:221], 0, v[130:131]
	s_mov_b32 m0, s28
	v_lshl_add_u64 v[220:221], v[220:221], 0, v[134:135]
	global_load_lds_dwordx4 v[240:241], off
	s_add_i32 m0, s28, 0x2000
	v_lshl_add_u64 v[240:241], s[30:31], 0, v[132:133]
	global_load_lds_dwordx4 v[220:221], off
	v_lshl_add_u64 v[220:221], s[30:31], 0, v[128:129]
	s_mov_b32 m0, s19
	s_nop 0
	global_load_lds_dwordx4 v[220:221], off
	s_waitcnt vmcnt(7)
	s_waitcnt lgkmcnt(0)
	s_barrier
	s_setprio 1
	s_waitcnt lgkmcnt(0)
	v_mfma_f32_16x16x32_bf16 v[60:63], v[152:155], v[194:197], v[60:63]
	v_mfma_f32_16x16x32_bf16 v[52:55], v[160:163], v[194:197], v[52:55]
	s_mov_b32 m0, s51
	s_nop 0
	global_load_lds_dwordx4 v[240:241], off
	v_mfma_f32_16x16x32_bf16 v[44:47], v[152:155], v[202:205], v[44:47]
	v_mfma_f32_16x16x32_bf16 v[36:39], v[160:163], v[202:205], v[36:39]
	v_mfma_f32_16x16x32_bf16 v[28:31], v[152:155], v[224:227], v[28:31]
	v_mfma_f32_16x16x32_bf16 v[20:23], v[160:163], v[224:227], v[20:23]
	v_mfma_f32_16x16x32_bf16 v[12:15], v[152:155], v[232:235], v[12:15]
	v_mfma_f32_16x16x32_bf16 v[4:7], v[160:163], v[232:235], v[4:7]
	v_mfma_f32_16x16x32_bf16 v[60:63], v[156:159], v[198:201], v[60:63]
	v_mfma_f32_16x16x32_bf16 v[52:55], v[164:167], v[198:201], v[52:55]
	v_mfma_f32_16x16x32_bf16 v[44:47], v[156:159], v[206:209], v[44:47]
	v_mfma_f32_16x16x32_bf16 v[36:39], v[164:167], v[206:209], v[36:39]
	v_mfma_f32_16x16x32_bf16 v[28:31], v[156:159], v[228:231], v[28:31]
	v_mfma_f32_16x16x32_bf16 v[20:23], v[164:167], v[228:231], v[20:23]
	v_mfma_f32_16x16x32_bf16 v[12:15], v[156:159], v[236:239], v[12:15]
	v_mfma_f32_16x16x32_bf16 v[4:7], v[164:167], v[236:239], v[4:7]
	s_setprio 0
	s_setprio 1
	v_mfma_f32_16x16x32_bf16 v[56:59], v[168:171], v[194:197], v[56:59]
	v_mfma_f32_16x16x32_bf16 v[48:51], v[176:179], v[194:197], v[48:51]
	v_mfma_f32_16x16x32_bf16 v[40:43], v[168:171], v[202:205], v[40:43]
	v_mfma_f32_16x16x32_bf16 v[32:35], v[176:179], v[202:205], v[32:35]
	v_mfma_f32_16x16x32_bf16 v[24:27], v[168:171], v[224:227], v[24:27]
	v_mfma_f32_16x16x32_bf16 v[16:19], v[176:179], v[224:227], v[16:19]
	v_mfma_f32_16x16x32_bf16 v[8:11], v[168:171], v[232:235], v[8:11]
	v_mfma_f32_16x16x32_bf16 v[0:3], v[176:179], v[232:235], v[0:3]
	v_mfma_f32_16x16x32_bf16 v[56:59], v[172:175], v[198:201], v[56:59]
	v_mfma_f32_16x16x32_bf16 v[48:51], v[180:183], v[198:201], v[48:51]
	v_mfma_f32_16x16x32_bf16 v[40:43], v[172:175], v[206:209], v[40:43]
	v_mfma_f32_16x16x32_bf16 v[32:35], v[180:183], v[206:209], v[32:35]
	v_mfma_f32_16x16x32_bf16 v[24:27], v[172:175], v[228:231], v[24:27]
	v_mfma_f32_16x16x32_bf16 v[16:19], v[180:183], v[228:231], v[16:19]
	v_mfma_f32_16x16x32_bf16 v[8:11], v[172:175], v[236:239], v[8:11]
	v_mfma_f32_16x16x32_bf16 v[0:3], v[180:183], v[236:239], v[0:3]
	s_setprio 0
	s_barrier
	s_add_i32 s48, 0, 0x18000
	s_add_i32 s49, 0, 0x1c000
	v_add_u32_e32 v164, s48, v147
	v_add_u32_e32 v180, s49, v147
	ds_read_b128 v[152:155], v164
	ds_read_b128 v[156:159], v164 offset:1024
	ds_read_b128 v[160:163], v164 offset:2048
	ds_read_b128 v[164:167], v164 offset:3072
	ds_read_b128 v[168:171], v180
	ds_read_b128 v[172:175], v180 offset:1024
	ds_read_b128 v[176:179], v180 offset:2048
	ds_read_b128 v[180:183], v180 offset:3072
	s_add_u32 s28, s30, 0x80000
	s_addc_u32 s29, s31, 0
	s_mov_b32 m0, s52
	v_lshl_add_u64 v[242:243], s[28:29], 0, v[128:129]
	ds_read_b128 v[194:197], v149 offset:32768
	ds_read_b128 v[198:201], v149 offset:33792
	ds_read_b128 v[202:205], v149 offset:34816
	ds_read_b128 v[206:209], v149 offset:35840
	ds_read_b128 v[224:227], v149 offset:36864
	ds_read_b128 v[228:231], v149 offset:37888
	ds_read_b128 v[232:235], v149 offset:38912
	ds_read_b128 v[236:239], v149 offset:39936
	global_load_lds_dwordx4 v[242:243], off
	v_lshl_add_u64 v[242:243], s[28:29], 0, v[132:133]
	s_waitcnt vmcnt(7)
	s_waitcnt lgkmcnt(0)
	s_barrier
	s_setprio 1
	s_waitcnt lgkmcnt(0)
	v_mfma_f32_16x16x32_bf16 v[124:127], v[152:155], v[194:197], v[124:127]
	v_mfma_f32_16x16x32_bf16 v[116:119], v[160:163], v[194:197], v[116:119]
	s_mov_b32 m0, s53
	s_nop 0
	global_load_lds_dwordx4 v[242:243], off
	v_mfma_f32_16x16x32_bf16 v[108:111], v[152:155], v[202:205], v[108:111]
	v_mfma_f32_16x16x32_bf16 v[100:103], v[160:163], v[202:205], v[100:103]
	v_mfma_f32_16x16x32_bf16 v[92:95], v[152:155], v[224:227], v[92:95]
	v_mfma_f32_16x16x32_bf16 v[84:87], v[160:163], v[224:227], v[84:87]
	v_mfma_f32_16x16x32_bf16 v[76:79], v[152:155], v[232:235], v[76:79]
	v_mfma_f32_16x16x32_bf16 v[68:71], v[160:163], v[232:235], v[68:71]
	v_mfma_f32_16x16x32_bf16 v[124:127], v[156:159], v[198:201], v[124:127]
	v_mfma_f32_16x16x32_bf16 v[116:119], v[164:167], v[198:201], v[116:119]
	v_mfma_f32_16x16x32_bf16 v[108:111], v[156:159], v[206:209], v[108:111]
	v_mfma_f32_16x16x32_bf16 v[100:103], v[164:167], v[206:209], v[100:103]
	v_mfma_f32_16x16x32_bf16 v[92:95], v[156:159], v[228:231], v[92:95]
	v_mfma_f32_16x16x32_bf16 v[84:87], v[164:167], v[228:231], v[84:87]
	v_mfma_f32_16x16x32_bf16 v[76:79], v[156:159], v[236:239], v[76:79]
	v_mfma_f32_16x16x32_bf16 v[68:71], v[164:167], v[236:239], v[68:71]
	s_setprio 0
	s_setprio 1
	v_mfma_f32_16x16x32_bf16 v[120:123], v[168:171], v[194:197], v[120:123]
	v_mfma_f32_16x16x32_bf16 v[112:115], v[176:179], v[194:197], v[112:115]
	v_mfma_f32_16x16x32_bf16 v[104:107], v[168:171], v[202:205], v[104:107]
	v_mfma_f32_16x16x32_bf16 v[96:99], v[176:179], v[202:205], v[96:99]
	v_mfma_f32_16x16x32_bf16 v[88:91], v[168:171], v[224:227], v[88:91]
	v_mfma_f32_16x16x32_bf16 v[80:83], v[176:179], v[224:227], v[80:83]
	v_mfma_f32_16x16x32_bf16 v[72:75], v[168:171], v[232:235], v[72:75]
	v_mfma_f32_16x16x32_bf16 v[64:67], v[176:179], v[232:235], v[64:67]
	v_mfma_f32_16x16x32_bf16 v[120:123], v[172:175], v[198:201], v[120:123]
	v_mfma_f32_16x16x32_bf16 v[112:115], v[180:183], v[198:201], v[112:115]
	v_mfma_f32_16x16x32_bf16 v[104:107], v[172:175], v[206:209], v[104:107]
	v_mfma_f32_16x16x32_bf16 v[96:99], v[180:183], v[206:209], v[96:99]
	v_mfma_f32_16x16x32_bf16 v[88:91], v[172:175], v[228:231], v[88:91]
	v_mfma_f32_16x16x32_bf16 v[80:83], v[180:183], v[228:231], v[80:83]
	v_mfma_f32_16x16x32_bf16 v[72:75], v[172:175], v[236:239], v[72:75]
	v_mfma_f32_16x16x32_bf16 v[64:67], v[180:183], v[236:239], v[64:67]
	s_setprio 0
	s_barrier
	s_add_i32 s28, s48, s50
	v_lshl_add_u64 v[216:217], v[216:217], 0, s[68:69]
	s_mov_b32 m0, s28
	ds_read_b128 v[194:197], v149 offset:49152
	ds_read_b128 v[198:201], v149 offset:50176
	ds_read_b128 v[202:205], v149 offset:51200
	ds_read_b128 v[206:209], v149 offset:52224
	ds_read_b128 v[224:227], v149 offset:53248
	ds_read_b128 v[228:231], v149 offset:54272
	ds_read_b128 v[232:235], v149 offset:55296
	ds_read_b128 v[236:239], v149 offset:56320
	global_load_lds_dwordx4 v[216:217], off
	v_lshl_add_u64 v[216:217], v[218:219], 0, s[68:69]
	s_add_i32 m0, s28, 0x2000
	v_lshl_add_u64 v[210:211], v[210:211], 0, s[74:75]
	s_add_i32 s28, s49, s50
	global_load_lds_dwordx4 v[216:217], off
	v_lshl_add_u64 v[216:217], v[210:211], 0, v[130:131]
	s_mov_b32 m0, s28
	v_lshl_add_u64 v[210:211], v[210:211], 0, v[134:135]
	global_load_lds_dwordx4 v[216:217], off
	s_add_i32 m0, s28, 0x2000
	s_nop 0
	global_load_lds_dwordx4 v[210:211], off
	v_lshl_add_u64 v[210:211], v[220:221], 0, s[68:69]
	s_mov_b32 m0, s58
	s_nop 0
	global_load_lds_dwordx4 v[210:211], off
	v_lshl_add_u64 v[210:211], v[240:241], 0, s[68:69]
	s_waitcnt vmcnt(7)
	s_waitcnt lgkmcnt(0)
	s_barrier
	s_setprio 1
	s_waitcnt lgkmcnt(0)
	v_mfma_f32_16x16x32_bf16 v[60:63], v[152:155], v[194:197], v[60:63]
	v_mfma_f32_16x16x32_bf16 v[52:55], v[160:163], v[194:197], v[52:55]
	s_mov_b32 m0, s59
	s_nop 0
	global_load_lds_dwordx4 v[210:211], off
	v_mfma_f32_16x16x32_bf16 v[44:47], v[152:155], v[202:205], v[44:47]
	v_mfma_f32_16x16x32_bf16 v[36:39], v[160:163], v[202:205], v[36:39]
	v_mfma_f32_16x16x32_bf16 v[28:31], v[152:155], v[224:227], v[28:31]
	v_mfma_f32_16x16x32_bf16 v[20:23], v[160:163], v[224:227], v[20:23]
	v_mfma_f32_16x16x32_bf16 v[12:15], v[152:155], v[232:235], v[12:15]
	v_mfma_f32_16x16x32_bf16 v[4:7], v[160:163], v[232:235], v[4:7]
	v_mfma_f32_16x16x32_bf16 v[60:63], v[156:159], v[198:201], v[60:63]
	v_mfma_f32_16x16x32_bf16 v[52:55], v[164:167], v[198:201], v[52:55]
	v_mfma_f32_16x16x32_bf16 v[44:47], v[156:159], v[206:209], v[44:47]
	v_mfma_f32_16x16x32_bf16 v[36:39], v[164:167], v[206:209], v[36:39]
	v_mfma_f32_16x16x32_bf16 v[28:31], v[156:159], v[228:231], v[28:31]
	v_mfma_f32_16x16x32_bf16 v[20:23], v[164:167], v[228:231], v[20:23]
	v_mfma_f32_16x16x32_bf16 v[12:15], v[156:159], v[236:239], v[12:15]
	v_mfma_f32_16x16x32_bf16 v[4:7], v[164:167], v[236:239], v[4:7]
	s_setprio 0
	s_setprio 1
	v_mfma_f32_16x16x32_bf16 v[56:59], v[168:171], v[194:197], v[56:59]
	v_mfma_f32_16x16x32_bf16 v[48:51], v[176:179], v[194:197], v[48:51]
	v_mfma_f32_16x16x32_bf16 v[40:43], v[168:171], v[202:205], v[40:43]
	v_mfma_f32_16x16x32_bf16 v[32:35], v[176:179], v[202:205], v[32:35]
	v_mfma_f32_16x16x32_bf16 v[24:27], v[168:171], v[224:227], v[24:27]
	v_mfma_f32_16x16x32_bf16 v[16:19], v[176:179], v[224:227], v[16:19]
	v_mfma_f32_16x16x32_bf16 v[8:11], v[168:171], v[232:235], v[8:11]
	v_mfma_f32_16x16x32_bf16 v[0:3], v[176:179], v[232:235], v[0:3]
	v_mfma_f32_16x16x32_bf16 v[56:59], v[172:175], v[198:201], v[56:59]
	v_mfma_f32_16x16x32_bf16 v[48:51], v[180:183], v[198:201], v[48:51]
	v_mfma_f32_16x16x32_bf16 v[40:43], v[172:175], v[206:209], v[40:43]
	v_mfma_f32_16x16x32_bf16 v[32:35], v[180:183], v[206:209], v[32:35]
	v_mfma_f32_16x16x32_bf16 v[24:27], v[172:175], v[228:231], v[24:27]
	v_mfma_f32_16x16x32_bf16 v[16:19], v[180:183], v[228:231], v[16:19]
	v_mfma_f32_16x16x32_bf16 v[8:11], v[172:175], v[236:239], v[8:11]
	v_mfma_f32_16x16x32_bf16 v[0:3], v[180:183], v[236:239], v[0:3]
	s_setprio 0
	s_barrier
	s_add_i32 s17, s17, 2
	s_add_u32 s24, s24, 0x100
	s_addc_u32 s25, s25, 0
	s_cmp_gt_u32 s17, 29
	v_lshl_add_u64 v[144:145], v[144:145], 0, s[76:77]
	s_cbranch_scc0 .LBB0_1419
	s_and_b64 vcc, exec, s[6:7]
	s_cbranch_vccz .LBB0_1422
	s_barrier

.LBB0_1491:
	s_add_u32 s14, s12, 0x100
	s_addc_u32 s15, s13, 0
	s_add_i32 s28, 0, 0x10000
	s_cmp_eq_u32 s59, 40
	s_cselect_b32 s17, s53, s15
	s_cselect_b32 s16, s58, s14
	s_cselect_b64 vcc, -1, 0
	s_add_i32 s29, 0, 0x14000
	v_add_u32_e32 v164, s28, v147
	v_add_u32_e32 v180, s29, v147
	ds_read_b128 v[152:155], v164
	ds_read_b128 v[156:159], v164 offset:1024
	ds_read_b128 v[160:163], v164 offset:2048
	ds_read_b128 v[164:167], v164 offset:3072
	ds_read_b128 v[168:171], v180
	ds_read_b128 v[172:175], v180 offset:1024
	ds_read_b128 v[176:179], v180 offset:2048
	ds_read_b128 v[180:183], v180 offset:3072
	v_cndmask_b32_e32 v211, v145, v150, vcc
	v_cndmask_b32_e32 v210, v144, v151, vcc
	v_lshl_add_u64 v[216:217], s[12:13], 0, v[136:137]
	s_add_i32 m0, s40, 0xc000
	ds_read_b128 v[194:197], v149
	ds_read_b128 v[198:201], v149 offset:1024
	ds_read_b128 v[202:205], v149 offset:2048
	ds_read_b128 v[206:209], v149 offset:3072
	ds_read_b128 v[224:227], v149 offset:4096
	ds_read_b128 v[228:231], v149 offset:5120
	ds_read_b128 v[232:235], v149 offset:6144
	ds_read_b128 v[236:239], v149 offset:7168
	global_load_lds_dwordx4 v[216:217], off
	v_lshl_add_u64 v[216:217], s[12:13], 0, v[138:139]
	s_waitcnt vmcnt(7)
	s_waitcnt lgkmcnt(0)
	s_barrier
	s_setprio 1
	s_waitcnt lgkmcnt(0)
	v_mfma_f32_16x16x32_bf16 v[124:127], v[152:155], v[194:197], v[124:127]
	v_mfma_f32_16x16x32_bf16 v[120:123], v[160:163], v[194:197], v[120:123]
	s_add_i32 m0, s40, 0xe000
	s_nop 0
	global_load_lds_dwordx4 v[216:217], off
	v_mfma_f32_16x16x32_bf16 v[116:119], v[152:155], v[202:205], v[116:119]
	v_mfma_f32_16x16x32_bf16 v[108:111], v[160:163], v[202:205], v[108:111]
	v_mfma_f32_16x16x32_bf16 v[100:103], v[152:155], v[224:227], v[100:103]
	v_mfma_f32_16x16x32_bf16 v[92:95], v[160:163], v[224:227], v[92:95]
	v_mfma_f32_16x16x32_bf16 v[80:83], v[152:155], v[232:235], v[80:83]
	v_mfma_f32_16x16x32_bf16 v[72:75], v[160:163], v[232:235], v[72:75]
	v_mfma_f32_16x16x32_bf16 v[124:127], v[156:159], v[198:201], v[124:127]
	v_mfma_f32_16x16x32_bf16 v[120:123], v[164:167], v[198:201], v[120:123]
	v_mfma_f32_16x16x32_bf16 v[116:119], v[156:159], v[206:209], v[116:119]
	v_mfma_f32_16x16x32_bf16 v[108:111], v[164:167], v[206:209], v[108:111]
	v_mfma_f32_16x16x32_bf16 v[100:103], v[156:159], v[228:231], v[100:103]
	v_mfma_f32_16x16x32_bf16 v[92:95], v[164:167], v[228:231], v[92:95]
	v_mfma_f32_16x16x32_bf16 v[80:83], v[156:159], v[236:239], v[80:83]
	v_mfma_f32_16x16x32_bf16 v[72:75], v[164:167], v[236:239], v[72:75]
	s_setprio 0
	s_setprio 1
	v_mfma_f32_16x16x32_bf16 v[112:115], v[168:171], v[194:197], v[112:115]
	v_mfma_f32_16x16x32_bf16 v[104:107], v[176:179], v[194:197], v[104:107]
	v_mfma_f32_16x16x32_bf16 v[96:99], v[168:171], v[202:205], v[96:99]
	v_mfma_f32_16x16x32_bf16 v[88:91], v[176:179], v[202:205], v[88:91]
	v_mfma_f32_16x16x32_bf16 v[84:87], v[168:171], v[224:227], v[84:87]
	v_mfma_f32_16x16x32_bf16 v[76:79], v[176:179], v[224:227], v[76:79]
	v_mfma_f32_16x16x32_bf16 v[68:71], v[168:171], v[232:235], v[68:71]
	v_mfma_f32_16x16x32_bf16 v[64:67], v[176:179], v[232:235], v[64:67]
	v_mfma_f32_16x16x32_bf16 v[112:115], v[172:175], v[198:201], v[112:115]
	v_mfma_f32_16x16x32_bf16 v[104:107], v[180:183], v[198:201], v[104:107]
	v_mfma_f32_16x16x32_bf16 v[96:99], v[172:175], v[206:209], v[96:99]
	v_mfma_f32_16x16x32_bf16 v[88:91], v[180:183], v[206:209], v[88:91]
	v_mfma_f32_16x16x32_bf16 v[84:87], v[172:175], v[228:231], v[84:87]
	v_mfma_f32_16x16x32_bf16 v[76:79], v[180:183], v[228:231], v[76:79]
	v_mfma_f32_16x16x32_bf16 v[68:71], v[172:175], v[236:239], v[68:71]
	v_mfma_f32_16x16x32_bf16 v[64:67], v[180:183], v[236:239], v[64:67]
	s_setprio 0
	s_barrier
	s_add_i32 s12, s28, s30
	v_lshl_add_u64 v[216:217], v[210:211], 0, v[132:133]
	s_mov_b32 m0, s12
	ds_read_b128 v[194:197], v149 offset:16384
	ds_read_b128 v[198:201], v149 offset:17408
	ds_read_b128 v[202:205], v149 offset:18432
	ds_read_b128 v[206:209], v149 offset:19456
	ds_read_b128 v[224:227], v149 offset:20480
	ds_read_b128 v[228:231], v149 offset:21504
	ds_read_b128 v[232:235], v149 offset:22528
	ds_read_b128 v[236:239], v149 offset:23552
	global_load_lds_dwordx4 v[216:217], off
	v_lshl_add_u64 v[218:219], v[210:211], 0, v[128:129]
	s_add_i32 m0, s12, 0x2000
	v_lshl_add_u64 v[220:221], v[210:211], 0, s[72:73]
	s_add_i32 s12, s29, s30
	global_load_lds_dwordx4 v[218:219], off
	v_lshl_add_u64 v[240:241], v[220:221], 0, v[132:133]
	s_mov_b32 m0, s12
	v_lshl_add_u64 v[220:221], v[220:221], 0, v[128:129]
	global_load_lds_dwordx4 v[240:241], off
	s_add_i32 m0, s12, 0x2000
	v_lshl_add_u64 v[240:241], s[16:17], 0, v[130:131]
	global_load_lds_dwordx4 v[220:221], off
	v_lshl_add_u64 v[220:221], s[16:17], 0, v[134:135]
	s_mov_b32 m0, s40
	s_nop 0
	global_load_lds_dwordx4 v[220:221], off
	s_waitcnt vmcnt(7)
	s_waitcnt lgkmcnt(0)
	s_barrier
	s_setprio 1
	s_waitcnt lgkmcnt(0)
	v_mfma_f32_16x16x32_bf16 v[60:63], v[152:155], v[194:197], v[60:63]
	v_mfma_f32_16x16x32_bf16 v[56:59], v[160:163], v[194:197], v[56:59]
	s_mov_b32 m0, s41
	s_nop 0
	global_load_lds_dwordx4 v[240:241], off
	v_mfma_f32_16x16x32_bf16 v[52:55], v[152:155], v[202:205], v[52:55]
	v_mfma_f32_16x16x32_bf16 v[44:47], v[160:163], v[202:205], v[44:47]
	v_mfma_f32_16x16x32_bf16 v[36:39], v[152:155], v[224:227], v[36:39]
	v_mfma_f32_16x16x32_bf16 v[28:31], v[160:163], v[224:227], v[28:31]
	v_mfma_f32_16x16x32_bf16 v[20:23], v[152:155], v[232:235], v[20:23]
	v_mfma_f32_16x16x32_bf16 v[12:15], v[160:163], v[232:235], v[12:15]
	v_mfma_f32_16x16x32_bf16 v[60:63], v[156:159], v[198:201], v[60:63]
	v_mfma_f32_16x16x32_bf16 v[56:59], v[164:167], v[198:201], v[56:59]
	v_mfma_f32_16x16x32_bf16 v[52:55], v[156:159], v[206:209], v[52:55]
	v_mfma_f32_16x16x32_bf16 v[44:47], v[164:167], v[206:209], v[44:47]
	v_mfma_f32_16x16x32_bf16 v[36:39], v[156:159], v[228:231], v[36:39]
	v_mfma_f32_16x16x32_bf16 v[28:31], v[164:167], v[228:231], v[28:31]
	v_mfma_f32_16x16x32_bf16 v[20:23], v[156:159], v[236:239], v[20:23]
	v_mfma_f32_16x16x32_bf16 v[12:15], v[164:167], v[236:239], v[12:15]
	s_setprio 0
	s_setprio 1
	v_mfma_f32_16x16x32_bf16 v[48:51], v[168:171], v[194:197], v[48:51]
	v_mfma_f32_16x16x32_bf16 v[40:43], v[176:179], v[194:197], v[40:43]
	v_mfma_f32_16x16x32_bf16 v[32:35], v[168:171], v[202:205], v[32:35]
	v_mfma_f32_16x16x32_bf16 v[24:27], v[176:179], v[202:205], v[24:27]
	v_mfma_f32_16x16x32_bf16 v[16:19], v[168:171], v[224:227], v[16:19]
	v_mfma_f32_16x16x32_bf16 v[8:11], v[176:179], v[224:227], v[8:11]
	v_mfma_f32_16x16x32_bf16 v[4:7], v[168:171], v[232:235], v[4:7]
	v_mfma_f32_16x16x32_bf16 v[0:3], v[176:179], v[232:235], v[0:3]
	v_mfma_f32_16x16x32_bf16 v[48:51], v[172:175], v[198:201], v[48:51]
	v_mfma_f32_16x16x32_bf16 v[40:43], v[180:183], v[198:201], v[40:43]
	v_mfma_f32_16x16x32_bf16 v[32:35], v[172:175], v[206:209], v[32:35]
	v_mfma_f32_16x16x32_bf16 v[24:27], v[180:183], v[206:209], v[24:27]
	v_mfma_f32_16x16x32_bf16 v[16:19], v[172:175], v[228:231], v[16:19]
	v_mfma_f32_16x16x32_bf16 v[8:11], v[180:183], v[228:231], v[8:11]
	v_mfma_f32_16x16x32_bf16 v[4:7], v[172:175], v[236:239], v[4:7]
	v_mfma_f32_16x16x32_bf16 v[0:3], v[180:183], v[236:239], v[0:3]
	s_setprio 0
	s_barrier
	s_add_i32 s28, 0, 0x18000
	s_add_i32 s29, 0, 0x1c000
	v_add_u32_e32 v164, s28, v147
	v_add_u32_e32 v180, s29, v147
	ds_read_b128 v[152:155], v164
	ds_read_b128 v[156:159], v164 offset:1024
	ds_read_b128 v[160:163], v164 offset:2048
	ds_read_b128 v[164:167], v164 offset:3072
	ds_read_b128 v[168:171], v180
	ds_read_b128 v[172:175], v180 offset:1024
	ds_read_b128 v[176:179], v180 offset:2048
	ds_read_b128 v[180:183], v180 offset:3072
	s_add_u32 s12, s16, 0xb0000
	s_addc_u32 s13, s17, 0
	s_mov_b32 m0, s42
	v_lshl_add_u64 v[242:243], s[12:13], 0, v[134:135]
	ds_read_b128 v[194:197], v149 offset:32768
	ds_read_b128 v[198:201], v149 offset:33792
	ds_read_b128 v[202:205], v149 offset:34816
	ds_read_b128 v[206:209], v149 offset:35840
	ds_read_b128 v[224:227], v149 offset:36864
	ds_read_b128 v[228:231], v149 offset:37888
	ds_read_b128 v[232:235], v149 offset:38912
	ds_read_b128 v[236:239], v149 offset:39936
	global_load_lds_dwordx4 v[242:243], off
	v_lshl_add_u64 v[242:243], s[12:13], 0, v[130:131]
	s_waitcnt vmcnt(7)
	s_waitcnt lgkmcnt(0)
	s_barrier
	s_setprio 1
	s_waitcnt lgkmcnt(0)
	v_mfma_f32_16x16x32_bf16 v[124:127], v[152:155], v[194:197], v[124:127]
	v_mfma_f32_16x16x32_bf16 v[120:123], v[160:163], v[194:197], v[120:123]
	s_mov_b32 m0, s43
	s_nop 0
	global_load_lds_dwordx4 v[242:243], off
	v_mfma_f32_16x16x32_bf16 v[116:119], v[152:155], v[202:205], v[116:119]
	v_mfma_f32_16x16x32_bf16 v[108:111], v[160:163], v[202:205], v[108:111]
	v_mfma_f32_16x16x32_bf16 v[100:103], v[152:155], v[224:227], v[100:103]
	v_mfma_f32_16x16x32_bf16 v[92:95], v[160:163], v[224:227], v[92:95]
	v_mfma_f32_16x16x32_bf16 v[80:83], v[152:155], v[232:235], v[80:83]
	v_mfma_f32_16x16x32_bf16 v[72:75], v[160:163], v[232:235], v[72:75]
	v_mfma_f32_16x16x32_bf16 v[124:127], v[156:159], v[198:201], v[124:127]
	v_mfma_f32_16x16x32_bf16 v[120:123], v[164:167], v[198:201], v[120:123]
	v_mfma_f32_16x16x32_bf16 v[116:119], v[156:159], v[206:209], v[116:119]
	v_mfma_f32_16x16x32_bf16 v[108:111], v[164:167], v[206:209], v[108:111]
	v_mfma_f32_16x16x32_bf16 v[100:103], v[156:159], v[228:231], v[100:103]
	v_mfma_f32_16x16x32_bf16 v[92:95], v[164:167], v[228:231], v[92:95]
	v_mfma_f32_16x16x32_bf16 v[80:83], v[156:159], v[236:239], v[80:83]
	v_mfma_f32_16x16x32_bf16 v[72:75], v[164:167], v[236:239], v[72:75]
	s_setprio 0
	s_setprio 1
	v_mfma_f32_16x16x32_bf16 v[112:115], v[168:171], v[194:197], v[112:115]
	v_mfma_f32_16x16x32_bf16 v[104:107], v[176:179], v[194:197], v[104:107]
	v_mfma_f32_16x16x32_bf16 v[96:99], v[168:171], v[202:205], v[96:99]
	v_mfma_f32_16x16x32_bf16 v[88:91], v[176:179], v[202:205], v[88:91]
	v_mfma_f32_16x16x32_bf16 v[84:87], v[168:171], v[224:227], v[84:87]
	v_mfma_f32_16x16x32_bf16 v[76:79], v[176:179], v[224:227], v[76:79]
	v_mfma_f32_16x16x32_bf16 v[68:71], v[168:171], v[232:235], v[68:71]
	v_mfma_f32_16x16x32_bf16 v[64:67], v[176:179], v[232:235], v[64:67]
	v_mfma_f32_16x16x32_bf16 v[112:115], v[172:175], v[198:201], v[112:115]
	v_mfma_f32_16x16x32_bf16 v[104:107], v[180:183], v[198:201], v[104:107]
	v_mfma_f32_16x16x32_bf16 v[96:99], v[172:175], v[206:209], v[96:99]
	v_mfma_f32_16x16x32_bf16 v[88:91], v[180:183], v[206:209], v[88:91]
	v_mfma_f32_16x16x32_bf16 v[84:87], v[172:175], v[228:231], v[84:87]
	v_mfma_f32_16x16x32_bf16 v[76:79], v[180:183], v[228:231], v[76:79]
	v_mfma_f32_16x16x32_bf16 v[68:71], v[172:175], v[236:239], v[68:71]
	v_mfma_f32_16x16x32_bf16 v[64:67], v[180:183], v[236:239], v[64:67]
	s_setprio 0
	s_barrier
	s_add_i32 s12, s28, s30
	v_lshl_add_u64 v[216:217], v[216:217], 0, s[68:69]
	s_mov_b32 m0, s12
	ds_read_b128 v[194:197], v149 offset:49152
	ds_read_b128 v[198:201], v149 offset:50176
	ds_read_b128 v[202:205], v149 offset:51200
	ds_read_b128 v[206:209], v149 offset:52224
	ds_read_b128 v[224:227], v149 offset:53248
	ds_read_b128 v[228:231], v149 offset:54272
	ds_read_b128 v[232:235], v149 offset:55296
	ds_read_b128 v[236:239], v149 offset:56320
	global_load_lds_dwordx4 v[216:217], off
	v_lshl_add_u64 v[216:217], v[218:219], 0, s[68:69]
	s_add_i32 m0, s12, 0x2000
	v_lshl_add_u64 v[210:211], v[210:211], 0, s[74:75]
	s_add_i32 s12, s29, s30
	global_load_lds_dwordx4 v[216:217], off
	v_lshl_add_u64 v[216:217], v[210:211], 0, v[132:133]
	s_mov_b32 m0, s12
	v_lshl_add_u64 v[210:211], v[210:211], 0, v[128:129]
	global_load_lds_dwordx4 v[216:217], off
	s_add_i32 m0, s12, 0x2000
	s_nop 0
	global_load_lds_dwordx4 v[210:211], off
	v_lshl_add_u64 v[210:211], v[220:221], 0, s[68:69]
	s_mov_b32 m0, s44
	s_nop 0
	global_load_lds_dwordx4 v[210:211], off
	v_lshl_add_u64 v[210:211], v[240:241], 0, s[68:69]
	s_waitcnt vmcnt(7)
	s_waitcnt lgkmcnt(0)
	s_barrier
	s_setprio 1
	s_waitcnt lgkmcnt(0)
	v_mfma_f32_16x16x32_bf16 v[60:63], v[152:155], v[194:197], v[60:63]
	v_mfma_f32_16x16x32_bf16 v[56:59], v[160:163], v[194:197], v[56:59]
	s_mov_b32 m0, s45
	s_nop 0
	global_load_lds_dwordx4 v[210:211], off
	v_mfma_f32_16x16x32_bf16 v[52:55], v[152:155], v[202:205], v[52:55]
	v_mfma_f32_16x16x32_bf16 v[44:47], v[160:163], v[202:205], v[44:47]
	v_mfma_f32_16x16x32_bf16 v[36:39], v[152:155], v[224:227], v[36:39]
	v_mfma_f32_16x16x32_bf16 v[28:31], v[160:163], v[224:227], v[28:31]
	v_mfma_f32_16x16x32_bf16 v[20:23], v[152:155], v[232:235], v[20:23]
	v_mfma_f32_16x16x32_bf16 v[12:15], v[160:163], v[232:235], v[12:15]
	v_mfma_f32_16x16x32_bf16 v[60:63], v[156:159], v[198:201], v[60:63]
	v_mfma_f32_16x16x32_bf16 v[56:59], v[164:167], v[198:201], v[56:59]
	v_mfma_f32_16x16x32_bf16 v[52:55], v[156:159], v[206:209], v[52:55]
	v_mfma_f32_16x16x32_bf16 v[44:47], v[164:167], v[206:209], v[44:47]
	v_mfma_f32_16x16x32_bf16 v[36:39], v[156:159], v[228:231], v[36:39]
	v_mfma_f32_16x16x32_bf16 v[28:31], v[164:167], v[228:231], v[28:31]
	v_mfma_f32_16x16x32_bf16 v[20:23], v[156:159], v[236:239], v[20:23]
	v_mfma_f32_16x16x32_bf16 v[12:15], v[164:167], v[236:239], v[12:15]
	s_setprio 0
	s_setprio 1
	v_mfma_f32_16x16x32_bf16 v[48:51], v[168:171], v[194:197], v[48:51]
	v_mfma_f32_16x16x32_bf16 v[40:43], v[176:179], v[194:197], v[40:43]
	v_mfma_f32_16x16x32_bf16 v[32:35], v[168:171], v[202:205], v[32:35]
	v_mfma_f32_16x16x32_bf16 v[24:27], v[176:179], v[202:205], v[24:27]
	v_mfma_f32_16x16x32_bf16 v[16:19], v[168:171], v[224:227], v[16:19]
	v_mfma_f32_16x16x32_bf16 v[8:11], v[176:179], v[224:227], v[8:11]
	v_mfma_f32_16x16x32_bf16 v[4:7], v[168:171], v[232:235], v[4:7]
	v_mfma_f32_16x16x32_bf16 v[0:3], v[176:179], v[232:235], v[0:3]
	v_mfma_f32_16x16x32_bf16 v[48:51], v[172:175], v[198:201], v[48:51]
	v_mfma_f32_16x16x32_bf16 v[40:43], v[180:183], v[198:201], v[40:43]
	v_mfma_f32_16x16x32_bf16 v[32:35], v[172:175], v[206:209], v[32:35]
	v_mfma_f32_16x16x32_bf16 v[24:27], v[180:183], v[206:209], v[24:27]
	v_mfma_f32_16x16x32_bf16 v[16:19], v[172:175], v[228:231], v[16:19]
	v_mfma_f32_16x16x32_bf16 v[8:11], v[180:183], v[228:231], v[8:11]
	v_mfma_f32_16x16x32_bf16 v[4:7], v[172:175], v[236:239], v[4:7]
	v_mfma_f32_16x16x32_bf16 v[0:3], v[180:183], v[236:239], v[0:3]
	s_setprio 0
	s_barrier
	s_add_i32 s59, s59, 2
	v_lshl_add_u64 v[144:145], v[144:145], 0, s[60:61]
	s_cmp_gt_u32 s59, 41
	s_mov_b64 s[12:13], s[14:15]
	s_cbranch_scc0 .LBB0_1491
	s_mov_b64 s[14:15], 0xb0000
	s_and_b64 vcc, exec, s[6:7]
	s_cbranch_vccz .LBB0_1494
	s_barrier

.LBB0_1587:
	s_add_u32 s28, s24, 0xfff80080
	s_addc_u32 s29, s25, -1
	s_add_i32 s48, 0, 0x10000
	s_cmp_eq_u32 s51, 28
	s_cselect_b32 s39, s9, s29
	s_cselect_b32 s38, s11, s28
	s_cselect_b32 s31, s45, s50
	s_cselect_b32 s30, s46, s47
	s_add_i32 s49, 0, 0x14000
	v_add_u32_e32 v154, s48, v139
	v_add_u32_e32 v170, s49, v139
	ds_read_b128 v[142:145], v154
	ds_read_b128 v[146:149], v154 offset:1024
	ds_read_b128 v[150:153], v154 offset:2048
	ds_read_b128 v[154:157], v154 offset:3072
	ds_read_b128 v[158:161], v170
	ds_read_b128 v[162:165], v170 offset:1024
	ds_read_b128 v[166:169], v170 offset:2048
	ds_read_b128 v[170:173], v170 offset:3072
	v_lshl_add_u64 v[182:183], s[24:25], 0, v[134:135]
	s_add_i32 m0, s20, 0xc000
	ds_read_b128 v[174:177], v141
	ds_read_b128 v[178:181], v141 offset:1024
	ds_read_b128 v[194:197], v141 offset:2048
	ds_read_b128 v[198:201], v141 offset:3072
	ds_read_b128 v[202:205], v141 offset:4096
	ds_read_b128 v[206:209], v141 offset:5120
	ds_read_b128 v[224:227], v141 offset:6144
	ds_read_b128 v[228:231], v141 offset:7168
	global_load_lds_dwordx4 v[182:183], off
	v_lshl_add_u64 v[182:183], s[24:25], 0, v[136:137]
	s_waitcnt vmcnt(7)
	s_waitcnt lgkmcnt(0)
	s_barrier
	s_setprio 1
	s_waitcnt lgkmcnt(0)
	v_mfma_f32_16x16x32_bf16 v[124:127], v[142:145], v[174:177], v[124:127]
	v_mfma_f32_16x16x32_bf16 v[116:119], v[150:153], v[174:177], v[116:119]
	s_add_i32 m0, s20, 0xe000
	s_nop 0
	global_load_lds_dwordx4 v[182:183], off
	v_mfma_f32_16x16x32_bf16 v[108:111], v[142:145], v[194:197], v[108:111]
	v_mfma_f32_16x16x32_bf16 v[100:103], v[150:153], v[194:197], v[100:103]
	v_mfma_f32_16x16x32_bf16 v[92:95], v[142:145], v[202:205], v[92:95]
	v_mfma_f32_16x16x32_bf16 v[84:87], v[150:153], v[202:205], v[84:87]
	v_mfma_f32_16x16x32_bf16 v[76:79], v[142:145], v[224:227], v[76:79]
	v_mfma_f32_16x16x32_bf16 v[68:71], v[150:153], v[224:227], v[68:71]
	v_mfma_f32_16x16x32_bf16 v[124:127], v[146:149], v[178:181], v[124:127]
	v_mfma_f32_16x16x32_bf16 v[116:119], v[154:157], v[178:181], v[116:119]
	v_mfma_f32_16x16x32_bf16 v[108:111], v[146:149], v[198:201], v[108:111]
	v_mfma_f32_16x16x32_bf16 v[100:103], v[154:157], v[198:201], v[100:103]
	v_mfma_f32_16x16x32_bf16 v[92:95], v[146:149], v[206:209], v[92:95]
	v_mfma_f32_16x16x32_bf16 v[84:87], v[154:157], v[206:209], v[84:87]
	v_mfma_f32_16x16x32_bf16 v[76:79], v[146:149], v[228:231], v[76:79]
	v_mfma_f32_16x16x32_bf16 v[68:71], v[154:157], v[228:231], v[68:71]
	s_setprio 0
	s_setprio 1
	v_mfma_f32_16x16x32_bf16 v[120:123], v[158:161], v[174:177], v[120:123]
	v_mfma_f32_16x16x32_bf16 v[112:115], v[166:169], v[174:177], v[112:115]
	v_mfma_f32_16x16x32_bf16 v[104:107], v[158:161], v[194:197], v[104:107]
	v_mfma_f32_16x16x32_bf16 v[96:99], v[166:169], v[194:197], v[96:99]
	v_mfma_f32_16x16x32_bf16 v[88:91], v[158:161], v[202:205], v[88:91]
	v_mfma_f32_16x16x32_bf16 v[80:83], v[166:169], v[202:205], v[80:83]
	v_mfma_f32_16x16x32_bf16 v[72:75], v[158:161], v[224:227], v[72:75]
	v_mfma_f32_16x16x32_bf16 v[64:67], v[166:169], v[224:227], v[64:67]
	v_mfma_f32_16x16x32_bf16 v[120:123], v[162:165], v[178:181], v[120:123]
	v_mfma_f32_16x16x32_bf16 v[112:115], v[170:173], v[178:181], v[112:115]
	v_mfma_f32_16x16x32_bf16 v[104:107], v[162:165], v[198:201], v[104:107]
	v_mfma_f32_16x16x32_bf16 v[96:99], v[170:173], v[198:201], v[96:99]
	v_mfma_f32_16x16x32_bf16 v[88:91], v[162:165], v[206:209], v[88:91]
	v_mfma_f32_16x16x32_bf16 v[80:83], v[170:173], v[206:209], v[80:83]
	v_mfma_f32_16x16x32_bf16 v[72:75], v[162:165], v[228:231], v[72:75]
	v_mfma_f32_16x16x32_bf16 v[64:67], v[170:173], v[228:231], v[64:67]
	s_setprio 0
	s_barrier
	s_add_i32 s28, s48, s4
	v_lshl_add_u64 v[182:183], s[30:31], 0, v[184:185]
	s_mov_b32 m0, s28
	ds_read_b128 v[174:177], v141 offset:16384
	ds_read_b128 v[178:181], v141 offset:17408
	ds_read_b128 v[194:197], v141 offset:18432
	ds_read_b128 v[198:201], v141 offset:19456
	ds_read_b128 v[202:205], v141 offset:20480
	ds_read_b128 v[206:209], v141 offset:21504
	ds_read_b128 v[224:227], v141 offset:22528
	ds_read_b128 v[228:231], v141 offset:23552
	global_load_lds_dwordx4 v[182:183], off
	s_add_i32 m0, s28, 0x2000
	s_add_u32 s28, s30, 0x80000
	v_lshl_add_u64 v[210:211], s[30:31], 0, v[128:129]
	s_addc_u32 s29, s31, 0
	s_add_i32 s48, s49, s4
	global_load_lds_dwordx4 v[210:211], off
	v_lshl_add_u64 v[216:217], s[28:29], 0, v[184:185]
	s_mov_b32 m0, s48
	v_lshl_add_u64 v[218:219], s[38:39], 0, v[130:131]
	global_load_lds_dwordx4 v[216:217], off
	v_lshl_add_u64 v[216:217], s[28:29], 0, v[128:129]
	s_add_i32 m0, s48, 0x2000
	s_nop 0
	global_load_lds_dwordx4 v[216:217], off
	v_lshl_add_u64 v[216:217], s[38:39], 0, v[132:133]
	s_mov_b32 m0, s20
	s_nop 0
	global_load_lds_dwordx4 v[216:217], off
	s_waitcnt vmcnt(7)
	s_waitcnt lgkmcnt(0)
	s_barrier
	s_setprio 1
	s_waitcnt lgkmcnt(0)
	v_mfma_f32_16x16x32_bf16 v[60:63], v[142:145], v[174:177], v[60:63]
	v_mfma_f32_16x16x32_bf16 v[52:55], v[150:153], v[174:177], v[52:55]
	s_mov_b32 m0, s21
	s_nop 0
	global_load_lds_dwordx4 v[218:219], off
	v_mfma_f32_16x16x32_bf16 v[44:47], v[142:145], v[194:197], v[44:47]
	v_mfma_f32_16x16x32_bf16 v[36:39], v[150:153], v[194:197], v[36:39]
	v_mfma_f32_16x16x32_bf16 v[28:31], v[142:145], v[202:205], v[28:31]
	v_mfma_f32_16x16x32_bf16 v[20:23], v[150:153], v[202:205], v[20:23]
	v_mfma_f32_16x16x32_bf16 v[12:15], v[142:145], v[224:227], v[12:15]
	v_mfma_f32_16x16x32_bf16 v[4:7], v[150:153], v[224:227], v[4:7]
	v_mfma_f32_16x16x32_bf16 v[60:63], v[146:149], v[178:181], v[60:63]
	v_mfma_f32_16x16x32_bf16 v[52:55], v[154:157], v[178:181], v[52:55]
	v_mfma_f32_16x16x32_bf16 v[44:47], v[146:149], v[198:201], v[44:47]
	v_mfma_f32_16x16x32_bf16 v[36:39], v[154:157], v[198:201], v[36:39]
	v_mfma_f32_16x16x32_bf16 v[28:31], v[146:149], v[206:209], v[28:31]
	v_mfma_f32_16x16x32_bf16 v[20:23], v[154:157], v[206:209], v[20:23]
	v_mfma_f32_16x16x32_bf16 v[12:15], v[146:149], v[228:231], v[12:15]
	v_mfma_f32_16x16x32_bf16 v[4:7], v[154:157], v[228:231], v[4:7]
	s_setprio 0
	s_setprio 1
	v_mfma_f32_16x16x32_bf16 v[56:59], v[158:161], v[174:177], v[56:59]
	v_mfma_f32_16x16x32_bf16 v[48:51], v[166:169], v[174:177], v[48:51]
	v_mfma_f32_16x16x32_bf16 v[40:43], v[158:161], v[194:197], v[40:43]
	v_mfma_f32_16x16x32_bf16 v[32:35], v[166:169], v[194:197], v[32:35]
	v_mfma_f32_16x16x32_bf16 v[24:27], v[158:161], v[202:205], v[24:27]
	v_mfma_f32_16x16x32_bf16 v[16:19], v[166:169], v[202:205], v[16:19]
	v_mfma_f32_16x16x32_bf16 v[8:11], v[158:161], v[224:227], v[8:11]
	v_mfma_f32_16x16x32_bf16 v[0:3], v[166:169], v[224:227], v[0:3]
	v_mfma_f32_16x16x32_bf16 v[56:59], v[162:165], v[178:181], v[56:59]
	v_mfma_f32_16x16x32_bf16 v[48:51], v[170:173], v[178:181], v[48:51]
	v_mfma_f32_16x16x32_bf16 v[40:43], v[162:165], v[198:201], v[40:43]
	v_mfma_f32_16x16x32_bf16 v[32:35], v[170:173], v[198:201], v[32:35]
	v_mfma_f32_16x16x32_bf16 v[24:27], v[162:165], v[206:209], v[24:27]
	v_mfma_f32_16x16x32_bf16 v[16:19], v[170:173], v[206:209], v[16:19]
	v_mfma_f32_16x16x32_bf16 v[8:11], v[162:165], v[228:231], v[8:11]
	v_mfma_f32_16x16x32_bf16 v[0:3], v[170:173], v[228:231], v[0:3]
	s_setprio 0
	s_barrier
	s_add_i32 s48, 0, 0x18000
	s_add_i32 s49, 0, 0x1c000
	v_add_u32_e32 v154, s48, v139
	v_add_u32_e32 v170, s49, v139
	ds_read_b128 v[142:145], v154
	ds_read_b128 v[146:149], v154 offset:1024
	ds_read_b128 v[150:153], v154 offset:2048
	ds_read_b128 v[154:157], v154 offset:3072
	ds_read_b128 v[158:161], v170
	ds_read_b128 v[162:165], v170 offset:1024
	ds_read_b128 v[166:169], v170 offset:2048
	ds_read_b128 v[170:173], v170 offset:3072
	s_add_u32 s28, s38, 0x80000
	s_addc_u32 s29, s39, 0
	s_mov_b32 m0, s26
	v_lshl_add_u64 v[232:233], s[28:29], 0, v[132:133]
	ds_read_b128 v[174:177], v141 offset:32768
	ds_read_b128 v[178:181], v141 offset:33792
	ds_read_b128 v[194:197], v141 offset:34816
	ds_read_b128 v[198:201], v141 offset:35840
	ds_read_b128 v[202:205], v141 offset:36864
	ds_read_b128 v[206:209], v141 offset:37888
	ds_read_b128 v[224:227], v141 offset:38912
	ds_read_b128 v[228:231], v141 offset:39936
	global_load_lds_dwordx4 v[232:233], off
	v_lshl_add_u64 v[232:233], s[28:29], 0, v[130:131]
	s_waitcnt vmcnt(7)
	s_waitcnt lgkmcnt(0)
	s_barrier
	s_setprio 1
	s_waitcnt lgkmcnt(0)
	v_mfma_f32_16x16x32_bf16 v[124:127], v[142:145], v[174:177], v[124:127]
	v_mfma_f32_16x16x32_bf16 v[116:119], v[150:153], v[174:177], v[116:119]
	s_mov_b32 m0, s27
	s_nop 0
	global_load_lds_dwordx4 v[232:233], off
	v_mfma_f32_16x16x32_bf16 v[108:111], v[142:145], v[194:197], v[108:111]
	v_mfma_f32_16x16x32_bf16 v[100:103], v[150:153], v[194:197], v[100:103]
	v_mfma_f32_16x16x32_bf16 v[92:95], v[142:145], v[202:205], v[92:95]
	v_mfma_f32_16x16x32_bf16 v[84:87], v[150:153], v[202:205], v[84:87]
	v_mfma_f32_16x16x32_bf16 v[76:79], v[142:145], v[224:227], v[76:79]
	v_mfma_f32_16x16x32_bf16 v[68:71], v[150:153], v[224:227], v[68:71]
	v_mfma_f32_16x16x32_bf16 v[124:127], v[146:149], v[178:181], v[124:127]
	v_mfma_f32_16x16x32_bf16 v[116:119], v[154:157], v[178:181], v[116:119]
	v_mfma_f32_16x16x32_bf16 v[108:111], v[146:149], v[198:201], v[108:111]
	v_mfma_f32_16x16x32_bf16 v[100:103], v[154:157], v[198:201], v[100:103]
	v_mfma_f32_16x16x32_bf16 v[92:95], v[146:149], v[206:209], v[92:95]
	v_mfma_f32_16x16x32_bf16 v[84:87], v[154:157], v[206:209], v[84:87]
	v_mfma_f32_16x16x32_bf16 v[76:79], v[146:149], v[228:231], v[76:79]
	v_mfma_f32_16x16x32_bf16 v[68:71], v[154:157], v[228:231], v[68:71]
	s_setprio 0
	s_setprio 1
	v_mfma_f32_16x16x32_bf16 v[120:123], v[158:161], v[174:177], v[120:123]
	v_mfma_f32_16x16x32_bf16 v[112:115], v[166:169], v[174:177], v[112:115]
	v_mfma_f32_16x16x32_bf16 v[104:107], v[158:161], v[194:197], v[104:107]
	v_mfma_f32_16x16x32_bf16 v[96:99], v[166:169], v[194:197], v[96:99]
	v_mfma_f32_16x16x32_bf16 v[88:91], v[158:161], v[202:205], v[88:91]
	v_mfma_f32_16x16x32_bf16 v[80:83], v[166:169], v[202:205], v[80:83]
	v_mfma_f32_16x16x32_bf16 v[72:75], v[158:161], v[224:227], v[72:75]
	v_mfma_f32_16x16x32_bf16 v[64:67], v[166:169], v[224:227], v[64:67]
	v_mfma_f32_16x16x32_bf16 v[120:123], v[162:165], v[178:181], v[120:123]
	v_mfma_f32_16x16x32_bf16 v[112:115], v[170:173], v[178:181], v[112:115]
	v_mfma_f32_16x16x32_bf16 v[104:107], v[162:165], v[198:201], v[104:107]
	v_mfma_f32_16x16x32_bf16 v[96:99], v[170:173], v[198:201], v[96:99]
	v_mfma_f32_16x16x32_bf16 v[88:91], v[162:165], v[206:209], v[88:91]
	v_mfma_f32_16x16x32_bf16 v[80:83], v[170:173], v[206:209], v[80:83]
	v_mfma_f32_16x16x32_bf16 v[72:75], v[162:165], v[228:231], v[72:75]
	v_mfma_f32_16x16x32_bf16 v[64:67], v[170:173], v[228:231], v[64:67]
	s_setprio 0
	s_barrier
	s_add_i32 s28, s48, s4
	v_lshl_add_u64 v[182:183], v[182:183], 0, s[68:69]
	s_mov_b32 m0, s28
	ds_read_b128 v[174:177], v141 offset:49152
	ds_read_b128 v[178:181], v141 offset:50176
	ds_read_b128 v[194:197], v141 offset:51200
	ds_read_b128 v[198:201], v141 offset:52224
	ds_read_b128 v[202:205], v141 offset:53248
	ds_read_b128 v[206:209], v141 offset:54272
	ds_read_b128 v[224:227], v141 offset:55296
	ds_read_b128 v[228:231], v141 offset:56320
	global_load_lds_dwordx4 v[182:183], off
	s_add_i32 m0, s28, 0x2000
	s_add_u32 s28, s30, 0x80080
	v_lshl_add_u64 v[182:183], v[210:211], 0, s[68:69]
	s_addc_u32 s29, s31, 0
	s_add_i32 s30, s49, s4
	global_load_lds_dwordx4 v[182:183], off
	v_lshl_add_u64 v[182:183], s[28:29], 0, v[184:185]
	s_mov_b32 m0, s30
	s_nop 0
	global_load_lds_dwordx4 v[182:183], off
	v_lshl_add_u64 v[182:183], s[28:29], 0, v[128:129]
	s_add_i32 m0, s30, 0x2000
	s_nop 0
	global_load_lds_dwordx4 v[182:183], off
	v_lshl_add_u64 v[182:183], v[216:217], 0, s[68:69]
	s_mov_b32 m0, s40
	s_nop 0
	global_load_lds_dwordx4 v[182:183], off
	v_lshl_add_u64 v[182:183], v[218:219], 0, s[68:69]
	s_waitcnt vmcnt(7)
	s_waitcnt lgkmcnt(0)
	s_barrier
	s_setprio 1
	s_waitcnt lgkmcnt(0)
	v_mfma_f32_16x16x32_bf16 v[60:63], v[142:145], v[174:177], v[60:63]
	v_mfma_f32_16x16x32_bf16 v[52:55], v[150:153], v[174:177], v[52:55]
	s_mov_b32 m0, s41
	s_nop 0
	global_load_lds_dwordx4 v[182:183], off
	v_mfma_f32_16x16x32_bf16 v[44:47], v[142:145], v[194:197], v[44:47]
	v_mfma_f32_16x16x32_bf16 v[36:39], v[150:153], v[194:197], v[36:39]
	v_mfma_f32_16x16x32_bf16 v[28:31], v[142:145], v[202:205], v[28:31]
	v_mfma_f32_16x16x32_bf16 v[20:23], v[150:153], v[202:205], v[20:23]
	v_mfma_f32_16x16x32_bf16 v[12:15], v[142:145], v[224:227], v[12:15]
	v_mfma_f32_16x16x32_bf16 v[4:7], v[150:153], v[224:227], v[4:7]
	v_mfma_f32_16x16x32_bf16 v[60:63], v[146:149], v[178:181], v[60:63]
	v_mfma_f32_16x16x32_bf16 v[52:55], v[154:157], v[178:181], v[52:55]
	v_mfma_f32_16x16x32_bf16 v[44:47], v[146:149], v[198:201], v[44:47]
	v_mfma_f32_16x16x32_bf16 v[36:39], v[154:157], v[198:201], v[36:39]
	v_mfma_f32_16x16x32_bf16 v[28:31], v[146:149], v[206:209], v[28:31]
	v_mfma_f32_16x16x32_bf16 v[20:23], v[154:157], v[206:209], v[20:23]
	v_mfma_f32_16x16x32_bf16 v[12:15], v[146:149], v[228:231], v[12:15]
	v_mfma_f32_16x16x32_bf16 v[4:7], v[154:157], v[228:231], v[4:7]
	s_setprio 0
	s_setprio 1
	v_mfma_f32_16x16x32_bf16 v[56:59], v[158:161], v[174:177], v[56:59]
	v_mfma_f32_16x16x32_bf16 v[48:51], v[166:169], v[174:177], v[48:51]
	v_mfma_f32_16x16x32_bf16 v[40:43], v[158:161], v[194:197], v[40:43]
	v_mfma_f32_16x16x32_bf16 v[32:35], v[166:169], v[194:197], v[32:35]
	v_mfma_f32_16x16x32_bf16 v[24:27], v[158:161], v[202:205], v[24:27]
	v_mfma_f32_16x16x32_bf16 v[16:19], v[166:169], v[202:205], v[16:19]
	v_mfma_f32_16x16x32_bf16 v[8:11], v[158:161], v[224:227], v[8:11]
	v_mfma_f32_16x16x32_bf16 v[0:3], v[166:169], v[224:227], v[0:3]
	v_mfma_f32_16x16x32_bf16 v[56:59], v[162:165], v[178:181], v[56:59]
	v_mfma_f32_16x16x32_bf16 v[48:51], v[170:173], v[178:181], v[48:51]
	v_mfma_f32_16x16x32_bf16 v[40:43], v[162:165], v[198:201], v[40:43]
	v_mfma_f32_16x16x32_bf16 v[32:35], v[170:173], v[198:201], v[32:35]
	v_mfma_f32_16x16x32_bf16 v[24:27], v[162:165], v[206:209], v[24:27]
	v_mfma_f32_16x16x32_bf16 v[16:19], v[170:173], v[206:209], v[16:19]
	v_mfma_f32_16x16x32_bf16 v[8:11], v[162:165], v[228:231], v[8:11]
	v_mfma_f32_16x16x32_bf16 v[0:3], v[170:173], v[228:231], v[0:3]
	s_setprio 0
	s_barrier
	s_add_i32 s51, s51, 2
	s_add_u32 s24, s24, 0x100
	s_addc_u32 s25, s25, 0
	s_add_u32 s47, s47, 0x100
	s_addc_u32 s50, s50, 0
	s_cmp_gt_u32 s51, 29
	s_cbranch_scc0 .LBB0_1587
	s_and_b64 vcc, exec, s[6:7]
	s_cbranch_vccz .LBB0_1590
	s_barrier

.LBB0_1661:
	s_add_u32 s24, s18, 0x100
	s_addc_u32 s25, s19, 0
	s_add_i32 s28, 0, 0x10000
	s_cmpk_eq_i32 s61, 0x54
	s_cselect_b32 s39, s51, s25
	s_cselect_b32 s38, s52, s24
	s_cselect_b32 s31, s53, s60
	s_cselect_b32 s30, s58, s59
	s_add_i32 s29, 0, 0x14000
	s_waitcnt vmcnt(0)
	v_add_u32_e32 v84, s28, v163
	v_add_u32_e32 v170, s29, v163
	ds_read_b128 v[64:67], v84
	ds_read_b128 v[68:71], v84 offset:1024
	ds_read_b128 v[80:83], v84 offset:2048
	ds_read_b128 v[84:87], v84 offset:3072
	ds_read_b128 v[154:157], v170
	ds_read_b128 v[158:161], v170 offset:1024
	ds_read_b128 v[166:169], v170 offset:2048
	ds_read_b128 v[170:173], v170 offset:3072
	v_lshl_add_u64 v[182:183], s[18:19], 0, v[150:151]
	s_add_i32 m0, s20, 0xc000
	ds_read_b128 v[174:177], v165
	ds_read_b128 v[178:181], v165 offset:1024
	ds_read_b128 v[194:197], v165 offset:2048
	ds_read_b128 v[198:201], v165 offset:3072
	ds_read_b128 v[202:205], v165 offset:4096
	ds_read_b128 v[206:209], v165 offset:5120
	ds_read_b128 v[224:227], v165 offset:6144
	ds_read_b128 v[228:231], v165 offset:7168
	global_load_lds_dwordx4 v[182:183], off
	v_lshl_add_u64 v[182:183], s[18:19], 0, v[152:153]
	s_waitcnt vmcnt(7)
	s_waitcnt lgkmcnt(0)
	s_barrier
	s_setprio 1
	s_waitcnt lgkmcnt(0)
	v_mfma_f32_16x16x32_bf16 v[140:143], v[64:67], v[174:177], v[140:143]
	v_mfma_f32_16x16x32_bf16 v[136:139], v[80:83], v[174:177], v[136:139]
	s_add_i32 m0, s20, 0xe000
	s_nop 0
	global_load_lds_dwordx4 v[182:183], off
	v_mfma_f32_16x16x32_bf16 v[124:127], v[64:67], v[194:197], v[124:127]
	v_mfma_f32_16x16x32_bf16 v[120:123], v[80:83], v[194:197], v[120:123]
	v_mfma_f32_16x16x32_bf16 v[108:111], v[64:67], v[202:205], v[108:111]
	v_mfma_f32_16x16x32_bf16 v[104:107], v[80:83], v[202:205], v[104:107]
	v_mfma_f32_16x16x32_bf16 v[92:95], v[64:67], v[224:227], v[92:95]
	v_mfma_f32_16x16x32_bf16 v[88:91], v[80:83], v[224:227], v[88:91]
	v_mfma_f32_16x16x32_bf16 v[140:143], v[68:71], v[178:181], v[140:143]
	v_mfma_f32_16x16x32_bf16 v[136:139], v[84:87], v[178:181], v[136:139]
	v_mfma_f32_16x16x32_bf16 v[124:127], v[68:71], v[198:201], v[124:127]
	v_mfma_f32_16x16x32_bf16 v[120:123], v[84:87], v[198:201], v[120:123]
	v_mfma_f32_16x16x32_bf16 v[108:111], v[68:71], v[206:209], v[108:111]
	v_mfma_f32_16x16x32_bf16 v[104:107], v[84:87], v[206:209], v[104:107]
	v_mfma_f32_16x16x32_bf16 v[92:95], v[68:71], v[228:231], v[92:95]
	v_mfma_f32_16x16x32_bf16 v[88:91], v[84:87], v[228:231], v[88:91]
	s_setprio 0
	s_setprio 1
	v_mfma_f32_16x16x32_bf16 v[132:135], v[154:157], v[174:177], v[132:135]
	v_mfma_f32_16x16x32_bf16 v[128:131], v[166:169], v[174:177], v[128:131]
	v_mfma_f32_16x16x32_bf16 v[116:119], v[154:157], v[194:197], v[116:119]
	v_mfma_f32_16x16x32_bf16 v[112:115], v[166:169], v[194:197], v[112:115]
	v_mfma_f32_16x16x32_bf16 v[100:103], v[154:157], v[202:205], v[100:103]
	v_mfma_f32_16x16x32_bf16 v[96:99], v[166:169], v[202:205], v[96:99]
	v_mfma_f32_16x16x32_bf16 v[76:79], v[154:157], v[224:227], v[76:79]
	v_mfma_f32_16x16x32_bf16 v[72:75], v[166:169], v[224:227], v[72:75]
	v_mfma_f32_16x16x32_bf16 v[132:135], v[158:161], v[178:181], v[132:135]
	v_mfma_f32_16x16x32_bf16 v[128:131], v[170:173], v[178:181], v[128:131]
	v_mfma_f32_16x16x32_bf16 v[116:119], v[158:161], v[198:201], v[116:119]
	v_mfma_f32_16x16x32_bf16 v[112:115], v[170:173], v[198:201], v[112:115]
	v_mfma_f32_16x16x32_bf16 v[100:103], v[158:161], v[206:209], v[100:103]
	v_mfma_f32_16x16x32_bf16 v[96:99], v[170:173], v[206:209], v[96:99]
	v_mfma_f32_16x16x32_bf16 v[76:79], v[158:161], v[228:231], v[76:79]
	v_mfma_f32_16x16x32_bf16 v[72:75], v[170:173], v[228:231], v[72:75]
	s_setprio 0
	s_barrier
	s_add_i32 s18, s28, s4
	v_lshl_add_u64 v[182:183], s[30:31], 0, v[184:185]
	s_mov_b32 m0, s18
	ds_read_b128 v[174:177], v165 offset:16384
	ds_read_b128 v[178:181], v165 offset:17408
	ds_read_b128 v[194:197], v165 offset:18432
	ds_read_b128 v[198:201], v165 offset:19456
	ds_read_b128 v[202:205], v165 offset:20480
	ds_read_b128 v[206:209], v165 offset:21504
	ds_read_b128 v[224:227], v165 offset:22528
	ds_read_b128 v[228:231], v165 offset:23552
	global_load_lds_dwordx4 v[182:183], off
	s_add_i32 m0, s18, 0x2000
	s_add_u32 s18, s30, 0x160000
	v_lshl_add_u64 v[210:211], s[30:31], 0, v[144:145]
	s_addc_u32 s19, s31, 0
	s_add_i32 s28, s29, s4
	global_load_lds_dwordx4 v[210:211], off
	v_lshl_add_u64 v[216:217], s[18:19], 0, v[184:185]
	s_mov_b32 m0, s28
	v_lshl_add_u64 v[218:219], s[38:39], 0, v[146:147]
	global_load_lds_dwordx4 v[216:217], off
	v_lshl_add_u64 v[216:217], s[18:19], 0, v[144:145]
	s_add_i32 m0, s28, 0x2000
	s_nop 0
	global_load_lds_dwordx4 v[216:217], off
	v_lshl_add_u64 v[216:217], s[38:39], 0, v[148:149]
	s_mov_b32 m0, s20
	s_nop 0
	global_load_lds_dwordx4 v[216:217], off
	s_waitcnt vmcnt(7)
	s_waitcnt lgkmcnt(0)
	s_barrier
	s_setprio 1
	s_waitcnt lgkmcnt(0)
	v_mfma_f32_16x16x32_bf16 v[60:63], v[64:67], v[174:177], v[60:63]
	v_mfma_f32_16x16x32_bf16 v[56:59], v[80:83], v[174:177], v[56:59]
	s_mov_b32 m0, s21
	s_nop 0
	global_load_lds_dwordx4 v[218:219], off
	v_mfma_f32_16x16x32_bf16 v[44:47], v[64:67], v[194:197], v[44:47]
	v_mfma_f32_16x16x32_bf16 v[40:43], v[80:83], v[194:197], v[40:43]
	v_mfma_f32_16x16x32_bf16 v[28:31], v[64:67], v[202:205], v[28:31]
	v_mfma_f32_16x16x32_bf16 v[24:27], v[80:83], v[202:205], v[24:27]
	v_mfma_f32_16x16x32_bf16 v[12:15], v[64:67], v[224:227], v[12:15]
	v_mfma_f32_16x16x32_bf16 v[8:11], v[80:83], v[224:227], v[8:11]
	v_mfma_f32_16x16x32_bf16 v[60:63], v[68:71], v[178:181], v[60:63]
	v_mfma_f32_16x16x32_bf16 v[56:59], v[84:87], v[178:181], v[56:59]
	v_mfma_f32_16x16x32_bf16 v[44:47], v[68:71], v[198:201], v[44:47]
	v_mfma_f32_16x16x32_bf16 v[40:43], v[84:87], v[198:201], v[40:43]
	v_mfma_f32_16x16x32_bf16 v[28:31], v[68:71], v[206:209], v[28:31]
	v_mfma_f32_16x16x32_bf16 v[24:27], v[84:87], v[206:209], v[24:27]
	v_mfma_f32_16x16x32_bf16 v[12:15], v[68:71], v[228:231], v[12:15]
	v_mfma_f32_16x16x32_bf16 v[8:11], v[84:87], v[228:231], v[8:11]
	s_setprio 0
	s_setprio 1
	v_mfma_f32_16x16x32_bf16 v[52:55], v[154:157], v[174:177], v[52:55]
	v_mfma_f32_16x16x32_bf16 v[48:51], v[166:169], v[174:177], v[48:51]
	v_mfma_f32_16x16x32_bf16 v[36:39], v[154:157], v[194:197], v[36:39]
	v_mfma_f32_16x16x32_bf16 v[32:35], v[166:169], v[194:197], v[32:35]
	v_mfma_f32_16x16x32_bf16 v[20:23], v[154:157], v[202:205], v[20:23]
	v_mfma_f32_16x16x32_bf16 v[16:19], v[166:169], v[202:205], v[16:19]
	v_mfma_f32_16x16x32_bf16 v[4:7], v[154:157], v[224:227], v[4:7]
	v_mfma_f32_16x16x32_bf16 v[0:3], v[166:169], v[224:227], v[0:3]
	v_mfma_f32_16x16x32_bf16 v[52:55], v[158:161], v[178:181], v[52:55]
	v_mfma_f32_16x16x32_bf16 v[48:51], v[170:173], v[178:181], v[48:51]
	v_mfma_f32_16x16x32_bf16 v[36:39], v[158:161], v[198:201], v[36:39]
	v_mfma_f32_16x16x32_bf16 v[32:35], v[170:173], v[198:201], v[32:35]
	v_mfma_f32_16x16x32_bf16 v[20:23], v[158:161], v[206:209], v[20:23]
	v_mfma_f32_16x16x32_bf16 v[16:19], v[170:173], v[206:209], v[16:19]
	v_mfma_f32_16x16x32_bf16 v[4:7], v[158:161], v[228:231], v[4:7]
	v_mfma_f32_16x16x32_bf16 v[0:3], v[170:173], v[228:231], v[0:3]
	s_setprio 0
	s_barrier
	s_add_i32 s28, 0, 0x18000
	s_add_i32 s29, 0, 0x1c000
	v_add_u32_e32 v84, s28, v163
	v_add_u32_e32 v170, s29, v163
	ds_read_b128 v[64:67], v84
	ds_read_b128 v[68:71], v84 offset:1024
	ds_read_b128 v[80:83], v84 offset:2048
	ds_read_b128 v[84:87], v84 offset:3072
	ds_read_b128 v[154:157], v170
	ds_read_b128 v[158:161], v170 offset:1024
	ds_read_b128 v[166:169], v170 offset:2048
	ds_read_b128 v[170:173], v170 offset:3072
	s_add_u32 s18, s38, 0x160000
	s_addc_u32 s19, s39, 0
	s_mov_b32 m0, s26
	v_lshl_add_u64 v[232:233], s[18:19], 0, v[148:149]
	ds_read_b128 v[174:177], v165 offset:32768
	ds_read_b128 v[178:181], v165 offset:33792
	ds_read_b128 v[194:197], v165 offset:34816
	ds_read_b128 v[198:201], v165 offset:35840
	ds_read_b128 v[202:205], v165 offset:36864
	ds_read_b128 v[206:209], v165 offset:37888
	ds_read_b128 v[224:227], v165 offset:38912
	ds_read_b128 v[228:231], v165 offset:39936
	global_load_lds_dwordx4 v[232:233], off
	v_lshl_add_u64 v[232:233], s[18:19], 0, v[146:147]
	s_waitcnt vmcnt(7)
	s_waitcnt lgkmcnt(0)
	s_barrier
	s_setprio 1
	s_waitcnt lgkmcnt(0)
	v_mfma_f32_16x16x32_bf16 v[140:143], v[64:67], v[174:177], v[140:143]
	v_mfma_f32_16x16x32_bf16 v[136:139], v[80:83], v[174:177], v[136:139]
	s_mov_b32 m0, s27
	s_nop 0
	global_load_lds_dwordx4 v[232:233], off
	v_mfma_f32_16x16x32_bf16 v[124:127], v[64:67], v[194:197], v[124:127]
	v_mfma_f32_16x16x32_bf16 v[120:123], v[80:83], v[194:197], v[120:123]
	v_mfma_f32_16x16x32_bf16 v[108:111], v[64:67], v[202:205], v[108:111]
	v_mfma_f32_16x16x32_bf16 v[104:107], v[80:83], v[202:205], v[104:107]
	v_mfma_f32_16x16x32_bf16 v[92:95], v[64:67], v[224:227], v[92:95]
	v_mfma_f32_16x16x32_bf16 v[88:91], v[80:83], v[224:227], v[88:91]
	v_mfma_f32_16x16x32_bf16 v[140:143], v[68:71], v[178:181], v[140:143]
	v_mfma_f32_16x16x32_bf16 v[136:139], v[84:87], v[178:181], v[136:139]
	v_mfma_f32_16x16x32_bf16 v[124:127], v[68:71], v[198:201], v[124:127]
	v_mfma_f32_16x16x32_bf16 v[120:123], v[84:87], v[198:201], v[120:123]
	v_mfma_f32_16x16x32_bf16 v[108:111], v[68:71], v[206:209], v[108:111]
	v_mfma_f32_16x16x32_bf16 v[104:107], v[84:87], v[206:209], v[104:107]
	v_mfma_f32_16x16x32_bf16 v[92:95], v[68:71], v[228:231], v[92:95]
	v_mfma_f32_16x16x32_bf16 v[88:91], v[84:87], v[228:231], v[88:91]
	s_setprio 0
	s_setprio 1
	v_mfma_f32_16x16x32_bf16 v[132:135], v[154:157], v[174:177], v[132:135]
	v_mfma_f32_16x16x32_bf16 v[128:131], v[166:169], v[174:177], v[128:131]
	v_mfma_f32_16x16x32_bf16 v[116:119], v[154:157], v[194:197], v[116:119]
	v_mfma_f32_16x16x32_bf16 v[112:115], v[166:169], v[194:197], v[112:115]
	v_mfma_f32_16x16x32_bf16 v[100:103], v[154:157], v[202:205], v[100:103]
	v_mfma_f32_16x16x32_bf16 v[96:99], v[166:169], v[202:205], v[96:99]
	v_mfma_f32_16x16x32_bf16 v[76:79], v[154:157], v[224:227], v[76:79]
	v_mfma_f32_16x16x32_bf16 v[72:75], v[166:169], v[224:227], v[72:75]
	v_mfma_f32_16x16x32_bf16 v[132:135], v[158:161], v[178:181], v[132:135]
	v_mfma_f32_16x16x32_bf16 v[128:131], v[170:173], v[178:181], v[128:131]
	v_mfma_f32_16x16x32_bf16 v[116:119], v[158:161], v[198:201], v[116:119]
	v_mfma_f32_16x16x32_bf16 v[112:115], v[170:173], v[198:201], v[112:115]
	v_mfma_f32_16x16x32_bf16 v[100:103], v[158:161], v[206:209], v[100:103]
	v_mfma_f32_16x16x32_bf16 v[96:99], v[170:173], v[206:209], v[96:99]
	v_mfma_f32_16x16x32_bf16 v[76:79], v[158:161], v[228:231], v[76:79]
	v_mfma_f32_16x16x32_bf16 v[72:75], v[170:173], v[228:231], v[72:75]
	s_setprio 0
	s_barrier
	s_add_i32 s18, s28, s4
	v_lshl_add_u64 v[182:183], v[182:183], 0, s[68:69]
	s_mov_b32 m0, s18
	ds_read_b128 v[174:177], v165 offset:49152
	ds_read_b128 v[178:181], v165 offset:50176
	ds_read_b128 v[194:197], v165 offset:51200
	ds_read_b128 v[198:201], v165 offset:52224
	ds_read_b128 v[202:205], v165 offset:53248
	ds_read_b128 v[206:209], v165 offset:54272
	ds_read_b128 v[224:227], v165 offset:55296
	ds_read_b128 v[228:231], v165 offset:56320
	global_load_lds_dwordx4 v[182:183], off
	s_add_i32 m0, s18, 0x2000
	s_add_u32 s18, s30, 0x160080
	v_lshl_add_u64 v[182:183], v[210:211], 0, s[68:69]
	s_addc_u32 s19, s31, 0
	s_add_i32 s28, s29, s4
	global_load_lds_dwordx4 v[182:183], off
	v_lshl_add_u64 v[182:183], s[18:19], 0, v[184:185]
	s_mov_b32 m0, s28
	s_nop 0
	global_load_lds_dwordx4 v[182:183], off
	v_lshl_add_u64 v[182:183], s[18:19], 0, v[144:145]
	s_add_i32 m0, s28, 0x2000
	s_nop 0
	global_load_lds_dwordx4 v[182:183], off
	v_lshl_add_u64 v[182:183], v[216:217], 0, s[68:69]
	s_mov_b32 m0, s42
	s_nop 0
	global_load_lds_dwordx4 v[182:183], off
	v_lshl_add_u64 v[182:183], v[218:219], 0, s[68:69]
	s_waitcnt vmcnt(7)
	s_waitcnt lgkmcnt(0)
	s_barrier
	s_setprio 1
	s_waitcnt lgkmcnt(0)
	v_mfma_f32_16x16x32_bf16 v[60:63], v[64:67], v[174:177], v[60:63]
	v_mfma_f32_16x16x32_bf16 v[56:59], v[80:83], v[174:177], v[56:59]
	s_mov_b32 m0, s43
	s_nop 0
	global_load_lds_dwordx4 v[182:183], off
	v_mfma_f32_16x16x32_bf16 v[44:47], v[64:67], v[194:197], v[44:47]
	v_mfma_f32_16x16x32_bf16 v[40:43], v[80:83], v[194:197], v[40:43]
	v_mfma_f32_16x16x32_bf16 v[28:31], v[64:67], v[202:205], v[28:31]
	v_mfma_f32_16x16x32_bf16 v[24:27], v[80:83], v[202:205], v[24:27]
	v_mfma_f32_16x16x32_bf16 v[12:15], v[64:67], v[224:227], v[12:15]
	v_mfma_f32_16x16x32_bf16 v[8:11], v[80:83], v[224:227], v[8:11]
	v_mfma_f32_16x16x32_bf16 v[60:63], v[68:71], v[178:181], v[60:63]
	v_mfma_f32_16x16x32_bf16 v[56:59], v[84:87], v[178:181], v[56:59]
	v_mfma_f32_16x16x32_bf16 v[44:47], v[68:71], v[198:201], v[44:47]
	v_mfma_f32_16x16x32_bf16 v[40:43], v[84:87], v[198:201], v[40:43]
	v_mfma_f32_16x16x32_bf16 v[28:31], v[68:71], v[206:209], v[28:31]
	v_mfma_f32_16x16x32_bf16 v[24:27], v[84:87], v[206:209], v[24:27]
	v_mfma_f32_16x16x32_bf16 v[12:15], v[68:71], v[228:231], v[12:15]
	v_mfma_f32_16x16x32_bf16 v[8:11], v[84:87], v[228:231], v[8:11]
	s_setprio 0
	s_setprio 1
	v_mfma_f32_16x16x32_bf16 v[52:55], v[154:157], v[174:177], v[52:55]
	v_mfma_f32_16x16x32_bf16 v[48:51], v[166:169], v[174:177], v[48:51]
	v_mfma_f32_16x16x32_bf16 v[36:39], v[154:157], v[194:197], v[36:39]
	v_mfma_f32_16x16x32_bf16 v[32:35], v[166:169], v[194:197], v[32:35]
	v_mfma_f32_16x16x32_bf16 v[20:23], v[154:157], v[202:205], v[20:23]
	v_mfma_f32_16x16x32_bf16 v[16:19], v[166:169], v[202:205], v[16:19]
	v_mfma_f32_16x16x32_bf16 v[4:7], v[154:157], v[224:227], v[4:7]
	v_mfma_f32_16x16x32_bf16 v[0:3], v[166:169], v[224:227], v[0:3]
	v_mfma_f32_16x16x32_bf16 v[52:55], v[158:161], v[178:181], v[52:55]
	v_mfma_f32_16x16x32_bf16 v[48:51], v[170:173], v[178:181], v[48:51]
	v_mfma_f32_16x16x32_bf16 v[36:39], v[158:161], v[198:201], v[36:39]
	v_mfma_f32_16x16x32_bf16 v[32:35], v[170:173], v[198:201], v[32:35]
	v_mfma_f32_16x16x32_bf16 v[20:23], v[158:161], v[206:209], v[20:23]
	v_mfma_f32_16x16x32_bf16 v[16:19], v[170:173], v[206:209], v[16:19]
	v_mfma_f32_16x16x32_bf16 v[4:7], v[158:161], v[228:231], v[4:7]
	v_mfma_f32_16x16x32_bf16 v[0:3], v[170:173], v[228:231], v[0:3]
	s_setprio 0
	s_barrier
	s_add_i32 s61, s61, 2
	s_add_u32 s59, s59, 0x100
	s_addc_u32 s60, s60, 0
	s_cmpk_gt_u32 s61, 0x55
	s_mov_b64 s[18:19], s[24:25]
	s_cbranch_scc0 .LBB0_1661
	s_and_b64 vcc, exec, s[8:9]
	s_cbranch_vccz .LBB0_1664
	s_barrier

.LBB0_1741:
	s_add_u32 s38, s36, 0x100
	s_addc_u32 s39, s37, 0
	s_add_i32 s28, 0, 0x10000
	s_cmp_eq_u32 s59, 4
	s_cselect_b32 s43, s11, s39
	s_cselect_b32 s42, s50, s38
	s_cselect_b32 s41, s51, s58
	s_cselect_b32 s40, s52, s53
	s_add_i32 s48, 0, 0x14000
	v_add_u32_e32 v124, s28, v172
	v_add_u32_e32 v170, s48, v172
	ds_read_b128 v[112:115], v124
	ds_read_b128 v[116:119], v124 offset:1024
	ds_read_b128 v[120:123], v124 offset:2048
	ds_read_b128 v[124:127], v124 offset:3072
	ds_read_b128 v[176:179], v170
	ds_read_b128 v[180:183], v170 offset:1024
	ds_read_b128 v[194:197], v170 offset:2048
	ds_read_b128 v[198:201], v170 offset:3072
	v_lshl_add_u64 v[170:171], s[36:37], 0, v[166:167]
	s_add_i32 m0, s20, 0xc000
	ds_read_b128 v[202:205], v174
	ds_read_b128 v[206:209], v174 offset:1024
	ds_read_b128 v[224:227], v174 offset:2048
	ds_read_b128 v[228:231], v174 offset:3072
	ds_read_b128 v[232:235], v174 offset:4096
	ds_read_b128 v[236:239], v174 offset:5120
	ds_read_b128 v[240:243], v174 offset:6144
	ds_read_b128 v[244:247], v174 offset:7168
	global_load_lds_dwordx4 v[170:171], off
	v_lshl_add_u64 v[170:171], s[36:37], 0, v[168:169]
	s_waitcnt vmcnt(7)
	s_waitcnt lgkmcnt(0)
	s_barrier
	s_setprio 1
	s_waitcnt lgkmcnt(0)
	v_mfma_f32_16x16x32_bf16 v[140:143], v[112:115], v[202:205], v[140:143]
	v_mfma_f32_16x16x32_bf16 v[136:139], v[120:123], v[202:205], v[136:139]
	s_add_i32 m0, s20, 0xe000
	s_nop 0
	global_load_lds_dwordx4 v[170:171], off
	v_mfma_f32_16x16x32_bf16 v[108:111], v[112:115], v[224:227], v[108:111]
	v_mfma_f32_16x16x32_bf16 v[104:107], v[120:123], v[224:227], v[104:107]
	v_mfma_f32_16x16x32_bf16 v[92:95], v[112:115], v[232:235], v[92:95]
	v_mfma_f32_16x16x32_bf16 v[88:91], v[120:123], v[232:235], v[88:91]
	v_mfma_f32_16x16x32_bf16 v[76:79], v[112:115], v[240:243], v[76:79]
	v_mfma_f32_16x16x32_bf16 v[72:75], v[120:123], v[240:243], v[72:75]
	v_mfma_f32_16x16x32_bf16 v[140:143], v[116:119], v[206:209], v[140:143]
	v_mfma_f32_16x16x32_bf16 v[136:139], v[124:127], v[206:209], v[136:139]
	v_mfma_f32_16x16x32_bf16 v[108:111], v[116:119], v[228:231], v[108:111]
	v_mfma_f32_16x16x32_bf16 v[104:107], v[124:127], v[228:231], v[104:107]
	v_mfma_f32_16x16x32_bf16 v[92:95], v[116:119], v[236:239], v[92:95]
	v_mfma_f32_16x16x32_bf16 v[88:91], v[124:127], v[236:239], v[88:91]
	v_mfma_f32_16x16x32_bf16 v[76:79], v[116:119], v[244:247], v[76:79]
	v_mfma_f32_16x16x32_bf16 v[72:75], v[124:127], v[244:247], v[72:75]
	s_setprio 0
	s_setprio 1
	v_mfma_f32_16x16x32_bf16 v[132:135], v[176:179], v[202:205], v[132:135]
	v_mfma_f32_16x16x32_bf16 v[128:131], v[194:197], v[202:205], v[128:131]
	v_mfma_f32_16x16x32_bf16 v[100:103], v[176:179], v[224:227], v[100:103]
	v_mfma_f32_16x16x32_bf16 v[96:99], v[194:197], v[224:227], v[96:99]
	v_mfma_f32_16x16x32_bf16 v[84:87], v[176:179], v[232:235], v[84:87]
	v_mfma_f32_16x16x32_bf16 v[80:83], v[194:197], v[232:235], v[80:83]
	v_mfma_f32_16x16x32_bf16 v[68:71], v[176:179], v[240:243], v[68:71]
	v_mfma_f32_16x16x32_bf16 v[64:67], v[194:197], v[240:243], v[64:67]
	v_mfma_f32_16x16x32_bf16 v[132:135], v[180:183], v[206:209], v[132:135]
	v_mfma_f32_16x16x32_bf16 v[128:131], v[198:201], v[206:209], v[128:131]
	v_mfma_f32_16x16x32_bf16 v[100:103], v[180:183], v[228:231], v[100:103]
	v_mfma_f32_16x16x32_bf16 v[96:99], v[198:201], v[228:231], v[96:99]
	v_mfma_f32_16x16x32_bf16 v[84:87], v[180:183], v[236:239], v[84:87]
	v_mfma_f32_16x16x32_bf16 v[80:83], v[198:201], v[236:239], v[80:83]
	v_mfma_f32_16x16x32_bf16 v[68:71], v[180:183], v[244:247], v[68:71]
	v_mfma_f32_16x16x32_bf16 v[64:67], v[198:201], v[244:247], v[64:67]
	s_setprio 0
	s_barrier
	s_add_i32 s28, s28, s4
	v_lshl_add_u64 v[170:171], s[40:41], 0, v[184:185]
	s_mov_b32 m0, s28
	ds_read_b128 v[202:205], v174 offset:16384
	ds_read_b128 v[206:209], v174 offset:17408
	ds_read_b128 v[224:227], v174 offset:18432
	ds_read_b128 v[228:231], v174 offset:19456
	ds_read_b128 v[232:235], v174 offset:20480
	ds_read_b128 v[236:239], v174 offset:21504
	ds_read_b128 v[240:243], v174 offset:22528
	ds_read_b128 v[244:247], v174 offset:23552
	global_load_lds_dwordx4 v[170:171], off
	s_add_i32 m0, s28, 0x2000
	s_add_u32 s28, s40, 0x160000
	v_lshl_add_u64 v[210:211], s[40:41], 0, v[144:145]
	s_addc_u32 s29, s41, 0
	s_add_i32 s36, s48, s4
	global_load_lds_dwordx4 v[210:211], off
	v_lshl_add_u64 v[216:217], s[28:29], 0, v[184:185]
	s_mov_b32 m0, s36
	v_lshl_add_u64 v[218:219], s[42:43], 0, v[146:147]
	global_load_lds_dwordx4 v[216:217], off
	v_lshl_add_u64 v[216:217], s[28:29], 0, v[144:145]
	s_add_i32 m0, s36, 0x2000
	s_nop 0
	global_load_lds_dwordx4 v[216:217], off
	v_lshl_add_u64 v[216:217], s[42:43], 0, v[148:149]
	s_mov_b32 m0, s20
	s_nop 0
	global_load_lds_dwordx4 v[216:217], off
	s_waitcnt vmcnt(7)
	s_waitcnt lgkmcnt(0)
	s_barrier
	s_setprio 1
	s_waitcnt lgkmcnt(0)
	v_mfma_f32_16x16x32_bf16 v[60:63], v[112:115], v[202:205], v[60:63]
	v_mfma_f32_16x16x32_bf16 v[56:59], v[120:123], v[202:205], v[56:59]
	s_mov_b32 m0, s21
	s_nop 0
	global_load_lds_dwordx4 v[218:219], off
	v_mfma_f32_16x16x32_bf16 v[44:47], v[112:115], v[224:227], v[44:47]
	v_mfma_f32_16x16x32_bf16 v[40:43], v[120:123], v[224:227], v[40:43]
	v_mfma_f32_16x16x32_bf16 v[36:39], v[112:115], v[232:235], v[36:39]
	v_mfma_f32_16x16x32_bf16 v[28:31], v[120:123], v[232:235], v[28:31]
	v_mfma_f32_16x16x32_bf16 v[20:23], v[112:115], v[240:243], v[20:23]
	v_mfma_f32_16x16x32_bf16 v[12:15], v[120:123], v[240:243], v[12:15]
	v_mfma_f32_16x16x32_bf16 v[60:63], v[116:119], v[206:209], v[60:63]
	v_mfma_f32_16x16x32_bf16 v[56:59], v[124:127], v[206:209], v[56:59]
	v_mfma_f32_16x16x32_bf16 v[44:47], v[116:119], v[228:231], v[44:47]
	v_mfma_f32_16x16x32_bf16 v[40:43], v[124:127], v[228:231], v[40:43]
	v_mfma_f32_16x16x32_bf16 v[36:39], v[116:119], v[236:239], v[36:39]
	v_mfma_f32_16x16x32_bf16 v[28:31], v[124:127], v[236:239], v[28:31]
	v_mfma_f32_16x16x32_bf16 v[20:23], v[116:119], v[244:247], v[20:23]
	v_mfma_f32_16x16x32_bf16 v[12:15], v[124:127], v[244:247], v[12:15]
	s_setprio 0
	s_setprio 1
	v_mfma_f32_16x16x32_bf16 v[52:55], v[176:179], v[202:205], v[52:55]
	v_mfma_f32_16x16x32_bf16 v[48:51], v[194:197], v[202:205], v[48:51]
	v_mfma_f32_16x16x32_bf16 v[32:35], v[176:179], v[224:227], v[32:35]
	v_mfma_f32_16x16x32_bf16 v[24:27], v[194:197], v[224:227], v[24:27]
	v_mfma_f32_16x16x32_bf16 v[16:19], v[176:179], v[232:235], v[16:19]
	v_mfma_f32_16x16x32_bf16 v[8:11], v[194:197], v[232:235], v[8:11]
	v_mfma_f32_16x16x32_bf16 v[4:7], v[176:179], v[240:243], v[4:7]
	v_mfma_f32_16x16x32_bf16 v[0:3], v[194:197], v[240:243], v[0:3]
	v_mfma_f32_16x16x32_bf16 v[52:55], v[180:183], v[206:209], v[52:55]
	v_mfma_f32_16x16x32_bf16 v[48:51], v[198:201], v[206:209], v[48:51]
	v_mfma_f32_16x16x32_bf16 v[32:35], v[180:183], v[228:231], v[32:35]
	v_mfma_f32_16x16x32_bf16 v[24:27], v[198:201], v[228:231], v[24:27]
	v_mfma_f32_16x16x32_bf16 v[16:19], v[180:183], v[236:239], v[16:19]
	v_mfma_f32_16x16x32_bf16 v[8:11], v[198:201], v[236:239], v[8:11]
	v_mfma_f32_16x16x32_bf16 v[4:7], v[180:183], v[244:247], v[4:7]
	v_mfma_f32_16x16x32_bf16 v[0:3], v[198:201], v[244:247], v[0:3]
	s_setprio 0
	s_barrier
	s_add_i32 s36, 0, 0x18000
	s_add_i32 s37, 0, 0x1c000
	v_add_u32_e32 v124, s36, v172
	v_add_u32_e32 v175, s37, v172
	ds_read_b128 v[112:115], v124
	ds_read_b128 v[116:119], v124 offset:1024
	ds_read_b128 v[120:123], v124 offset:2048
	ds_read_b128 v[124:127], v124 offset:3072
	ds_read_b128 v[176:179], v175
	ds_read_b128 v[180:183], v175 offset:1024
	ds_read_b128 v[194:197], v175 offset:2048
	ds_read_b128 v[198:201], v175 offset:3072
	s_add_u32 s28, s42, 0x160000
	s_addc_u32 s29, s43, 0
	s_mov_b32 m0, s26
	v_lshl_add_u64 v[220:221], s[28:29], 0, v[148:149]
	ds_read_b128 v[202:205], v174 offset:32768
	ds_read_b128 v[206:209], v174 offset:33792
	ds_read_b128 v[224:227], v174 offset:34816
	ds_read_b128 v[228:231], v174 offset:35840
	ds_read_b128 v[232:235], v174 offset:36864
	ds_read_b128 v[236:239], v174 offset:37888
	ds_read_b128 v[240:243], v174 offset:38912
	ds_read_b128 v[244:247], v174 offset:39936
	global_load_lds_dwordx4 v[220:221], off
	v_lshl_add_u64 v[220:221], s[28:29], 0, v[146:147]
	s_waitcnt vmcnt(7)
	s_waitcnt lgkmcnt(0)
	s_barrier
	s_setprio 1
	s_waitcnt lgkmcnt(0)
	v_mfma_f32_16x16x32_bf16 v[140:143], v[112:115], v[202:205], v[140:143]
	v_mfma_f32_16x16x32_bf16 v[136:139], v[120:123], v[202:205], v[136:139]
	s_mov_b32 m0, s27
	s_nop 0
	global_load_lds_dwordx4 v[220:221], off
	v_mfma_f32_16x16x32_bf16 v[108:111], v[112:115], v[224:227], v[108:111]
	v_mfma_f32_16x16x32_bf16 v[104:107], v[120:123], v[224:227], v[104:107]
	v_mfma_f32_16x16x32_bf16 v[92:95], v[112:115], v[232:235], v[92:95]
	v_mfma_f32_16x16x32_bf16 v[88:91], v[120:123], v[232:235], v[88:91]
	v_mfma_f32_16x16x32_bf16 v[76:79], v[112:115], v[240:243], v[76:79]
	v_mfma_f32_16x16x32_bf16 v[72:75], v[120:123], v[240:243], v[72:75]
	v_mfma_f32_16x16x32_bf16 v[140:143], v[116:119], v[206:209], v[140:143]
	v_mfma_f32_16x16x32_bf16 v[136:139], v[124:127], v[206:209], v[136:139]
	v_mfma_f32_16x16x32_bf16 v[108:111], v[116:119], v[228:231], v[108:111]
	v_mfma_f32_16x16x32_bf16 v[104:107], v[124:127], v[228:231], v[104:107]
	v_mfma_f32_16x16x32_bf16 v[92:95], v[116:119], v[236:239], v[92:95]
	v_mfma_f32_16x16x32_bf16 v[88:91], v[124:127], v[236:239], v[88:91]
	v_mfma_f32_16x16x32_bf16 v[76:79], v[116:119], v[244:247], v[76:79]
	v_mfma_f32_16x16x32_bf16 v[72:75], v[124:127], v[244:247], v[72:75]
	s_setprio 0
	s_setprio 1
	v_mfma_f32_16x16x32_bf16 v[132:135], v[176:179], v[202:205], v[132:135]
	v_mfma_f32_16x16x32_bf16 v[128:131], v[194:197], v[202:205], v[128:131]
	v_mfma_f32_16x16x32_bf16 v[100:103], v[176:179], v[224:227], v[100:103]
	v_mfma_f32_16x16x32_bf16 v[96:99], v[194:197], v[224:227], v[96:99]
	v_mfma_f32_16x16x32_bf16 v[84:87], v[176:179], v[232:235], v[84:87]
	v_mfma_f32_16x16x32_bf16 v[80:83], v[194:197], v[232:235], v[80:83]
	v_mfma_f32_16x16x32_bf16 v[68:71], v[176:179], v[240:243], v[68:71]
	v_mfma_f32_16x16x32_bf16 v[64:67], v[194:197], v[240:243], v[64:67]
	v_mfma_f32_16x16x32_bf16 v[132:135], v[180:183], v[206:209], v[132:135]
	v_mfma_f32_16x16x32_bf16 v[128:131], v[198:201], v[206:209], v[128:131]
	v_mfma_f32_16x16x32_bf16 v[100:103], v[180:183], v[228:231], v[100:103]
	v_mfma_f32_16x16x32_bf16 v[96:99], v[198:201], v[228:231], v[96:99]
	v_mfma_f32_16x16x32_bf16 v[84:87], v[180:183], v[236:239], v[84:87]
	v_mfma_f32_16x16x32_bf16 v[80:83], v[198:201], v[236:239], v[80:83]
	v_mfma_f32_16x16x32_bf16 v[68:71], v[180:183], v[244:247], v[68:71]
	v_mfma_f32_16x16x32_bf16 v[64:67], v[198:201], v[244:247], v[64:67]
	s_setprio 0
	s_barrier
	s_add_i32 s28, s36, s4
	v_lshl_add_u64 v[170:171], v[170:171], 0, s[68:69]
	s_mov_b32 m0, s28
	ds_read_b128 v[202:205], v174 offset:49152
	ds_read_b128 v[206:209], v174 offset:50176
	ds_read_b128 v[224:227], v174 offset:51200
	ds_read_b128 v[228:231], v174 offset:52224
	ds_read_b128 v[232:235], v174 offset:53248
	ds_read_b128 v[236:239], v174 offset:54272
	ds_read_b128 v[240:243], v174 offset:55296
	ds_read_b128 v[244:247], v174 offset:56320
	global_load_lds_dwordx4 v[170:171], off
	s_add_i32 m0, s28, 0x2000
	s_add_u32 s28, s40, 0x160080
	v_lshl_add_u64 v[170:171], v[210:211], 0, s[68:69]
	s_addc_u32 s29, s41, 0
	s_add_i32 s36, s37, s4
	global_load_lds_dwordx4 v[170:171], off
	v_lshl_add_u64 v[170:171], s[28:29], 0, v[184:185]
	s_mov_b32 m0, s36
	s_nop 0
	global_load_lds_dwordx4 v[170:171], off
	v_lshl_add_u64 v[170:171], s[28:29], 0, v[144:145]
	s_add_i32 m0, s36, 0x2000
	s_nop 0
	global_load_lds_dwordx4 v[170:171], off
	v_lshl_add_u64 v[170:171], v[216:217], 0, s[68:69]
	s_mov_b32 m0, s44
	s_nop 0
	global_load_lds_dwordx4 v[170:171], off
	v_lshl_add_u64 v[170:171], v[218:219], 0, s[68:69]
	s_waitcnt vmcnt(7)
	s_waitcnt lgkmcnt(0)
	s_barrier
	s_setprio 1
	s_waitcnt lgkmcnt(0)
	v_mfma_f32_16x16x32_bf16 v[60:63], v[112:115], v[202:205], v[60:63]
	v_mfma_f32_16x16x32_bf16 v[56:59], v[120:123], v[202:205], v[56:59]
	s_mov_b32 m0, s45
	s_nop 0
	global_load_lds_dwordx4 v[170:171], off
	v_mfma_f32_16x16x32_bf16 v[44:47], v[112:115], v[224:227], v[44:47]
	v_mfma_f32_16x16x32_bf16 v[40:43], v[120:123], v[224:227], v[40:43]
	v_mfma_f32_16x16x32_bf16 v[36:39], v[112:115], v[232:235], v[36:39]
	v_mfma_f32_16x16x32_bf16 v[28:31], v[120:123], v[232:235], v[28:31]
	v_mfma_f32_16x16x32_bf16 v[20:23], v[112:115], v[240:243], v[20:23]
	v_mfma_f32_16x16x32_bf16 v[12:15], v[120:123], v[240:243], v[12:15]
	v_mfma_f32_16x16x32_bf16 v[60:63], v[116:119], v[206:209], v[60:63]
	v_mfma_f32_16x16x32_bf16 v[56:59], v[124:127], v[206:209], v[56:59]
	v_mfma_f32_16x16x32_bf16 v[44:47], v[116:119], v[228:231], v[44:47]
	v_mfma_f32_16x16x32_bf16 v[40:43], v[124:127], v[228:231], v[40:43]
	v_mfma_f32_16x16x32_bf16 v[36:39], v[116:119], v[236:239], v[36:39]
	v_mfma_f32_16x16x32_bf16 v[28:31], v[124:127], v[236:239], v[28:31]
	v_mfma_f32_16x16x32_bf16 v[20:23], v[116:119], v[244:247], v[20:23]
	v_mfma_f32_16x16x32_bf16 v[12:15], v[124:127], v[244:247], v[12:15]
	s_setprio 0
	s_setprio 1
	v_mfma_f32_16x16x32_bf16 v[52:55], v[176:179], v[202:205], v[52:55]
	v_mfma_f32_16x16x32_bf16 v[48:51], v[194:197], v[202:205], v[48:51]
	v_mfma_f32_16x16x32_bf16 v[32:35], v[176:179], v[224:227], v[32:35]
	v_mfma_f32_16x16x32_bf16 v[24:27], v[194:197], v[224:227], v[24:27]
	v_mfma_f32_16x16x32_bf16 v[16:19], v[176:179], v[232:235], v[16:19]
	v_mfma_f32_16x16x32_bf16 v[8:11], v[194:197], v[232:235], v[8:11]
	v_mfma_f32_16x16x32_bf16 v[4:7], v[176:179], v[240:243], v[4:7]
	v_mfma_f32_16x16x32_bf16 v[0:3], v[194:197], v[240:243], v[0:3]
	v_mfma_f32_16x16x32_bf16 v[52:55], v[180:183], v[206:209], v[52:55]
	v_mfma_f32_16x16x32_bf16 v[48:51], v[198:201], v[206:209], v[48:51]
	v_mfma_f32_16x16x32_bf16 v[32:35], v[180:183], v[228:231], v[32:35]
	v_mfma_f32_16x16x32_bf16 v[24:27], v[198:201], v[228:231], v[24:27]
	v_mfma_f32_16x16x32_bf16 v[16:19], v[180:183], v[236:239], v[16:19]
	v_mfma_f32_16x16x32_bf16 v[8:11], v[198:201], v[236:239], v[8:11]
	v_mfma_f32_16x16x32_bf16 v[4:7], v[180:183], v[244:247], v[4:7]
	v_mfma_f32_16x16x32_bf16 v[0:3], v[198:201], v[244:247], v[0:3]
	s_setprio 0
	s_barrier
	s_add_i32 s59, s59, 2
	s_add_u32 s53, s53, 0x100
	s_addc_u32 s58, s58, 0
	s_cmp_gt_u32 s59, 5
	s_mov_b64 s[36:37], s[38:39]
	s_cbranch_scc0 .LBB0_1741
	s_and_b64 vcc, exec, s[8:9]
	s_cbranch_vccz .LBB0_1744
	s_barrier
